# remove m0 save/restore around all 229 LDS-DMA blocks
# baseline (speedup 1.0000x reference)
.LBB0_230:
	s_mul_i32 s3, s44, 11
	s_add_i32 s2, s3, 1
	s_cmp_gt_i32 s89, s2
	s_waitcnt lgkmcnt(0)
	s_cselect_b64 s[4:5], -1, 0
	v_writelane_b32 v254, s3, 36
	s_add_i32 s3, s3, 12
	s_cmp_lt_i32 s88, s3
	s_cselect_b64 s[6:7], -1, 0
	s_and_b64 s[4:5], s[4:5], s[6:7]
	s_andn2_b64 vcc, exec, s[4:5]
	s_cbranch_vccnz .LBB0_229
	v_writelane_b32 v254, s3, 37
	s_cmp_le_i32 s88, s2
	s_mov_b64 s[2:3], -1
	v_writelane_b32 v254, s44, 38
	s_cbranch_scc0 .LBB0_334
	v_readlane_b32 s6, v252, 0
	v_readlane_b32 s7, v252, 1
	s_waitcnt vmcnt(0) expcnt(0) lgkmcnt(0)
	s_load_dwordx2 s[4:5], s[6:7], 0x98
	v_mbcnt_lo_u32_b32 v0, -1, 0
	v_mbcnt_hi_u32_b32 v0, -1, v0
	v_readlane_b32 s2, v252, 8
	v_add_u32_e32 v156, s93, v0
	v_readlane_b32 s3, v252, 9
	v_mov_b32_e32 v0, v156
	s_andn2_b64 vcc, exec, s[2:3]
	v_readfirstlane_b32 s16, v0
	s_cbranch_vccnz .LBB0_256
	v_bfe_i32 v3, v0, 27, 1
	v_lshlrev_b32_e32 v1, 4, v0
	v_lshrrev_b32_e32 v3, 22, v3
	v_add_u32_e32 v3, v1, v3
	v_and_b32_e32 v3, 0xfffffc00, v3
	v_sub_u32_e32 v3, v1, v3
	v_ashrrev_i32_e32 v2, 31, v0
	v_lshrrev_b32_e32 v4, 4, v3
	v_lshrrev_b32_e32 v2, 26, v2
	v_bitop3_b32 v3, v4, v3, 32 bitop3:0x6c
	v_add_u32_e32 v2, v0, v2
	v_ashrrev_i32_e32 v5, 31, v3
	s_mul_i32 s3, s44, 0x500000
	v_ashrrev_i32_e32 v2, 6, v2
	v_lshrrev_b32_e32 v5, 26, v5
	s_mul_hi_u32 s2, s44, 0x500000
	s_waitcnt lgkmcnt(0)
	s_add_u32 s3, s4, s3
	v_lshlrev_b32_e32 v4, 3, v2
	v_add_u32_e32 v5, v3, v5
	s_addc_u32 s2, s5, s2
	v_and_b32_e32 v4, -16, v4
	v_ashrrev_i32_e32 v6, 6, v5
	v_and_b32_e32 v5, 0xc0, v5
	s_add_u32 s38, s3, 0x100000
	v_add_u32_e32 v4, v6, v4
	v_sub_u32_e32 v3, v3, v5
	s_addc_u32 s39, s2, 0
	s_load_dwordx2 s[2:3], s[6:7], 0x10
	s_load_dwordx2 s[12:13], s[6:7], 0x20
	v_lshlrev_b32_e32 v2, 5, v2
	v_ashrrev_i16_sdwa v3, v239, sext(v3) dst_sel:DWORD dst_unused:UNUSED_PAD src0_sel:DWORD src1_sel:BYTE_0
	v_lshlrev_b32_e32 v5, 1, v4
	v_lshrrev_b32_e32 v7, 2, v4
	v_and_b32_e32 v6, 3, v6
	s_mov_b32 s6, 0x1fffe0
	v_and_b32_e32 v2, 32, v2
	v_bfe_i32 v3, v3, 0, 16
	v_and_b32_e32 v5, 24, v5
	v_and_b32_e32 v7, 4, v7
	v_and_or_b32 v6, v4, s6, v6
	v_or3_b32 v5, v6, v7, v5
	v_add_lshl_u32 v2, v2, v3, 1
	v_add_u32_e32 v1, 0x2000, v1
	v_lshl_add_u32 v157, v4, 11, v2
	v_lshl_add_u32 v158, v5, 11, v2
	v_ashrrev_i32_e32 v2, 31, v1
	v_lshrrev_b32_e32 v2, 22, v2
	v_add_u32_e32 v2, v1, v2
	v_ashrrev_i32_e32 v2, 10, v2
	v_mul_i32_i24_e32 v3, 0x400, v2
	v_sub_u32_e32 v1, v1, v3
	v_lshrrev_b32_e32 v3, 4, v1
	v_bitop3_b32 v1, v3, v1, 32 bitop3:0x6c
	v_ashrrev_i32_e32 v4, 31, v1
	v_lshrrev_b32_e32 v4, 26, v4
	v_lshlrev_b32_e32 v3, 3, v2
	v_add_u32_e32 v4, v1, v4
	s_add_u32 s40, s4, 0x33b00000
	v_and_b32_e32 v3, -16, v3
	v_ashrrev_i32_e32 v5, 6, v4
	s_addc_u32 s41, s5, 0
	s_ashr_i32 s17, s16, 6
	v_add_u32_e32 v3, v5, v3
	v_and_b32_e32 v4, 0xc0, v4
	v_and_b32_e32 v5, 3, v5
	v_sub_u32_e32 v1, v1, v4
	v_and_or_b32 v5, v3, s6, v5
	s_ashr_i32 s18, s16, 8
	s_lshl_b32 s6, s17, 10
	v_readlane_b32 s8, v253, 14
	v_lshlrev_b32_e32 v2, 5, v2
	v_ashrrev_i16_sdwa v1, v239, sext(v1) dst_sel:DWORD dst_unused:UNUSED_PAD src0_sel:DWORD src1_sel:BYTE_0
	v_lshlrev_b32_e32 v4, 1, v3
	v_lshrrev_b32_e32 v6, 2, v3
	v_readlane_b32 s9, v253, 15
	s_add_u32 s28, s38, s8
	v_and_b32_e32 v2, 32, v2
	v_bfe_i32 v1, v1, 0, 16
	v_and_b32_e32 v4, 24, v4
	v_and_b32_e32 v6, 4, v6
	s_addc_u32 s29, s39, s9
	s_add_i32 s42, s6, 0
	v_or3_b32 v4, v5, v6, v4
	v_add_lshl_u32 v1, v2, v1, 1
	s_add_i32 s43, s42, 0x10000
	s_mov_b32 m0, s43
	s_nop 0
	global_load_lds_dwordx4 v158, s[28:29]
	v_lshl_add_u32 v160, v4, 11, v1
	s_add_i32 s44, s42, 0x12000
	s_mov_b32 m0, s44
	s_nop 0
	global_load_lds_dwordx4 v160, s[28:29]
	s_add_u32 s6, s28, 0x40000
	s_addc_u32 s7, s29, 0
	s_add_i32 s45, s42, 0x14000
	s_mov_b32 m0, s45
	s_nop 0
	global_load_lds_dwordx4 v158, s[6:7]
	s_add_i32 s46, s42, 0x16000
	s_mov_b32 m0, s46
	s_nop 0
	global_load_lds_dwordx4 v160, s[6:7]
	v_readlane_b32 s6, v253, 25
	v_readlane_b32 s7, v253, 26
	s_add_u32 s26, s40, s6
	s_addc_u32 s27, s41, s7
	s_mov_b32 m0, s42
	s_nop 0
	global_load_lds_dwordx4 v157, s[26:27]
	v_lshl_add_u32 v159, v3, 11, v1
	s_add_i32 s47, s42, 0x2000
	s_mov_b32 m0, s47
	s_nop 0
	global_load_lds_dwordx4 v159, s[26:27]
	s_add_u32 s6, s26, 0x40000
	s_addc_u32 s7, s27, 0
	s_add_i32 s48, s42, 0x4000
	s_mov_b32 m0, s48
	s_nop 0
	global_load_lds_dwordx4 v157, s[6:7]
	s_add_i32 s49, s42, 0x6000
	s_mov_b32 m0, s49
	s_nop 0
	global_load_lds_dwordx4 v159, s[6:7]
	s_cmp_eq_u32 s18, 1
	s_cselect_b64 s[6:7], -1, 0
	s_cmp_lg_u32 s18, 1
	s_cbranch_scc1 .LBB0_235
	s_barrier
.LBB0_235:
	s_add_u32 s50, s4, 0x37b00000
	s_addc_u32 s51, s5, 0
	s_add_u32 s8, s4, 0x42300000
	s_addc_u32 s9, s5, 0
	s_add_u32 s10, s4, 0x42b00000
	v_readlane_b32 s19, v254, 38
	s_addc_u32 s11, s5, 0
	s_lshl_b32 s86, s19, 7
	s_lshl_b64 s[14:15], s[86:87], 2
	s_waitcnt lgkmcnt(0)
	s_add_u32 s12, s12, s14
	s_addc_u32 s13, s13, s15
	s_lshl_b32 s86, s19, 2
	s_lshl_b64 s[14:15], s[86:87], 2
	v_bfe_u32 v162, v0, 4, 2
	s_add_u32 s14, s2, s14
	v_and_b32_e32 v161, 15, v0
	v_lshlrev_b32_e32 v1, 4, v162
	v_lshlrev_b32_e32 v0, 2, v0
	s_addc_u32 s15, s3, s15
	s_and_b32 s52, s17, 3
	v_lshl_or_b32 v1, v161, 6, v1
	s_lshl_b32 s2, s18, 13
	v_and_b32_e32 v0, 32, v0
	s_lshl_b32 s53, s18, 6
	v_bitop3_b32 v2, v1, s2, v0 bitop3:0xde
	s_lshl_b32 s54, s52, 5
	s_lshl_b32 s2, s52, 12
	v_bitop3_b32 v0, v1, s2, v0 bitop3:0xde
	s_add_u32 s2, s28, 0x80
	s_waitcnt vmcnt(2)
	s_barrier
	s_addc_u32 s3, s29, 0
	s_add_i32 s55, s42, 0x18000
	s_mov_b32 m0, s55
	s_nop 0
	global_load_lds_dwordx4 v158, s[2:3]
	s_add_i32 s56, s42, 0x1a000
	s_mov_b32 m0, s56
	s_nop 0
	global_load_lds_dwordx4 v160, s[2:3]
	s_add_u32 s2, s26, 0x80
	s_addc_u32 s3, s27, 0
	s_add_i32 s57, s42, 0x8000
	s_mov_b32 m0, s57
	s_nop 0
	global_load_lds_dwordx4 v157, s[2:3]
	s_add_i32 s58, s42, 0xa000
	s_mov_b32 m0, s58
	s_nop 0
	global_load_lds_dwordx4 v159, s[2:3]
	s_add_u32 s2, s28, 0x40080
	s_addc_u32 s3, s29, 0
	s_add_i32 s59, s42, 0x1c000
	s_mov_b32 m0, s59
	s_nop 0
	global_load_lds_dwordx4 v158, s[2:3]
	s_add_i32 s60, s42, 0x1e000
	s_mov_b32 m0, s60
	s_nop 0
	global_load_lds_dwordx4 v160, s[2:3]
	s_waitcnt vmcnt(6)
	s_add_i32 s61, s42, 0xc000
	s_cmpk_lt_u32 s16, 0x100
	v_add_u32_e32 v0, 0, v0
	v_readlane_b32 s2, v253, 12
	s_mov_b32 s62, 0
	s_cselect_b64 s[16:17], -1, 0
	v_add_u32_e32 v163, 0x10000, v0
	v_add_u32_e32 v164, 0x14000, v0
	v_add_u32_e32 v165, 0, v2
	v_add_u32_e32 v166, 0x18000, v0
	v_add_u32_e32 v167, 0x1c000, v0
	s_mov_b32 s24, s2
	v_readlane_b32 s25, v253, 13
	s_barrier
	s_branch .LBB0_238

.LBB0_243:
	ds_read_b128 v[130:133], v163
	ds_read_b128 v[134:137], v163 offset:1024
	ds_read_b128 v[138:141], v163 offset:2048
	ds_read_b128 v[142:145], v163 offset:3072
	ds_read_b128 v[146:149], v164
	ds_read_b128 v[150:153], v164 offset:1024
	ds_read_b128 v[168:171], v164 offset:2048
	ds_read_b128 v[172:175], v164 offset:3072
	s_add_u32 s2, s26, 0x100
	s_addc_u32 s3, s27, 0
	s_cmp_eq_u32 s65, 12
	s_cselect_b32 s34, s22, s2
	s_cselect_b32 s35, s23, s3
	s_cselect_b32 s30, s20, s19
	s_cselect_b32 s31, s21, s64
	s_add_u32 s28, s34, 0x80
	s_addc_u32 s29, s35, 0
	ds_read_b128 v[176:179], v165
	ds_read_b128 v[180:183], v165 offset:1024
	ds_read_b128 v[184:187], v165 offset:2048
	ds_read_b128 v[188:191], v165 offset:3072
	ds_read_b128 v[198:201], v165 offset:4096
	ds_read_b128 v[202:205], v165 offset:5120
	ds_read_b128 v[206:209], v165 offset:6144
	ds_read_b128 v[210:213], v165 offset:7168
	s_add_u32 s26, s26, 0x40080
	s_addc_u32 s27, s27, 0
	s_mov_b32 m0, s61
	s_nop 0
	global_load_lds_dwordx4 v157, s[26:27]
	s_add_i32 s66, s42, 0xe000
	s_mov_b32 m0, s66
	s_nop 0
	global_load_lds_dwordx4 v159, s[26:27]
	s_waitcnt vmcnt(8)
	s_waitcnt lgkmcnt(0)
	s_barrier
	s_setprio 1
	s_waitcnt lgkmcnt(7)
	v_mfma_f32_16x16x32_bf16 v[126:129], v[130:133], v[176:179], v[126:129]
	v_mfma_f32_16x16x32_bf16 v[122:125], v[138:141], v[176:179], v[122:125]
	s_waitcnt lgkmcnt(5)
	v_mfma_f32_16x16x32_bf16 v[118:121], v[130:133], v[184:187], v[118:121]
	v_mfma_f32_16x16x32_bf16 v[110:113], v[138:141], v[184:187], v[110:113]
	s_waitcnt lgkmcnt(3)
	v_mfma_f32_16x16x32_bf16 v[102:105], v[130:133], v[198:201], v[102:105]
	v_mfma_f32_16x16x32_bf16 v[92:95], v[138:141], v[198:201], v[92:95]
	s_waitcnt lgkmcnt(1)
	v_mfma_f32_16x16x32_bf16 v[84:87], v[130:133], v[206:209], v[84:87]
	v_mfma_f32_16x16x32_bf16 v[76:79], v[138:141], v[206:209], v[76:79]
	v_mfma_f32_16x16x32_bf16 v[126:129], v[134:137], v[180:183], v[126:129]
	v_mfma_f32_16x16x32_bf16 v[122:125], v[142:145], v[180:183], v[122:125]
	v_mfma_f32_16x16x32_bf16 v[118:121], v[134:137], v[188:191], v[118:121]
	v_mfma_f32_16x16x32_bf16 v[110:113], v[142:145], v[188:191], v[110:113]
	v_mfma_f32_16x16x32_bf16 v[102:105], v[134:137], v[202:205], v[102:105]
	v_mfma_f32_16x16x32_bf16 v[92:95], v[142:145], v[202:205], v[92:95]
	s_waitcnt lgkmcnt(0)
	v_mfma_f32_16x16x32_bf16 v[84:87], v[134:137], v[210:213], v[84:87]
	v_mfma_f32_16x16x32_bf16 v[76:79], v[142:145], v[210:213], v[76:79]
	s_setprio 0
	s_setprio 1
	v_mfma_f32_16x16x32_bf16 v[114:117], v[146:149], v[176:179], v[114:117]
	v_mfma_f32_16x16x32_bf16 v[106:109], v[168:171], v[176:179], v[106:109]
	v_mfma_f32_16x16x32_bf16 v[98:101], v[146:149], v[184:187], v[98:101]
	v_mfma_f32_16x16x32_bf16 v[88:91], v[168:171], v[184:187], v[88:91]
	v_mfma_f32_16x16x32_bf16 v[80:83], v[146:149], v[198:201], v[80:83]
	v_mfma_f32_16x16x32_bf16 v[72:75], v[168:171], v[198:201], v[72:75]
	v_mfma_f32_16x16x32_bf16 v[68:71], v[146:149], v[206:209], v[68:71]
	v_mfma_f32_16x16x32_bf16 v[64:67], v[168:171], v[206:209], v[64:67]
	v_mfma_f32_16x16x32_bf16 v[114:117], v[150:153], v[180:183], v[114:117]
	v_mfma_f32_16x16x32_bf16 v[106:109], v[172:175], v[180:183], v[106:109]
	v_mfma_f32_16x16x32_bf16 v[98:101], v[150:153], v[188:191], v[98:101]
	v_mfma_f32_16x16x32_bf16 v[88:91], v[172:175], v[188:191], v[88:91]
	v_mfma_f32_16x16x32_bf16 v[80:83], v[150:153], v[202:205], v[80:83]
	v_mfma_f32_16x16x32_bf16 v[72:75], v[172:175], v[202:205], v[72:75]
	v_mfma_f32_16x16x32_bf16 v[68:71], v[150:153], v[210:213], v[68:71]
	v_mfma_f32_16x16x32_bf16 v[64:67], v[172:175], v[210:213], v[64:67]
	s_setprio 0
	s_barrier
	ds_read_b128 v[176:179], v165 offset:16384
	ds_read_b128 v[180:183], v165 offset:17408
	ds_read_b128 v[184:187], v165 offset:18432
	ds_read_b128 v[188:191], v165 offset:19456
	ds_read_b128 v[198:201], v165 offset:20480
	ds_read_b128 v[202:205], v165 offset:21504
	ds_read_b128 v[206:209], v165 offset:22528
	ds_read_b128 v[210:213], v165 offset:23552
	s_mov_b32 m0, s43
	s_nop 0
	global_load_lds_dwordx4 v158, s[30:31]
	s_nop 0
	s_mov_b32 m0, s44
	s_nop 0
	global_load_lds_dwordx4 v160, s[30:31]
	s_add_u32 s26, s30, 0x40000
	s_addc_u32 s27, s31, 0
	s_mov_b32 m0, s45
	s_nop 0
	global_load_lds_dwordx4 v158, s[26:27]
	s_nop 0
	s_mov_b32 m0, s46
	s_nop 0
	global_load_lds_dwordx4 v160, s[26:27]
	s_mov_b32 m0, s42
	s_nop 0
	global_load_lds_dwordx4 v157, s[34:35]
	s_nop 0
	s_mov_b32 m0, s47
	s_nop 0
	global_load_lds_dwordx4 v159, s[34:35]
	s_waitcnt vmcnt(8)
	s_waitcnt lgkmcnt(0)
	s_barrier
	s_setprio 1
	s_waitcnt lgkmcnt(7)
	v_mfma_f32_16x16x32_bf16 v[60:63], v[130:133], v[176:179], v[60:63]
	v_mfma_f32_16x16x32_bf16 v[56:59], v[138:141], v[176:179], v[56:59]
	s_waitcnt lgkmcnt(5)
	v_mfma_f32_16x16x32_bf16 v[52:55], v[130:133], v[184:187], v[52:55]
	v_mfma_f32_16x16x32_bf16 v[44:47], v[138:141], v[184:187], v[44:47]
	s_waitcnt lgkmcnt(3)
	v_mfma_f32_16x16x32_bf16 v[36:39], v[130:133], v[198:201], v[36:39]
	v_mfma_f32_16x16x32_bf16 v[28:31], v[138:141], v[198:201], v[28:31]
	s_waitcnt lgkmcnt(1)
	v_mfma_f32_16x16x32_bf16 v[20:23], v[130:133], v[206:209], v[20:23]
	v_mfma_f32_16x16x32_bf16 v[12:15], v[138:141], v[206:209], v[12:15]
	v_mfma_f32_16x16x32_bf16 v[60:63], v[134:137], v[180:183], v[60:63]
	v_mfma_f32_16x16x32_bf16 v[56:59], v[142:145], v[180:183], v[56:59]
	v_mfma_f32_16x16x32_bf16 v[52:55], v[134:137], v[188:191], v[52:55]
	v_mfma_f32_16x16x32_bf16 v[44:47], v[142:145], v[188:191], v[44:47]
	v_mfma_f32_16x16x32_bf16 v[36:39], v[134:137], v[202:205], v[36:39]
	v_mfma_f32_16x16x32_bf16 v[28:31], v[142:145], v[202:205], v[28:31]
	s_waitcnt lgkmcnt(0)
	v_mfma_f32_16x16x32_bf16 v[20:23], v[134:137], v[210:213], v[20:23]
	v_mfma_f32_16x16x32_bf16 v[12:15], v[142:145], v[210:213], v[12:15]
	s_setprio 0
	s_setprio 1
	v_mfma_f32_16x16x32_bf16 v[48:51], v[146:149], v[176:179], v[48:51]
	v_mfma_f32_16x16x32_bf16 v[40:43], v[168:171], v[176:179], v[40:43]
	v_mfma_f32_16x16x32_bf16 v[32:35], v[146:149], v[184:187], v[32:35]
	v_mfma_f32_16x16x32_bf16 v[24:27], v[168:171], v[184:187], v[24:27]
	v_mfma_f32_16x16x32_bf16 v[16:19], v[146:149], v[198:201], v[16:19]
	v_mfma_f32_16x16x32_bf16 v[8:11], v[168:171], v[198:201], v[8:11]
	v_mfma_f32_16x16x32_bf16 v[4:7], v[146:149], v[206:209], v[4:7]
	v_mfma_f32_16x16x32_bf16 v[0:3], v[168:171], v[206:209], v[0:3]
	v_mfma_f32_16x16x32_bf16 v[48:51], v[150:153], v[180:183], v[48:51]
	v_mfma_f32_16x16x32_bf16 v[40:43], v[172:175], v[180:183], v[40:43]
	v_mfma_f32_16x16x32_bf16 v[32:35], v[150:153], v[188:191], v[32:35]
	v_mfma_f32_16x16x32_bf16 v[24:27], v[172:175], v[188:191], v[24:27]
	v_mfma_f32_16x16x32_bf16 v[16:19], v[150:153], v[202:205], v[16:19]
	v_mfma_f32_16x16x32_bf16 v[8:11], v[172:175], v[202:205], v[8:11]
	v_mfma_f32_16x16x32_bf16 v[4:7], v[150:153], v[210:213], v[4:7]
	v_mfma_f32_16x16x32_bf16 v[0:3], v[172:175], v[210:213], v[0:3]
	s_setprio 0
	s_barrier
	ds_read_b128 v[130:133], v166
	ds_read_b128 v[134:137], v166 offset:1024
	ds_read_b128 v[138:141], v166 offset:2048
	ds_read_b128 v[142:145], v166 offset:3072
	ds_read_b128 v[146:149], v167
	ds_read_b128 v[150:153], v167 offset:1024
	ds_read_b128 v[168:171], v167 offset:2048
	ds_read_b128 v[172:175], v167 offset:3072
	ds_read_b128 v[176:179], v165 offset:32768
	ds_read_b128 v[180:183], v165 offset:33792
	ds_read_b128 v[184:187], v165 offset:34816
	ds_read_b128 v[188:191], v165 offset:35840
	ds_read_b128 v[198:201], v165 offset:36864
	ds_read_b128 v[202:205], v165 offset:37888
	ds_read_b128 v[206:209], v165 offset:38912
	ds_read_b128 v[210:213], v165 offset:39936
	s_add_u32 s26, s34, 0x40000
	s_addc_u32 s27, s35, 0
	s_mov_b32 m0, s48
	s_nop 0
	global_load_lds_dwordx4 v157, s[26:27]
	s_nop 0
	s_mov_b32 m0, s49
	s_nop 0
	global_load_lds_dwordx4 v159, s[26:27]
	s_waitcnt vmcnt(8)
	s_waitcnt lgkmcnt(0)
	s_barrier
	s_setprio 1
	s_waitcnt lgkmcnt(7)
	v_mfma_f32_16x16x32_bf16 v[126:129], v[130:133], v[176:179], v[126:129]
	v_mfma_f32_16x16x32_bf16 v[122:125], v[138:141], v[176:179], v[122:125]
	s_waitcnt lgkmcnt(5)
	v_mfma_f32_16x16x32_bf16 v[118:121], v[130:133], v[184:187], v[118:121]
	v_mfma_f32_16x16x32_bf16 v[110:113], v[138:141], v[184:187], v[110:113]
	s_waitcnt lgkmcnt(3)
	v_mfma_f32_16x16x32_bf16 v[102:105], v[130:133], v[198:201], v[102:105]
	v_mfma_f32_16x16x32_bf16 v[92:95], v[138:141], v[198:201], v[92:95]
	s_waitcnt lgkmcnt(1)
	v_mfma_f32_16x16x32_bf16 v[84:87], v[130:133], v[206:209], v[84:87]
	v_mfma_f32_16x16x32_bf16 v[76:79], v[138:141], v[206:209], v[76:79]
	v_mfma_f32_16x16x32_bf16 v[126:129], v[134:137], v[180:183], v[126:129]
	v_mfma_f32_16x16x32_bf16 v[122:125], v[142:145], v[180:183], v[122:125]
	v_mfma_f32_16x16x32_bf16 v[118:121], v[134:137], v[188:191], v[118:121]
	v_mfma_f32_16x16x32_bf16 v[110:113], v[142:145], v[188:191], v[110:113]
	v_mfma_f32_16x16x32_bf16 v[102:105], v[134:137], v[202:205], v[102:105]
	v_mfma_f32_16x16x32_bf16 v[92:95], v[142:145], v[202:205], v[92:95]
	s_waitcnt lgkmcnt(0)
	v_mfma_f32_16x16x32_bf16 v[84:87], v[134:137], v[210:213], v[84:87]
	v_mfma_f32_16x16x32_bf16 v[76:79], v[142:145], v[210:213], v[76:79]
	s_setprio 0
	s_setprio 1
	v_mfma_f32_16x16x32_bf16 v[114:117], v[146:149], v[176:179], v[114:117]
	v_mfma_f32_16x16x32_bf16 v[106:109], v[168:171], v[176:179], v[106:109]
	v_mfma_f32_16x16x32_bf16 v[98:101], v[146:149], v[184:187], v[98:101]
	v_mfma_f32_16x16x32_bf16 v[88:91], v[168:171], v[184:187], v[88:91]
	v_mfma_f32_16x16x32_bf16 v[80:83], v[146:149], v[198:201], v[80:83]
	v_mfma_f32_16x16x32_bf16 v[72:75], v[168:171], v[198:201], v[72:75]
	v_mfma_f32_16x16x32_bf16 v[68:71], v[146:149], v[206:209], v[68:71]
	v_mfma_f32_16x16x32_bf16 v[64:67], v[168:171], v[206:209], v[64:67]
	v_mfma_f32_16x16x32_bf16 v[114:117], v[150:153], v[180:183], v[114:117]
	v_mfma_f32_16x16x32_bf16 v[106:109], v[172:175], v[180:183], v[106:109]
	v_mfma_f32_16x16x32_bf16 v[98:101], v[150:153], v[188:191], v[98:101]
	v_mfma_f32_16x16x32_bf16 v[88:91], v[172:175], v[188:191], v[88:91]
	v_mfma_f32_16x16x32_bf16 v[80:83], v[150:153], v[202:205], v[80:83]
	v_mfma_f32_16x16x32_bf16 v[72:75], v[172:175], v[202:205], v[72:75]
	v_mfma_f32_16x16x32_bf16 v[68:71], v[150:153], v[210:213], v[68:71]
	v_mfma_f32_16x16x32_bf16 v[64:67], v[172:175], v[210:213], v[64:67]
	s_setprio 0
	s_barrier
	ds_read_b128 v[176:179], v165 offset:49152
	ds_read_b128 v[180:183], v165 offset:50176
	ds_read_b128 v[184:187], v165 offset:51200
	ds_read_b128 v[188:191], v165 offset:52224
	ds_read_b128 v[198:201], v165 offset:53248
	ds_read_b128 v[202:205], v165 offset:54272
	ds_read_b128 v[206:209], v165 offset:55296
	ds_read_b128 v[210:213], v165 offset:56320
	s_add_u32 s26, s30, 0x80
	s_addc_u32 s27, s31, 0
	s_mov_b32 m0, s55
	s_nop 0
	global_load_lds_dwordx4 v158, s[26:27]
	s_nop 0
	s_mov_b32 m0, s56
	s_nop 0
	global_load_lds_dwordx4 v160, s[26:27]
	s_add_u32 s26, s30, 0x40080
	s_addc_u32 s27, s31, 0
	s_mov_b32 m0, s59
	s_nop 0
	global_load_lds_dwordx4 v158, s[26:27]
	s_nop 0
	s_mov_b32 m0, s60
	s_nop 0
	global_load_lds_dwordx4 v160, s[26:27]
	s_mov_b32 m0, s57
	s_nop 0
	global_load_lds_dwordx4 v157, s[28:29]
	s_nop 0
	s_mov_b32 m0, s58
	s_nop 0
	global_load_lds_dwordx4 v159, s[28:29]
	s_waitcnt vmcnt(8)
	s_waitcnt lgkmcnt(0)
	s_barrier
	s_setprio 1
	s_waitcnt lgkmcnt(7)
	v_mfma_f32_16x16x32_bf16 v[60:63], v[130:133], v[176:179], v[60:63]
	v_mfma_f32_16x16x32_bf16 v[56:59], v[138:141], v[176:179], v[56:59]
	s_waitcnt lgkmcnt(5)
	v_mfma_f32_16x16x32_bf16 v[52:55], v[130:133], v[184:187], v[52:55]
	v_mfma_f32_16x16x32_bf16 v[44:47], v[138:141], v[184:187], v[44:47]
	s_waitcnt lgkmcnt(3)
	v_mfma_f32_16x16x32_bf16 v[36:39], v[130:133], v[198:201], v[36:39]
	v_mfma_f32_16x16x32_bf16 v[28:31], v[138:141], v[198:201], v[28:31]
	s_waitcnt lgkmcnt(1)
	v_mfma_f32_16x16x32_bf16 v[20:23], v[130:133], v[206:209], v[20:23]
	v_mfma_f32_16x16x32_bf16 v[12:15], v[138:141], v[206:209], v[12:15]
	v_mfma_f32_16x16x32_bf16 v[60:63], v[134:137], v[180:183], v[60:63]
	v_mfma_f32_16x16x32_bf16 v[56:59], v[142:145], v[180:183], v[56:59]
	v_mfma_f32_16x16x32_bf16 v[52:55], v[134:137], v[188:191], v[52:55]
	v_mfma_f32_16x16x32_bf16 v[44:47], v[142:145], v[188:191], v[44:47]
	v_mfma_f32_16x16x32_bf16 v[36:39], v[134:137], v[202:205], v[36:39]
	v_mfma_f32_16x16x32_bf16 v[28:31], v[142:145], v[202:205], v[28:31]
	s_waitcnt lgkmcnt(0)
	v_mfma_f32_16x16x32_bf16 v[20:23], v[134:137], v[210:213], v[20:23]
	v_mfma_f32_16x16x32_bf16 v[12:15], v[142:145], v[210:213], v[12:15]
	s_setprio 0
	s_setprio 1
	v_mfma_f32_16x16x32_bf16 v[48:51], v[146:149], v[176:179], v[48:51]
	v_mfma_f32_16x16x32_bf16 v[40:43], v[168:171], v[176:179], v[40:43]
	v_mfma_f32_16x16x32_bf16 v[32:35], v[146:149], v[184:187], v[32:35]
	v_mfma_f32_16x16x32_bf16 v[24:27], v[168:171], v[184:187], v[24:27]
	v_mfma_f32_16x16x32_bf16 v[16:19], v[146:149], v[198:201], v[16:19]
	v_mfma_f32_16x16x32_bf16 v[8:11], v[168:171], v[198:201], v[8:11]
	v_mfma_f32_16x16x32_bf16 v[4:7], v[146:149], v[206:209], v[4:7]
	v_mfma_f32_16x16x32_bf16 v[0:3], v[168:171], v[206:209], v[0:3]
	v_mfma_f32_16x16x32_bf16 v[48:51], v[150:153], v[180:183], v[48:51]
	v_mfma_f32_16x16x32_bf16 v[40:43], v[172:175], v[180:183], v[40:43]
	v_mfma_f32_16x16x32_bf16 v[32:35], v[150:153], v[188:191], v[32:35]
	v_mfma_f32_16x16x32_bf16 v[24:27], v[172:175], v[188:191], v[24:27]
	v_mfma_f32_16x16x32_bf16 v[16:19], v[150:153], v[202:205], v[16:19]
	v_mfma_f32_16x16x32_bf16 v[8:11], v[172:175], v[202:205], v[8:11]
	v_mfma_f32_16x16x32_bf16 v[4:7], v[150:153], v[210:213], v[4:7]
	v_mfma_f32_16x16x32_bf16 v[0:3], v[172:175], v[210:213], v[0:3]
	s_setprio 0
	s_barrier
	s_add_i32 s65, s65, 2
	s_add_u32 s19, s19, 0x100
	s_addc_u32 s64, s64, 0
	s_cmp_gt_u32 s65, 13
	s_mov_b64 s[26:27], s[2:3]
	s_cbranch_scc0 .LBB0_243
	s_and_b64 vcc, exec, s[16:17]
	s_cbranch_vccz .LBB0_246
	s_barrier

.LBB0_256:
	s_waitcnt vmcnt(0)
	s_waitcnt vmcnt(0)
	v_readlane_b32 s2, v252, 14
	s_movk_i32 s6, 0x400
	v_readlane_b32 s3, v252, 15
	s_waitcnt lgkmcnt(0)
	s_barrier
	s_andn2_b64 vcc, exec, s[2:3]
	v_readfirstlane_b32 s16, v156
	s_cbranch_vccnz .LBB0_280
	v_bfe_i32 v2, v156, 27, 1
	v_lshlrev_b32_e32 v1, 4, v156
	v_lshrrev_b32_e32 v2, 22, v2
	v_add_u32_e32 v2, v1, v2
	v_and_b32_e32 v2, 0xfffffc00, v2
	v_sub_u32_e32 v2, v1, v2
	v_ashrrev_i32_e32 v0, 31, v156
	v_lshrrev_b32_e32 v3, 4, v2
	v_lshrrev_b32_e32 v0, 26, v0
	v_bitop3_b32 v2, v3, v2, 32 bitop3:0x6c
	v_add_u32_e32 v0, v156, v0
	v_ashrrev_i32_e32 v4, 31, v2
	v_ashrrev_i32_e32 v0, 6, v0
	v_lshrrev_b32_e32 v4, 26, v4
	v_lshlrev_b32_e32 v3, 3, v0
	v_add_u32_e32 v4, v2, v4
	v_and_b32_e32 v3, -16, v3
	v_ashrrev_i32_e32 v5, 6, v4
	v_and_b32_e32 v4, 0xc0, v4
	s_mul_i32 s3, s44, 0x300000
	v_add_u32_e32 v3, v5, v3
	v_sub_u32_e32 v2, v2, v4
	s_mul_hi_u32 s2, s44, 0x300000
	s_add_u32 s3, s4, s3
	v_lshlrev_b32_e32 v0, 5, v0
	v_ashrrev_i16_sdwa v2, v239, sext(v2) dst_sel:DWORD dst_unused:UNUSED_PAD src0_sel:DWORD src1_sel:BYTE_0
	v_lshlrev_b32_e32 v4, 1, v3
	v_lshrrev_b32_e32 v6, 2, v3
	v_and_b32_e32 v5, 3, v5
	s_movk_i32 s7, 0xffe0
	s_addc_u32 s2, s5, s2
	v_and_b32_e32 v0, 32, v0
	v_bfe_i32 v2, v2, 0, 16
	v_and_b32_e32 v4, 24, v4
	v_and_b32_e32 v6, 4, v6
	v_and_or_b32 v5, v3, s7, v5
	s_add_u32 s28, s3, 0x6b100000
	v_or3_b32 v4, v5, v6, v4
	v_add_lshl_u32 v0, v0, v2, 1
	s_addc_u32 s29, s2, 0
	v_mad_u64_u32 v[130:131], s[2:3], v3, s6, v[0:1]
	v_mad_u64_u32 v[132:133], s[2:3], v4, s6, v[0:1]
	v_add_u32_e32 v0, 0x2000, v1
	v_ashrrev_i32_e32 v1, 31, v0
	v_lshrrev_b32_e32 v1, 22, v1
	v_add_u32_e32 v1, v0, v1
	v_ashrrev_i32_e32 v1, 10, v1
	v_mul_i32_i24_e32 v2, 0x400, v1
	v_sub_u32_e32 v0, v0, v2
	v_lshrrev_b32_e32 v2, 4, v0
	v_bitop3_b32 v0, v2, v0, 32 bitop3:0x6c
	v_ashrrev_i32_e32 v3, 31, v0
	v_lshrrev_b32_e32 v3, 26, v3
	v_lshlrev_b32_e32 v2, 3, v1
	v_add_u32_e32 v3, v0, v3
	v_and_b32_e32 v2, -16, v2
	v_ashrrev_i32_e32 v4, 6, v3
	v_and_b32_e32 v3, 0xc0, v3
	v_add_u32_e32 v2, v4, v2
	v_sub_u32_e32 v0, v0, v3
	v_lshlrev_b32_e32 v1, 5, v1
	v_ashrrev_i16_sdwa v0, v239, sext(v0) dst_sel:DWORD dst_unused:UNUSED_PAD src0_sel:DWORD src1_sel:BYTE_0
	v_lshlrev_b32_e32 v3, 1, v2
	v_lshrrev_b32_e32 v5, 2, v2
	v_and_b32_e32 v4, 3, v4
	v_and_b32_e32 v1, 32, v1
	v_bfe_i32 v0, v0, 0, 16
	v_and_b32_e32 v3, 24, v3
	v_and_b32_e32 v5, 4, v5
	v_and_or_b32 v4, v2, s7, v4
	s_add_u32 s30, s4, 0x6a100000
	v_or3_b32 v3, v4, v5, v3
	v_add_lshl_u32 v0, v1, v0, 1
	s_addc_u32 s31, s5, 0
	v_mad_u64_u32 v[134:135], s[2:3], v2, s6, v[0:1]
	v_mad_u64_u32 v[136:137], s[2:3], v3, s6, v[0:1]
	s_ashr_i32 s7, s6, 31
	v_readlane_b32 s10, v253, 22
	v_readlane_b32 s20, v253, 17
	s_mul_hi_u32 s2, s10, s6
	s_mul_i32 s3, s10, s7
	s_mul_i32 s17, s10, s6
	s_lshl_b64 s[10:11], s[6:7], 8
	v_readlane_b32 s21, v253, 18
	s_add_i32 s13, s2, s3
	s_mul_i32 s2, s10, s21
	s_mul_hi_u32 s3, s10, s20
	s_add_i32 s18, s3, s2
	s_lshr_b64 s[2:3], s[6:7], 24
	s_ashr_i32 s14, s16, 6
	s_mul_i32 s2, s2, s20
	s_ashr_i32 s15, s16, 8
	s_lshl_b64 s[8:9], s[6:7], 7
	s_lshl_b32 s12, s14, 10
	s_add_i32 s18, s18, s2
	s_mul_i32 s2, s10, s20
	s_add_u32 s20, s28, s2
	s_addc_u32 s21, s29, s18
	s_add_i32 s34, s12, 0
	s_add_i32 s35, s34, 0x10000
	s_mov_b32 m0, s35
	s_nop 0
	global_load_lds_dwordx4 v132, s[20:21]
	s_add_i32 s36, s34, 0x12000
	s_mov_b32 m0, s36
	s_nop 0
	global_load_lds_dwordx4 v136, s[20:21]
	s_add_u32 s2, s20, s8
	s_addc_u32 s3, s21, s9
	s_add_i32 s37, s34, 0x14000
	s_mov_b32 m0, s37
	s_nop 0
	global_load_lds_dwordx4 v132, s[2:3]
	s_add_i32 s38, s34, 0x16000
	s_mov_b32 m0, s38
	s_nop 0
	global_load_lds_dwordx4 v136, s[2:3]
	s_add_u32 s22, s30, s17
	s_addc_u32 s23, s31, s13
	s_mov_b32 m0, s34
	s_nop 0
	global_load_lds_dwordx4 v130, s[22:23]
	s_add_i32 s39, s34, 0x2000
	s_mov_b32 m0, s39
	s_nop 0
	global_load_lds_dwordx4 v134, s[22:23]
	s_add_u32 s12, s22, s8
	s_addc_u32 s13, s23, s9
	s_add_i32 s40, s34, 0x4000
	s_mov_b32 m0, s40
	s_nop 0
	global_load_lds_dwordx4 v130, s[12:13]
	s_add_i32 s41, s34, 0x6000
	s_mov_b32 m0, s41
	s_nop 0
	global_load_lds_dwordx4 v134, s[12:13]
	s_cmp_eq_u32 s15, 1
	s_cselect_b64 s[12:13], -1, 0
	s_cmp_lg_u32 s15, 1
	s_cbranch_scc1 .LBB0_259
	s_barrier
.LBB0_259:
	s_and_b32 s17, s14, 3
	v_and_b32_e32 v131, 15, v156
	s_lshr_b32 s14, s7, 25
	v_bfe_u32 v96, v156, 4, 2
	s_add_i32 s14, s6, s14
	v_lshlrev_b32_e32 v0, 6, v131
	v_lshlrev_b32_e32 v1, 2, v156
	s_ashr_i32 s42, s14, 7
	v_lshl_or_b32 v0, v96, 4, v0
	s_lshl_b32 s14, s15, 13
	v_and_b32_e32 v1, 32, v1
	v_bitop3_b32 v2, v0, s14, v1 bitop3:0xde
	s_lshl_b32 s14, s17, 12
	s_add_u32 s43, s4, 0x3c300000
	s_addc_u32 s44, s5, 0
	s_add_u32 s4, s20, 0x80
	v_bitop3_b32 v0, v0, s14, v1 bitop3:0xde
	s_waitcnt vmcnt(2)
	s_barrier
	s_addc_u32 s5, s21, 0
	s_add_i32 s45, s34, 0x18000
	s_mov_b32 m0, s45
	s_nop 0
	global_load_lds_dwordx4 v132, s[4:5]
	s_add_i32 s46, s34, 0x1a000
	s_mov_b32 m0, s46
	s_nop 0
	global_load_lds_dwordx4 v136, s[4:5]
	s_add_u32 s4, s22, 0x80
	s_addc_u32 s5, s23, 0
	s_add_i32 s47, s34, 0x8000
	s_mov_b32 m0, s47
	s_nop 0
	global_load_lds_dwordx4 v130, s[4:5]
	s_add_i32 s48, s34, 0xa000
	s_mov_b32 m0, s48
	s_nop 0
	global_load_lds_dwordx4 v134, s[4:5]
	s_add_u32 s2, s2, 0x80
	s_addc_u32 s3, s3, 0
	s_add_i32 s49, s34, 0x1c000
	s_mov_b32 m0, s49
	s_nop 0
	global_load_lds_dwordx4 v132, s[2:3]
	s_add_i32 s50, s34, 0x1e000
	s_mov_b32 m0, s50
	s_nop 0
	global_load_lds_dwordx4 v136, s[2:3]
	s_cmpk_gt_i32 s6, 0x7f
	s_cselect_b64 s[4:5], -1, 0
	s_add_i32 s51, s42, -2
	s_add_i32 s52, s34, 0xc000
	s_waitcnt vmcnt(6)
	s_cmpk_lt_u32 s16, 0x100
	s_cselect_b64 s[14:15], -1, 0
	s_and_b32 s2, s16, 0xfffff00
	s_lshl_b32 s3, s17, 6
	s_or_b32 s53, s3, s2
	s_mov_b32 s16, 0
	v_add_u32_e32 v133, 0, v0
	v_add_u32_e32 v135, 0, v2
	v_readlane_b32 s57, v253, 16
	v_readlane_b32 s58, v253, 21
	s_barrier
	s_branch .LBB0_262

.LBB0_272:
	v_add_u32_e32 v137, 0x10000, v133
	ds_read_b128 v[138:141], v137
	ds_read_b128 v[142:145], v137 offset:1024
	ds_read_b128 v[146:149], v137 offset:2048
	ds_read_b128 v[150:153], v137 offset:3072
	v_add_u32_e32 v137, 0x14000, v133
	ds_read_b128 v[154:157], v137
	ds_read_b128 v[158:161], v137 offset:1024
	ds_read_b128 v[162:165], v137 offset:2048
	ds_read_b128 v[166:169], v137 offset:3072
	s_add_i32 s63, s22, 2
	s_cmp_eq_u32 s51, s22
	s_cselect_b32 s26, s18, s61
	s_cselect_b32 s27, s19, s62
	s_cselect_b32 s24, s16, s59
	s_cselect_b32 s25, s17, s60
	s_add_u32 s22, s26, 0x80
	s_addc_u32 s23, s27, 0
	ds_read_b128 v[170:173], v135
	ds_read_b128 v[174:177], v135 offset:1024
	ds_read_b128 v[178:181], v135 offset:2048
	ds_read_b128 v[182:185], v135 offset:3072
	ds_read_b128 v[186:189], v135 offset:4096
	ds_read_b128 v[190:193], v135 offset:5120
	ds_read_b128 v[198:201], v135 offset:6144
	ds_read_b128 v[202:205], v135 offset:7168
	s_mov_b32 m0, s52
	s_nop 0
	global_load_lds_dwordx4 v130, s[20:21]
	s_add_i32 s64, s34, 0xe000
	s_mov_b32 m0, s64
	s_nop 0
	global_load_lds_dwordx4 v134, s[20:21]
	s_waitcnt vmcnt(8)
	s_waitcnt lgkmcnt(0)
	s_barrier
	s_setprio 1
	s_waitcnt lgkmcnt(6)
	v_mfma_scale_f32_16x16x128_f8f6f4 v[126:129], v[138:145], v[170:177], v[126:129], v243, v243 op_sel_hi:[0,0,0]
	v_mfma_scale_f32_16x16x128_f8f6f4 v[122:125], v[146:153], v[170:177], v[122:125], v243, v243 op_sel_hi:[0,0,0]
	s_waitcnt lgkmcnt(4)
	v_mfma_scale_f32_16x16x128_f8f6f4 v[110:113], v[138:145], v[178:185], v[110:113], v243, v243 op_sel_hi:[0,0,0]
	v_mfma_scale_f32_16x16x128_f8f6f4 v[106:109], v[146:153], v[178:185], v[106:109], v243, v243 op_sel_hi:[0,0,0]
	s_waitcnt lgkmcnt(2)
	v_mfma_scale_f32_16x16x128_f8f6f4 v[206:209], v[138:145], v[186:193], v[92:95], v243, v243 op_sel_hi:[0,0,0]
	v_mfma_scale_f32_16x16x128_f8f6f4 v[210:213], v[146:153], v[186:193], v[88:91], v243, v243 op_sel_hi:[0,0,0]
	s_waitcnt lgkmcnt(0)
	v_mfma_scale_f32_16x16x128_f8f6f4 v[214:217], v[138:145], v[198:205], v[76:79], v243, v243 op_sel_hi:[0,0,0]
	v_mfma_scale_f32_16x16x128_f8f6f4 v[218:221], v[146:153], v[198:205], v[72:75], v243, v243 op_sel_hi:[0,0,0]
	s_setprio 0
	s_setprio 1
	v_mfma_scale_f32_16x16x128_f8f6f4 v[118:121], v[154:161], v[170:177], v[118:121], v243, v243 op_sel_hi:[0,0,0]
	v_mfma_scale_f32_16x16x128_f8f6f4 v[114:117], v[162:169], v[170:177], v[114:117], v243, v243 op_sel_hi:[0,0,0]
	v_mfma_scale_f32_16x16x128_f8f6f4 v[102:105], v[154:161], v[178:185], v[102:105], v243, v243 op_sel_hi:[0,0,0]
	v_mfma_scale_f32_16x16x128_f8f6f4 v[98:101], v[162:169], v[178:185], v[98:101], v243, v243 op_sel_hi:[0,0,0]
	v_mfma_scale_f32_16x16x128_f8f6f4 v[170:173], v[154:161], v[186:193], v[84:87], v243, v243 op_sel_hi:[0,0,0]
	v_mfma_scale_f32_16x16x128_f8f6f4 v[174:177], v[162:169], v[186:193], v[80:83], v243, v243 op_sel_hi:[0,0,0]
	v_mfma_scale_f32_16x16x128_f8f6f4 v[178:181], v[154:161], v[198:205], v[68:71], v243, v243 op_sel_hi:[0,0,0]
	v_mfma_scale_f32_16x16x128_f8f6f4 v[182:185], v[162:169], v[198:205], v[64:67], v243, v243 op_sel_hi:[0,0,0]
	s_setprio 0
	s_barrier
	s_nop 4
	ds_read_b128 v[64:67], v135 offset:16384
	ds_read_b128 v[68:71], v135 offset:17408
	ds_read_b128 v[72:75], v135 offset:18432
	ds_read_b128 v[76:79], v135 offset:19456
	ds_read_b128 v[80:83], v135 offset:20480
	ds_read_b128 v[84:87], v135 offset:21504
	ds_read_b128 v[88:91], v135 offset:22528
	ds_read_b128 v[92:95], v135 offset:23552
	s_mov_b32 m0, s35
	s_nop 0
	global_load_lds_dwordx4 v132, s[24:25]
	s_nop 0
	s_mov_b32 m0, s36
	s_nop 0
	global_load_lds_dwordx4 v136, s[24:25]
	s_add_u32 s64, s24, s8
	s_addc_u32 s65, s25, s9
	s_mov_b32 m0, s37
	s_nop 0
	global_load_lds_dwordx4 v132, s[64:65]
	s_nop 0
	s_mov_b32 m0, s38
	s_nop 0
	global_load_lds_dwordx4 v136, s[64:65]
	s_mov_b32 m0, s34
	s_nop 0
	global_load_lds_dwordx4 v130, s[26:27]
	s_nop 0
	s_mov_b32 m0, s39
	s_nop 0
	global_load_lds_dwordx4 v134, s[26:27]
	s_waitcnt vmcnt(8)
	s_waitcnt lgkmcnt(0)
	s_barrier
	s_setprio 1
	s_waitcnt lgkmcnt(6)
	v_mfma_scale_f32_16x16x128_f8f6f4 v[60:63], v[138:145], v[64:71], v[60:63], v243, v243 op_sel_hi:[0,0,0]
	v_mfma_scale_f32_16x16x128_f8f6f4 v[56:59], v[146:153], v[64:71], v[56:59], v243, v243 op_sel_hi:[0,0,0]
	s_waitcnt lgkmcnt(4)
	v_mfma_scale_f32_16x16x128_f8f6f4 v[186:189], v[138:145], v[72:79], v[44:47], v243, v243 op_sel_hi:[0,0,0]
	v_mfma_scale_f32_16x16x128_f8f6f4 v[190:193], v[146:153], v[72:79], v[40:43], v243, v243 op_sel_hi:[0,0,0]
	s_waitcnt lgkmcnt(2)
	v_mfma_scale_f32_16x16x128_f8f6f4 v[198:201], v[138:145], v[80:87], v[28:31], v243, v243 op_sel_hi:[0,0,0]
	v_mfma_scale_f32_16x16x128_f8f6f4 v[202:205], v[146:153], v[80:87], v[24:27], v243, v243 op_sel_hi:[0,0,0]
	s_waitcnt lgkmcnt(0)
	v_mfma_scale_f32_16x16x128_f8f6f4 v[244:247], v[138:145], v[88:95], v[12:15], v243, v243 op_sel_hi:[0,0,0]
	v_mfma_scale_f32_16x16x128_f8f6f4 v[248:251], v[146:153], v[88:95], v[8:11], v243, v243 op_sel_hi:[0,0,0]
	s_setprio 0
	s_setprio 1
	v_mfma_scale_f32_16x16x128_f8f6f4 v[52:55], v[154:161], v[64:71], v[52:55], v243, v243 op_sel_hi:[0,0,0]
	v_mfma_scale_f32_16x16x128_f8f6f4 v[48:51], v[162:169], v[64:71], v[48:51], v243, v243 op_sel_hi:[0,0,0]
	v_mfma_scale_f32_16x16x128_f8f6f4 v[194:197], v[154:161], v[72:79], v[36:39], v243, v243 op_sel_hi:[0,0,0]
	v_mfma_scale_f32_16x16x128_f8f6f4 v[230:233], v[162:169], v[72:79], v[32:35], v243, v243 op_sel_hi:[0,0,0]
	v_mfma_scale_f32_16x16x128_f8f6f4 v[226:229], v[154:161], v[80:87], v[20:23], v243, v243 op_sel_hi:[0,0,0]
	v_mfma_scale_f32_16x16x128_f8f6f4 v[238:241], v[162:169], v[80:87], v[16:19], v243, v243 op_sel_hi:[0,0,0]
	v_mfma_scale_f32_16x16x128_f8f6f4 v[234:237], v[154:161], v[88:95], v[4:7], v243, v243 op_sel_hi:[0,0,0]
	v_mfma_scale_f32_16x16x128_f8f6f4 v[222:225], v[162:169], v[88:95], v[0:3], v243, v243 op_sel_hi:[0,0,0]
	s_setprio 0
	s_barrier
	v_add_u32_e32 v8, 0x18000, v133
	s_nop 3
	ds_read_b128 v[0:3], v8
	ds_read_b128 v[4:7], v8 offset:1024
	ds_read_b128 v[16:19], v8 offset:2048
	ds_read_b128 v[20:23], v8 offset:3072
	v_add_u32_e32 v8, 0x1c000, v133
	ds_read_b128 v[138:141], v8
	ds_read_b128 v[142:145], v8 offset:1024
	ds_read_b128 v[146:149], v8 offset:2048
	ds_read_b128 v[150:153], v8 offset:3072
	ds_read_b128 v[8:11], v135 offset:32768
	ds_read_b128 v[12:15], v135 offset:33792
	ds_read_b128 v[24:27], v135 offset:34816
	ds_read_b128 v[28:31], v135 offset:35840
	ds_read_b128 v[32:35], v135 offset:36864
	ds_read_b128 v[36:39], v135 offset:37888
	ds_read_b128 v[40:43], v135 offset:38912
	ds_read_b128 v[44:47], v135 offset:39936
	s_add_u32 s26, s26, s8
	s_addc_u32 s27, s27, s9
	s_mov_b32 m0, s40
	s_nop 0
	global_load_lds_dwordx4 v130, s[26:27]
	s_nop 0
	s_mov_b32 m0, s41
	s_nop 0
	global_load_lds_dwordx4 v134, s[26:27]
	s_waitcnt vmcnt(8)
	s_waitcnt lgkmcnt(0)
	s_barrier
	s_setprio 1
	s_waitcnt lgkmcnt(6)
	v_mfma_scale_f32_16x16x128_f8f6f4 v[126:129], v[0:7], v[8:15], v[126:129], v243, v243 op_sel_hi:[0,0,0]
	v_mfma_scale_f32_16x16x128_f8f6f4 v[122:125], v[16:23], v[8:15], v[122:125], v243, v243 op_sel_hi:[0,0,0]
	s_waitcnt lgkmcnt(4)
	v_mfma_scale_f32_16x16x128_f8f6f4 v[110:113], v[0:7], v[24:31], v[110:113], v243, v243 op_sel_hi:[0,0,0]
	v_mfma_scale_f32_16x16x128_f8f6f4 v[106:109], v[16:23], v[24:31], v[106:109], v243, v243 op_sel_hi:[0,0,0]
	s_waitcnt lgkmcnt(2)
	v_mfma_scale_f32_16x16x128_f8f6f4 v[92:95], v[0:7], v[32:39], v[206:209], v243, v243 op_sel_hi:[0,0,0]
	v_mfma_scale_f32_16x16x128_f8f6f4 v[88:91], v[16:23], v[32:39], v[210:213], v243, v243 op_sel_hi:[0,0,0]
	s_waitcnt lgkmcnt(0)
	v_mfma_scale_f32_16x16x128_f8f6f4 v[76:79], v[0:7], v[40:47], v[214:217], v243, v243 op_sel_hi:[0,0,0]
	v_mfma_scale_f32_16x16x128_f8f6f4 v[72:75], v[16:23], v[40:47], v[218:221], v243, v243 op_sel_hi:[0,0,0]
	s_setprio 0
	s_setprio 1
	v_mfma_scale_f32_16x16x128_f8f6f4 v[118:121], v[138:145], v[8:15], v[118:121], v243, v243 op_sel_hi:[0,0,0]
	v_mfma_scale_f32_16x16x128_f8f6f4 v[114:117], v[146:153], v[8:15], v[114:117], v243, v243 op_sel_hi:[0,0,0]
	v_mfma_scale_f32_16x16x128_f8f6f4 v[102:105], v[138:145], v[24:31], v[102:105], v243, v243 op_sel_hi:[0,0,0]
	v_mfma_scale_f32_16x16x128_f8f6f4 v[98:101], v[146:153], v[24:31], v[98:101], v243, v243 op_sel_hi:[0,0,0]
	v_mfma_scale_f32_16x16x128_f8f6f4 v[84:87], v[138:145], v[32:39], v[170:173], v243, v243 op_sel_hi:[0,0,0]
	v_mfma_scale_f32_16x16x128_f8f6f4 v[80:83], v[146:153], v[32:39], v[174:177], v243, v243 op_sel_hi:[0,0,0]
	v_mfma_scale_f32_16x16x128_f8f6f4 v[68:71], v[138:145], v[40:47], v[178:181], v243, v243 op_sel_hi:[0,0,0]
	v_mfma_scale_f32_16x16x128_f8f6f4 v[64:67], v[146:153], v[40:47], v[182:185], v243, v243 op_sel_hi:[0,0,0]
	s_setprio 0
	s_barrier
	ds_read_b128 v[32:35], v135 offset:49152
	ds_read_b128 v[36:39], v135 offset:50176
	ds_read_b128 v[154:157], v135 offset:51200
	ds_read_b128 v[158:161], v135 offset:52224
	ds_read_b128 v[162:165], v135 offset:53248
	ds_read_b128 v[166:169], v135 offset:54272
	ds_read_b128 v[170:173], v135 offset:55296
	ds_read_b128 v[174:177], v135 offset:56320
	s_add_u32 s24, s24, 0x80
	s_addc_u32 s25, s25, 0
	s_mov_b32 m0, s45
	s_nop 0
	global_load_lds_dwordx4 v132, s[24:25]
	s_nop 0
	s_mov_b32 m0, s46
	s_nop 0
	global_load_lds_dwordx4 v136, s[24:25]
	s_add_u32 s24, s24, s8
	s_addc_u32 s25, s25, s9
	s_mov_b32 m0, s49
	s_nop 0
	global_load_lds_dwordx4 v132, s[24:25]
	s_nop 0
	s_mov_b32 m0, s50
	s_nop 0
	global_load_lds_dwordx4 v136, s[24:25]
	s_mov_b32 m0, s47
	s_nop 0
	global_load_lds_dwordx4 v130, s[22:23]
	s_nop 0
	s_mov_b32 m0, s48
	s_nop 0
	global_load_lds_dwordx4 v134, s[22:23]
	s_waitcnt vmcnt(8)
	s_waitcnt lgkmcnt(0)
	s_barrier
	s_setprio 1
	s_waitcnt lgkmcnt(6)
	v_mfma_scale_f32_16x16x128_f8f6f4 v[60:63], v[0:7], v[32:39], v[60:63], v243, v243 op_sel_hi:[0,0,0]
	v_mfma_scale_f32_16x16x128_f8f6f4 v[56:59], v[16:23], v[32:39], v[56:59], v243, v243 op_sel_hi:[0,0,0]
	s_waitcnt lgkmcnt(4)
	v_mfma_scale_f32_16x16x128_f8f6f4 v[44:47], v[0:7], v[154:161], v[186:189], v243, v243 op_sel_hi:[0,0,0]
	v_mfma_scale_f32_16x16x128_f8f6f4 v[40:43], v[16:23], v[154:161], v[190:193], v243, v243 op_sel_hi:[0,0,0]
	s_waitcnt lgkmcnt(2)
	v_mfma_scale_f32_16x16x128_f8f6f4 v[28:31], v[0:7], v[162:169], v[198:201], v243, v243 op_sel_hi:[0,0,0]
	v_mfma_scale_f32_16x16x128_f8f6f4 v[24:27], v[16:23], v[162:169], v[202:205], v243, v243 op_sel_hi:[0,0,0]
	s_waitcnt lgkmcnt(0)
	v_mfma_scale_f32_16x16x128_f8f6f4 v[12:15], v[0:7], v[170:177], v[244:247], v243, v243 op_sel_hi:[0,0,0]
	v_mfma_scale_f32_16x16x128_f8f6f4 v[8:11], v[16:23], v[170:177], v[248:251], v243, v243 op_sel_hi:[0,0,0]
	s_setprio 0
	s_setprio 1
	v_mfma_scale_f32_16x16x128_f8f6f4 v[52:55], v[138:145], v[32:39], v[52:55], v243, v243 op_sel_hi:[0,0,0]
	v_mfma_scale_f32_16x16x128_f8f6f4 v[48:51], v[146:153], v[32:39], v[48:51], v243, v243 op_sel_hi:[0,0,0]
	v_mfma_scale_f32_16x16x128_f8f6f4 v[36:39], v[138:145], v[154:161], v[194:197], v243, v243 op_sel_hi:[0,0,0]
	v_mfma_scale_f32_16x16x128_f8f6f4 v[32:35], v[146:153], v[154:161], v[230:233], v243, v243 op_sel_hi:[0,0,0]
	v_mfma_scale_f32_16x16x128_f8f6f4 v[20:23], v[138:145], v[162:169], v[226:229], v243, v243 op_sel_hi:[0,0,0]
	v_mfma_scale_f32_16x16x128_f8f6f4 v[16:19], v[146:153], v[162:169], v[238:241], v243, v243 op_sel_hi:[0,0,0]
	v_mfma_scale_f32_16x16x128_f8f6f4 v[4:7], v[138:145], v[170:177], v[234:237], v243, v243 op_sel_hi:[0,0,0]
	v_mfma_scale_f32_16x16x128_f8f6f4 v[0:3], v[146:153], v[170:177], v[222:225], v243, v243 op_sel_hi:[0,0,0]
	s_setprio 0
	s_barrier
	s_add_u32 s59, s59, 0x100
	s_addc_u32 s60, s60, 0
	s_add_u32 s61, s61, 0x100
	s_addc_u32 s62, s62, 0
	s_add_u32 s20, s20, 0x100
	s_addc_u32 s21, s21, 0
	s_cmp_ge_i32 s63, s42
	s_mov_b32 s22, s63
	s_cbranch_scc0 .LBB0_272
	v_mov_b32_e32 v239, 1
	v_mov_b32_e32 v240, 0x260
	v_mov_b32_e32 v241, 0x358637bd
	v_mov_b32_e32 v224, 0x3727c5ac
	v_bfrev_b32_e32 v226, -2
	v_mov_b32_e32 v227, 0x600
	v_mov_b64_e32 v[230:231], 0x100
	v_mov_b64_e32 v[232:233], 0xff
	v_mov_b32_e32 v229, 0x3d800000

.LBB0_827:
	s_or_b64 exec, exec, s[18:19]
	s_lshl_b32 s3, s24, 1
	s_add_u32 s18, s31, s3
	s_addc_u32 s19, s34, 0
	s_lshl_b32 s2, s2, 6
	s_ashr_i32 s3, s2, 31
	v_lshlrev_b64 v[4:5], 9, v[4:5]
	s_lshl_b64 s[2:3], s[2:3], 1
	s_lshl_b64 s[20:21], s[22:23], 9
	v_lshl_add_u64 v[4:5], s[18:19], 0, v[4:5]
	s_add_u32 s18, s18, s20
	s_addc_u32 s19, s19, s21
	v_lshl_add_u64 v[4:5], v[4:5], 0, s[2:3]
	s_add_u32 s2, s18, s2
	s_addc_u32 s3, s19, s3
	s_add_u32 s18, s2, 0x800000
	s_addc_u32 s19, s3, 0
	s_add_u32 s20, s2, 0x1000000
	s_addc_u32 s21, s3, 0
	s_ashr_i32 s50, s25, 6
	s_lshl_b32 s22, s50, 4
	v_add_u32_e32 v247, s22, v208
	v_and_or_b32 v7, s22, 48, v209
	s_ashr_i32 s22, s25, 3
	s_and_b32 s22, s22, 0x7fffffe0
	v_lshl_add_u32 v7, v7, 8, s22
	s_lshl_b32 s22, s50, 10
	s_cmp_lg_u32 0, -1
	s_cselect_b32 s23, 0, 0
	s_add_i32 s53, s22, s23
	v_or_b32_e32 v7, v7, v210
	s_add_i32 s54, s53, 0x6000
	s_mov_b32 m0, s53
	s_nop 0
	global_load_lds_dwordx4 v247, s[18:19]
	v_lshlrev_b32_e32 v248, 1, v7
	s_mov_b32 m0, s54
	s_nop 0
	global_load_lds_dwordx4 v248, s[20:21]
	s_add_u32 s2, s2, 0x808000
	s_addc_u32 s3, s3, 0
	s_add_i32 s23, s53, 0x2000
	s_mov_b32 m0, s23
	s_nop 0
	global_load_lds_dwordx4 v247, s[2:3]
	v_lshl_add_u64 v[4:5], v[4:5], 0, v[96:97]
	global_load_dwordx4 v[110:113], v[4:5], off
	global_load_dwordx4 v[106:109], v[4:5], off offset:32
	global_load_dwordx4 v[102:105], v[4:5], off offset:64
	global_load_dwordx4 v[98:101], v[4:5], off offset:96
	v_add_u32_e32 v4, 0, v211
	v_add_u32_e32 v4, 0x14800, v4
	s_waitcnt vmcnt(4)
	ds_write_b128 v4, v[0:3]
	s_and_saveexec_b64 s[2:3], s[40:41]
	v_lshl_add_u32 v0, s50, 7, v215
	ds_write_b32 v0, v6
	s_or_b64 exec, exec, s[2:3]
	s_add_u32 s2, s18, 0x10000
	s_addc_u32 s3, s19, 0
	s_cmp_lg_u32 0, -1
	s_cselect_b32 s23, 0, 0
	s_add_i32 s23, s23, s22
	s_addk_i32 s23, 0x4000
	s_mov_b32 m0, s23
	s_nop 0
	global_load_lds_dwordx4 v247, s[2:3]
	s_waitcnt vmcnt(3) lgkmcnt(0)
	s_barrier
	ds_read_b128 v[16:19], v214 offset:128
	ds_read_b128 v[0:3], v214
	ds_read_b128 v[4:7], v214 offset:32
	ds_read_b128 v[20:23], v214 offset:160
	ds_read_b128 v[8:11], v214 offset:64
	ds_read_b128 v[24:27], v214 offset:192
	ds_read_b128 v[12:15], v214 offset:96
	ds_read_b128 v[28:31], v214 offset:224
	ds_read_b128 v[34:37], v213
	ds_read_b128 v[38:41], v213 offset:512
	s_waitcnt lgkmcnt(5)
	v_sub_f32_e32 v11, v32, v11
	v_sub_f32_e32 v10, v32, v10
	s_waitcnt lgkmcnt(3)
	v_sub_f32_e32 v15, v32, v15
	v_sub_f32_e32 v14, v32, v14
	v_sub_f32_e32 v13, v32, v13
	v_sub_f32_e32 v12, v32, v12
	v_sub_f32_e32 v9, v32, v9
	v_sub_f32_e32 v8, v32, v8
	v_sub_f32_e32 v7, v32, v7
	v_sub_f32_e32 v6, v32, v6
	v_sub_f32_e32 v5, v32, v5
	v_sub_f32_e32 v4, v32, v4
	v_sub_f32_e32 v3, v32, v3
	v_sub_f32_e32 v2, v32, v2
	v_sub_f32_e32 v1, v32, v1
	v_sub_f32_e32 v0, v32, v0
	s_waitcnt lgkmcnt(2)
	v_sub_f32_e32 v31, v32, v31
	v_sub_f32_e32 v30, v32, v30
	v_sub_f32_e32 v29, v32, v29
	v_sub_f32_e32 v28, v32, v28
	v_sub_f32_e32 v27, v32, v27
	v_sub_f32_e32 v26, v32, v26
	v_sub_f32_e32 v25, v32, v25
	v_sub_f32_e32 v24, v32, v24
	v_sub_f32_e32 v23, v32, v23
	v_sub_f32_e32 v22, v32, v22
	v_sub_f32_e32 v21, v32, v21
	v_sub_f32_e32 v20, v32, v20
	v_sub_f32_e32 v19, v32, v19
	v_sub_f32_e32 v18, v32, v18
	v_sub_f32_e32 v17, v32, v17
	v_sub_f32_e32 v16, v32, v16
	s_waitcnt vmcnt(3) lgkmcnt(1)
	v_mfma_f32_32x32x16_bf16 v[0:15], v[34:37], v[110:113], v[0:15]
	s_cmp_gt_i32 s52, 4
	s_cselect_b64 s[2:3], -1, 0
	s_xor_b64 s[26:27], s[16:17], -1
	s_or_b64 s[2:3], s[26:27], s[2:3]
	v_lshl_or_b32 v246, s50, 5, v198
	s_and_b64 vcc, exec, s[2:3]
	s_waitcnt lgkmcnt(0)
	v_mfma_f32_32x32x16_bf16 v[16:31], v[38:41], v[110:113], v[16:31]
	ds_read_b128 v[34:37], v213 offset:2048
	ds_read_b128 v[38:41], v213 offset:2560
	s_waitcnt vmcnt(2) lgkmcnt(1)
	v_mfma_f32_32x32x16_bf16 v[0:15], v[34:37], v[106:109], v[0:15]
	s_waitcnt lgkmcnt(0)
	v_mfma_f32_32x32x16_bf16 v[16:31], v[38:41], v[106:109], v[16:31]
	ds_read_b128 v[34:37], v213 offset:4096
	ds_read_b128 v[38:41], v213 offset:4608
	s_waitcnt vmcnt(1) lgkmcnt(1)
	v_mfma_f32_32x32x16_bf16 v[0:15], v[34:37], v[102:105], v[0:15]
	s_waitcnt lgkmcnt(0)
	v_mfma_f32_32x32x16_bf16 v[16:31], v[38:41], v[102:105], v[16:31]
	ds_read_b128 v[34:37], v213 offset:6144
	ds_read_b128 v[38:41], v213 offset:6656
	s_waitcnt vmcnt(0) lgkmcnt(1)
	v_mfma_f32_32x32x16_bf16 v[0:15], v[34:37], v[98:101], v[0:15]
	s_waitcnt lgkmcnt(0)
	v_mfma_f32_32x32x16_bf16 v[16:31], v[38:41], v[98:101], v[16:31]
	s_nop 15
	s_nop 7
	s_cbranch_vccnz .LBB0_831
	v_subrev_u32_e32 v33, s28, v206
	v_add_u32_e32 v35, 0x120, v33
	v_add_u32_e32 v34, 0x100, v33
	v_cmp_le_i32_e32 vcc, v35, v246
	s_nop 6
	v_cndmask_b32_e32 v16, v242, v16, vcc
	v_cmp_lt_i32_e32 vcc, v34, v246
	s_nop 1
	v_cndmask_b32_e32 v1, v242, v1, vcc
	v_cmp_le_i32_e32 vcc, v34, v246
	v_add_u32_e32 v34, 0x121, v33
	s_nop 0
	v_cndmask_b32_e32 v0, v242, v0, vcc
	v_cmp_le_i32_e32 vcc, v34, v246
	v_add_u32_e32 v34, 0x102, v33
	s_nop 0
	v_cndmask_b32_e32 v17, v242, v17, vcc
	v_cmp_le_i32_e32 vcc, v34, v246
	v_add_u32_e32 v34, 0x122, v33
	s_nop 0
	v_cndmask_b32_e32 v2, v242, v2, vcc
	v_cmp_le_i32_e32 vcc, v34, v246
	v_add_u32_e32 v34, 0x103, v33
	s_nop 0
	v_cndmask_b32_e32 v18, v242, v18, vcc
	v_cmp_le_i32_e32 vcc, v34, v246
	v_add_u32_e32 v34, 0x123, v33
	s_nop 0
	v_cndmask_b32_e32 v3, v242, v3, vcc
	v_cmp_le_i32_e32 vcc, v34, v246
	v_add_u32_e32 v34, 0x108, v33
	s_nop 0
	v_cndmask_b32_e32 v19, v242, v19, vcc
	v_cmp_le_i32_e32 vcc, v34, v246
	v_add_u32_e32 v34, 0x128, v33
	s_nop 0
	v_cndmask_b32_e32 v4, v242, v4, vcc
	v_cmp_le_i32_e32 vcc, v34, v246
	v_add_u32_e32 v34, 0x109, v33
	s_nop 0
	v_cndmask_b32_e32 v20, v242, v20, vcc
	v_cmp_le_i32_e32 vcc, v34, v246
	v_add_u32_e32 v34, 0x129, v33
	s_nop 0
	v_cndmask_b32_e32 v5, v242, v5, vcc
	v_cmp_le_i32_e32 vcc, v34, v246
	v_add_u32_e32 v34, 0x10a, v33
	s_nop 0
	v_cndmask_b32_e32 v21, v242, v21, vcc
	v_cmp_le_i32_e32 vcc, v34, v246
	v_add_u32_e32 v34, 0x12a, v33
	s_nop 0
	v_cndmask_b32_e32 v6, v242, v6, vcc
	v_cmp_le_i32_e32 vcc, v34, v246
	v_add_u32_e32 v34, 0x10b, v33
	s_nop 0
	v_cndmask_b32_e32 v22, v242, v22, vcc
	v_cmp_le_i32_e32 vcc, v34, v246
	v_add_u32_e32 v34, 0x12b, v33
	s_nop 0
	v_cndmask_b32_e32 v7, v242, v7, vcc
	v_cmp_le_i32_e32 vcc, v34, v246
	v_add_u32_e32 v34, 0x110, v33
	s_nop 0
	v_cndmask_b32_e32 v23, v242, v23, vcc
	v_cmp_le_i32_e32 vcc, v34, v246
	v_add_u32_e32 v34, 0x130, v33
	s_nop 0
	v_cndmask_b32_e32 v8, v242, v8, vcc
	v_cmp_le_i32_e32 vcc, v34, v246
	v_add_u32_e32 v34, 0x111, v33
	s_nop 0
	v_cndmask_b32_e32 v24, v242, v24, vcc
	v_cmp_le_i32_e32 vcc, v34, v246
	v_add_u32_e32 v34, 0x131, v33
	s_nop 0
	v_cndmask_b32_e32 v9, v242, v9, vcc
	v_cmp_le_i32_e32 vcc, v34, v246
	v_add_u32_e32 v34, 0x112, v33
	s_nop 0
	v_cndmask_b32_e32 v25, v242, v25, vcc
	v_cmp_le_i32_e32 vcc, v34, v246
	v_add_u32_e32 v34, 0x132, v33
	s_nop 0
	v_cndmask_b32_e32 v10, v242, v10, vcc
	v_cmp_le_i32_e32 vcc, v34, v246
	v_add_u32_e32 v34, 0x113, v33
	s_nop 0
	v_cndmask_b32_e32 v26, v242, v26, vcc
	v_cmp_le_i32_e32 vcc, v34, v246
	v_add_u32_e32 v34, 0x133, v33
	s_nop 0
	v_cndmask_b32_e32 v11, v242, v11, vcc
	v_cmp_le_i32_e32 vcc, v34, v246
	v_add_u32_e32 v34, 0x118, v33
	s_nop 0
	v_cndmask_b32_e32 v27, v242, v27, vcc
	v_cmp_le_i32_e32 vcc, v34, v246
	v_add_u32_e32 v34, 0x138, v33
	s_nop 0
	v_cndmask_b32_e32 v12, v242, v12, vcc
	v_cmp_le_i32_e32 vcc, v34, v246
	v_add_u32_e32 v34, 0x119, v33
	s_nop 0
	v_cndmask_b32_e32 v28, v242, v28, vcc
	v_cmp_le_i32_e32 vcc, v34, v246
	v_add_u32_e32 v34, 0x139, v33
	s_nop 0
	v_cndmask_b32_e32 v13, v242, v13, vcc
	v_cmp_le_i32_e32 vcc, v34, v246
	v_add_u32_e32 v34, 0x11a, v33
	s_nop 0
	v_cndmask_b32_e32 v29, v242, v29, vcc
	v_cmp_le_i32_e32 vcc, v34, v246
	v_add_u32_e32 v34, 0x13a, v33
	s_nop 0
	v_cndmask_b32_e32 v14, v242, v14, vcc
	v_cmp_le_i32_e32 vcc, v34, v246
	v_add_u32_e32 v34, 0x11b, v33
	v_add_u32_e32 v33, 0x13b, v33
	v_cndmask_b32_e32 v30, v242, v30, vcc
	v_cmp_le_i32_e32 vcc, v34, v246
	s_nop 1
	v_cndmask_b32_e32 v15, v242, v15, vcc
	v_cmp_le_i32_e32 vcc, v33, v246
	s_nop 1
	v_cndmask_b32_e32 v31, v242, v31, vcc
.LBB0_831:
	v_max3_f32 v33, v0, v1, v16
	v_max3_f32 v34, v2, v3, v17
	s_and_b32 s2, s25, 0x3fffffc0
	v_max3_f32 v33, v33, v18, v19
	v_max3_f32 v34, v34, v6, v7
	s_lshl_b32 s2, s2, 2
	v_max3_f32 v33, v33, v4, v5
	v_max3_f32 v34, v34, v22, v23
	s_add_i32 s51, s2, 0
	v_max3_f32 v33, v33, v20, v21
	v_max3_f32 v34, v34, v10, v11
	s_add_u32 s2, s18, 0x18000
	v_max3_f32 v33, v33, v8, v9
	v_max3_f32 v34, v34, v26, v27
	s_addc_u32 s3, s19, 0
	v_max3_f32 v33, v33, v24, v25
	v_max3_f32 v34, v34, v14, v15
	s_mov_b32 s29, 0
	v_max3_f32 v33, v33, v12, v13
	v_max3_f32 v34, v34, v30, v31
	v_lshl_add_u32 v245, v198, 2, s51
	v_max3_f32 v33, v33, v28, v29
	s_nop 0
	v_max_f32_e32 v33, v33, v34
	s_nop 0
	v_mov_b32_e32 v34, v33
	s_nop 1
	v_permlane32_swap_b32_e32 v33, v34
	v_max_f32_e32 v33, v33, v34
	s_nop 0
	v_sub_f32_e32 v0, v0, v33
	v_sub_f32_e32 v16, v16, v33
	v_sub_f32_e32 v1, v1, v33
	v_sub_f32_e32 v17, v17, v33
	v_sub_f32_e32 v2, v2, v33
	v_sub_f32_e32 v18, v18, v33
	v_sub_f32_e32 v3, v3, v33
	v_sub_f32_e32 v19, v19, v33
	v_sub_f32_e32 v4, v4, v33
	v_sub_f32_e32 v20, v20, v33
	v_sub_f32_e32 v5, v5, v33
	v_sub_f32_e32 v21, v21, v33
	v_sub_f32_e32 v6, v6, v33
	v_sub_f32_e32 v22, v22, v33
	v_sub_f32_e32 v7, v7, v33
	v_sub_f32_e32 v23, v23, v33
	v_sub_f32_e32 v8, v8, v33
	v_sub_f32_e32 v24, v24, v33
	v_sub_f32_e32 v9, v9, v33
	v_sub_f32_e32 v25, v25, v33
	v_sub_f32_e32 v10, v10, v33
	v_sub_f32_e32 v26, v26, v33
	v_sub_f32_e32 v11, v11, v33
	v_sub_f32_e32 v27, v27, v33
	v_sub_f32_e32 v12, v12, v33
	v_sub_f32_e32 v28, v28, v33
	v_sub_f32_e32 v13, v13, v33
	v_sub_f32_e32 v29, v29, v33
	v_sub_f32_e32 v14, v14, v33
	v_sub_f32_e32 v30, v30, v33
	v_sub_f32_e32 v15, v15, v33
	v_sub_f32_e32 v31, v31, v33
	s_nop 0
	v_exp_f32_e32 v80, v0
	v_exp_f32_e32 v81, v1
	v_exp_f32_e32 v82, v2
	v_exp_f32_e32 v83, v3
	v_exp_f32_e32 v84, v4
	v_exp_f32_e32 v85, v5
	v_exp_f32_e32 v86, v6
	v_exp_f32_e32 v87, v7
	v_exp_f32_e32 v88, v8
	v_exp_f32_e32 v89, v9
	v_exp_f32_e32 v90, v10
	v_exp_f32_e32 v91, v11
	v_exp_f32_e32 v92, v12
	v_exp_f32_e32 v93, v13
	v_exp_f32_e32 v94, v14
	v_exp_f32_e32 v95, v15
	v_exp_f32_e32 v64, v16
	v_exp_f32_e32 v65, v17
	v_exp_f32_e32 v66, v18
	v_exp_f32_e32 v67, v19
	v_exp_f32_e32 v68, v20
	v_exp_f32_e32 v69, v21
	v_exp_f32_e32 v70, v22
	v_exp_f32_e32 v71, v23
	v_exp_f32_e32 v72, v24
	v_exp_f32_e32 v73, v25
	v_exp_f32_e32 v74, v26
	v_exp_f32_e32 v75, v27
	v_exp_f32_e32 v76, v28
	v_exp_f32_e32 v77, v29
	v_exp_f32_e32 v78, v30
	v_exp_f32_e32 v79, v31
	ds_read_b128 v[0:3], v214 offset:256
	ds_read_b128 v[4:7], v214 offset:288
	ds_read_b128 v[8:11], v214 offset:320
	ds_read_b128 v[12:15], v214 offset:352
	ds_read_b128 v[16:19], v214 offset:384
	ds_read_b128 v[20:23], v214 offset:416
	ds_read_b128 v[24:27], v214 offset:448
	ds_read_b128 v[28:31], v214 offset:480
	s_waitcnt vmcnt(0) lgkmcnt(0)
	s_barrier
	s_mov_b32 m0, s53
	s_nop 0
	global_load_lds_dwordx4 v247, s[2:3]
	s_add_u32 s2, s20, 0x8000
	s_addc_u32 s3, s21, 0
	s_cmp_lg_u32 0, -1
	s_cselect_b32 s23, 0, 0
	s_add_i32 s22, s23, s22
	s_add_i32 s22, s22, 0x8000
	s_mov_b32 m0, s22
	s_nop 0
	global_load_lds_dwordx4 v248, s[2:3]
	ds_read_b128 v[158:161], v213 offset:8192
	ds_read_b128 v[154:157], v213 offset:8704
	ds_read_b128 v[150:153], v213 offset:10240
	ds_read_b128 v[146:149], v213 offset:10752
	ds_read_b128 v[142:145], v213 offset:12288
	ds_read_b128 v[138:141], v213 offset:12800
	ds_read_b128 v[134:137], v213 offset:14336
	ds_read_b128 v[130:133], v213 offset:14848
	s_waitcnt vmcnt(2) lgkmcnt(0)
	s_barrier
	v_add_f32_e32 v244, v97, v33
	v_sub_f32_e32 v249, v32, v33
	s_cmp_lt_i32 s52, 7
	s_waitcnt lgkmcnt(12)
	v_sub_f32_e32 v63, v249, v15
	v_sub_f32_e32 v62, v249, v14
	v_sub_f32_e32 v61, v249, v13
	v_sub_f32_e32 v60, v249, v12
	v_sub_f32_e32 v59, v249, v11
	v_sub_f32_e32 v58, v249, v10
	v_sub_f32_e32 v57, v249, v9
	v_sub_f32_e32 v56, v249, v8
	v_sub_f32_e32 v55, v249, v7
	v_sub_f32_e32 v54, v249, v6
	v_sub_f32_e32 v53, v249, v5
	v_sub_f32_e32 v52, v249, v4
	v_sub_f32_e32 v51, v249, v3
	v_sub_f32_e32 v50, v249, v2
	v_sub_f32_e32 v49, v249, v1
	v_sub_f32_e32 v48, v249, v0
	s_waitcnt lgkmcnt(8)
	v_sub_f32_e32 v47, v249, v31
	v_sub_f32_e32 v46, v249, v30
	v_sub_f32_e32 v45, v249, v29
	v_sub_f32_e32 v44, v249, v28
	v_sub_f32_e32 v43, v249, v27
	v_sub_f32_e32 v42, v249, v26
	v_sub_f32_e32 v41, v249, v25
	v_sub_f32_e32 v40, v249, v24
	v_sub_f32_e32 v39, v249, v23
	v_sub_f32_e32 v38, v249, v22
	v_sub_f32_e32 v37, v249, v21
	v_sub_f32_e32 v36, v249, v20
	v_sub_f32_e32 v35, v249, v19
	v_sub_f32_e32 v34, v249, v18
	v_sub_f32_e32 v33, v249, v17
	v_sub_f32_e32 v32, v249, v16
	s_cbranch_scc1 .LBB0_847
	s_add_u32 s2, s20, 0x18000
	s_addc_u32 s3, s21, 0
	v_mov_b32_e32 v16, v97
	v_mov_b32_e32 v17, v97
	s_add_u32 s22, s18, 0x28000
	v_mov_b32_e32 v18, v97
	v_mov_b32_e32 v19, v97
	v_mov_b32_e32 v20, v97
	v_mov_b32_e32 v21, v97
	v_mov_b32_e32 v22, v97
	v_mov_b32_e32 v23, v97
	v_mov_b32_e32 v24, v97
	v_mov_b32_e32 v25, v97
	v_mov_b32_e32 v26, v97
	v_mov_b32_e32 v27, v97
	v_mov_b32_e32 v28, v97
	v_mov_b32_e32 v29, v97
	v_mov_b32_e32 v30, v97
	v_mov_b32_e32 v31, v97
	v_mov_b64_e32 v[0:1], v[16:17]
	s_addc_u32 s23, s19, 0
	s_mov_b32 s24, 0
	s_movk_i32 s29, 0x4000
	s_movk_i32 s58, 0x2000
	v_mov_b32_e32 v250, 0
	s_mov_b32 s57, 6
	v_mov_b32_e32 v166, v221
	v_mov_b64_e32 v[2:3], v[18:19]
	v_mov_b64_e32 v[4:5], v[20:21]
	v_mov_b64_e32 v[6:7], v[22:23]
	v_mov_b64_e32 v[8:9], v[24:25]
	v_mov_b64_e32 v[10:11], v[26:27]
	v_mov_b64_e32 v[12:13], v[28:29]
	v_mov_b64_e32 v[14:15], v[30:31]
.LBB0_833:
	v_add_u32_e32 v167, s24, v212
	ds_read_b64_tr_b16 v[162:163], v167 offset:24576
	ds_read_b64_tr_b16 v[164:165], v167 offset:25088
	s_waitcnt lgkmcnt(9)
	v_mfma_f32_32x32x16_bf16 v[48:63], v[158:161], v[110:113], v[48:63]
	v_add_f32_e32 v114, v80, v81
	v_add_f32_e32 v114, v82, v114
	v_add_f32_e32 v114, v83, v114
	v_add_f32_e32 v114, v84, v114
	v_add_f32_e32 v114, v85, v114
	v_cvt_pk_bf16_f32 v126, v80, v81
	v_cvt_pk_bf16_f32 v127, v82, v83
	ds_read_b64_tr_b16 v[80:81], v167 offset:28672
	ds_read_b64_tr_b16 v[82:83], v167 offset:29184
	s_waitcnt lgkmcnt(10)
	v_mfma_f32_32x32x16_bf16 v[32:47], v[154:157], v[110:113], v[32:47]
	v_add_f32_e32 v114, v86, v114
	v_add_f32_e32 v114, v87, v114
	v_add_f32_e32 v114, v88, v114
	v_add_f32_e32 v114, v89, v114
	v_cvt_pk_bf16_f32 v128, v84, v85
	v_cvt_pk_bf16_f32 v129, v86, v87
	ds_read_b64_tr_b16 v[84:85], v167 offset:25600
	ds_read_b64_tr_b16 v[86:87], v167 offset:26112
	s_waitcnt lgkmcnt(11)
	v_mfma_f32_32x32x16_bf16 v[48:63], v[150:153], v[106:109], v[48:63]
	v_add_f32_e32 v114, v90, v114
	v_add_f32_e32 v114, v91, v114
	v_add_f32_e32 v114, v92, v114
	v_add_f32_e32 v114, v93, v114
	v_cvt_pk_bf16_f32 v122, v88, v89
	v_cvt_pk_bf16_f32 v123, v90, v91
	ds_read_b64_tr_b16 v[88:89], v167 offset:29696
	ds_read_b64_tr_b16 v[90:91], v167 offset:30208
	s_waitcnt lgkmcnt(12)
	v_mfma_f32_32x32x16_bf16 v[32:47], v[146:149], v[106:109], v[32:47]
	v_add_f32_e32 v114, v94, v114
	v_add_f32_e32 v114, v95, v114
	v_add_f32_e32 v114, v64, v114
	v_add_f32_e32 v114, v65, v114
	v_cvt_pk_bf16_f32 v124, v92, v93
	v_cvt_pk_bf16_f32 v125, v94, v95
	ds_read_b64_tr_b16 v[92:93], v167 offset:26624
	ds_read_b64_tr_b16 v[94:95], v167 offset:27136
	s_waitcnt lgkmcnt(13)
	v_mfma_f32_32x32x16_bf16 v[48:63], v[142:145], v[102:105], v[48:63]
	v_add_f32_e32 v114, v66, v114
	v_add_f32_e32 v114, v67, v114
	v_add_f32_e32 v114, v68, v114
	v_add_f32_e32 v114, v69, v114
	v_cvt_pk_bf16_f32 v118, v64, v65
	v_cvt_pk_bf16_f32 v119, v66, v67
	ds_read_b64_tr_b16 v[64:65], v167 offset:30720
	ds_read_b64_tr_b16 v[66:67], v167 offset:31232
	s_waitcnt lgkmcnt(14)
	v_mfma_f32_32x32x16_bf16 v[32:47], v[138:141], v[102:105], v[32:47]
	v_add_f32_e32 v114, v70, v114
	v_add_f32_e32 v114, v71, v114
	v_add_f32_e32 v114, v72, v114
	v_add_f32_e32 v114, v73, v114
	v_cvt_pk_bf16_f32 v120, v68, v69
	v_cvt_pk_bf16_f32 v121, v70, v71
	ds_read_b64_tr_b16 v[68:69], v167 offset:27648
	ds_read_b64_tr_b16 v[70:71], v167 offset:28160
	s_waitcnt lgkmcnt(14)
	v_mfma_f32_32x32x16_bf16 v[48:63], v[134:137], v[98:101], v[48:63]
	v_add_f32_e32 v114, v74, v114
	v_add_f32_e32 v114, v75, v114
	v_add_f32_e32 v114, v76, v114
	v_add_f32_e32 v134, v77, v114
	v_cvt_pk_bf16_f32 v114, v72, v73
	v_cvt_pk_bf16_f32 v115, v74, v75
	ds_read_b64_tr_b16 v[72:73], v167 offset:31744
	ds_read_b64_tr_b16 v[74:75], v167 offset:32256
	v_mfma_f32_32x32x16_bf16 v[32:47], v[130:133], v[98:101], v[32:47]
	v_add_f32_e32 v116, v78, v134
	v_add_f32_e32 v116, v79, v116
	v_add_f32_e32 v130, 0, v116
	v_cvt_pk_bf16_f32 v116, v76, v77
	v_cvt_pk_bf16_f32 v117, v78, v79
	v_max_f32_e32 v76, v49, v49
	v_max_f32_e32 v77, v48, v48
	v_max_f32_e32 v76, v77, v76
	s_nop 3
	v_max3_f32 v77, v50, v51, v33
	v_max3_f32 v76, v76, v32, v34
	v_max3_f32 v76, v76, v35, v52
	v_max3_f32 v77, v77, v54, v55
	v_max3_f32 v76, v76, v53, v36
	v_max3_f32 v77, v77, v38, v39
	v_max3_f32 v76, v76, v37, v56
	v_max3_f32 v77, v77, v58, v59
	v_max3_f32 v76, v76, v57, v40
	v_max3_f32 v77, v77, v42, v43
	v_max3_f32 v76, v76, v41, v60
	v_max3_f32 v77, v77, v62, v63
	v_max3_f32 v76, v76, v61, v44
	v_max3_f32 v77, v77, v46, v47
	v_max3_f32 v76, v76, v45, v77
	s_add_u32 s24, s22, 0xffff8000
	v_mov_b32_e32 v77, v76
	s_addc_u32 s25, s23, -1
	s_add_i32 s26, s58, s53
	v_permlane32_swap_b32_e32 v76, v77
	s_mov_b32 m0, s26
	s_nop 0
	global_load_lds_dwordx4 v247, s[24:25]
	s_add_u32 s24, s2, 0xffff8000
	v_max_f32_e32 v77, v77, v77
	v_max_f32_e32 v76, v76, v76
	s_addc_u32 s25, s3, -1
	s_add_i32 s26, s29, s54
	s_mov_b32 m0, s26
	s_nop 0
	global_load_lds_dwordx4 v248, s[24:25]
	v_max_f32_e32 v76, v76, v77
	s_mov_b32 s24, 0x41000000
	v_cmp_lt_f32_e32 vcc, s24, v76
	s_cmp_lg_u64 vcc, 0
	v_add_f32_e32 v167, v250, v130
	s_cselect_b64 s[24:25], -1, 0
	s_cbranch_vccnz .LBB0_841

.LBB0_836:
	s_add_i32 s24, s29, 0x2000
	s_cmpk_lg_i32 s29, 0x4000
	s_cselect_b32 s55, s24, 0
	v_add_u32_e32 v168, s58, v212
	ds_read_b64_tr_b16 v[150:151], v168 offset:24576
	ds_read_b64_tr_b16 v[152:153], v168 offset:25088
	s_waitcnt lgkmcnt(9)
	v_mfma_f32_32x32x16_bf16 v[80:95], v[162:165], v[110:113], v[80:95]
	v_add_f32_e32 v114, v48, v49
	v_add_f32_e32 v114, v50, v114
	v_add_f32_e32 v114, v51, v114
	v_add_f32_e32 v114, v52, v114
	v_add_f32_e32 v114, v53, v114
	v_cvt_pk_bf16_f32 v126, v48, v49
	v_cvt_pk_bf16_f32 v127, v50, v51
	ds_read_b64_tr_b16 v[48:49], v168 offset:28672
	ds_read_b64_tr_b16 v[50:51], v168 offset:29184
	s_waitcnt lgkmcnt(10)
	v_mfma_f32_32x32x16_bf16 v[64:79], v[158:161], v[110:113], v[64:79]
	v_add_f32_e32 v114, v54, v114
	v_add_f32_e32 v114, v55, v114
	v_add_f32_e32 v114, v56, v114
	v_add_f32_e32 v114, v57, v114
	v_cvt_pk_bf16_f32 v128, v52, v53
	v_cvt_pk_bf16_f32 v129, v54, v55
	ds_read_b64_tr_b16 v[52:53], v168 offset:25600
	ds_read_b64_tr_b16 v[54:55], v168 offset:26112
	s_waitcnt lgkmcnt(11)
	v_mfma_f32_32x32x16_bf16 v[80:95], v[154:157], v[106:109], v[80:95]
	v_add_f32_e32 v114, v58, v114
	v_add_f32_e32 v114, v59, v114
	v_add_f32_e32 v114, v60, v114
	v_add_f32_e32 v114, v61, v114
	v_cvt_pk_bf16_f32 v122, v56, v57
	v_cvt_pk_bf16_f32 v123, v58, v59
	ds_read_b64_tr_b16 v[56:57], v168 offset:29696
	ds_read_b64_tr_b16 v[58:59], v168 offset:30208
	s_waitcnt lgkmcnt(12)
	v_mfma_f32_32x32x16_bf16 v[64:79], v[146:149], v[106:109], v[64:79]
	v_add_f32_e32 v114, v62, v114
	v_add_f32_e32 v114, v63, v114
	v_add_f32_e32 v114, v32, v114
	v_add_f32_e32 v114, v33, v114
	v_cvt_pk_bf16_f32 v124, v60, v61
	v_cvt_pk_bf16_f32 v125, v62, v63
	ds_read_b64_tr_b16 v[60:61], v168 offset:26624
	ds_read_b64_tr_b16 v[62:63], v168 offset:27136
	s_waitcnt lgkmcnt(13)
	v_mfma_f32_32x32x16_bf16 v[80:95], v[142:145], v[102:105], v[80:95]
	v_add_f32_e32 v114, v34, v114
	v_add_f32_e32 v114, v35, v114
	v_add_f32_e32 v114, v36, v114
	v_add_f32_e32 v114, v37, v114
	v_cvt_pk_bf16_f32 v118, v32, v33
	v_cvt_pk_bf16_f32 v119, v34, v35
	ds_read_b64_tr_b16 v[32:33], v168 offset:30720
	ds_read_b64_tr_b16 v[34:35], v168 offset:31232
	s_waitcnt lgkmcnt(14)
	v_mfma_f32_32x32x16_bf16 v[64:79], v[138:141], v[102:105], v[64:79]
	v_add_f32_e32 v114, v38, v114
	v_add_f32_e32 v114, v39, v114
	v_add_f32_e32 v114, v40, v114
	v_add_f32_e32 v114, v41, v114
	v_cvt_pk_bf16_f32 v120, v36, v37
	v_cvt_pk_bf16_f32 v121, v38, v39
	ds_read_b64_tr_b16 v[36:37], v168 offset:27648
	ds_read_b64_tr_b16 v[38:39], v168 offset:28160
	s_waitcnt lgkmcnt(14)
	v_mfma_f32_32x32x16_bf16 v[80:95], v[134:137], v[98:101], v[80:95]
	v_add_f32_e32 v114, v42, v114
	v_add_f32_e32 v114, v43, v114
	v_add_f32_e32 v114, v44, v114
	v_add_f32_e32 v134, v45, v114
	v_cvt_pk_bf16_f32 v114, v40, v41
	v_cvt_pk_bf16_f32 v115, v42, v43
	ds_read_b64_tr_b16 v[40:41], v168 offset:31744
	ds_read_b64_tr_b16 v[42:43], v168 offset:32256
	v_mfma_f32_32x32x16_bf16 v[64:79], v[130:133], v[98:101], v[64:79]
	v_add_f32_e32 v116, v46, v134
	v_add_f32_e32 v116, v47, v116
	v_add_f32_e32 v130, 0, v116
	v_cvt_pk_bf16_f32 v116, v44, v45
	v_cvt_pk_bf16_f32 v117, v46, v47
	v_max_f32_e32 v44, v81, v81
	v_max_f32_e32 v45, v80, v80
	v_max_f32_e32 v44, v45, v44
	s_nop 3
	v_max3_f32 v45, v82, v83, v65
	v_max3_f32 v44, v44, v64, v66
	v_max3_f32 v44, v44, v67, v84
	v_max3_f32 v45, v45, v86, v87
	v_max3_f32 v44, v44, v85, v68
	v_max3_f32 v45, v45, v70, v71
	v_max3_f32 v44, v44, v69, v88
	v_max3_f32 v45, v45, v90, v91
	v_max3_f32 v44, v44, v89, v72
	v_max3_f32 v45, v45, v74, v75
	v_max3_f32 v44, v44, v73, v92
	v_max3_f32 v45, v45, v94, v95
	v_max3_f32 v44, v44, v93, v76
	v_max3_f32 v45, v45, v78, v79
	v_max3_f32 v44, v44, v77, v45
	v_mov_b32_e32 v45, v44
	s_add_i32 s24, s29, s53
	s_nop 0
	v_permlane32_swap_b32_e32 v44, v45
	s_mov_b32 m0, s24
	s_nop 0
	global_load_lds_dwordx4 v247, s[22:23]
	s_add_i32 s24, s55, s54
	v_max_f32_e32 v45, v45, v45
	v_max_f32_e32 v44, v44, v44
	s_mov_b32 m0, s24
	s_nop 0
	global_load_lds_dwordx4 v248, s[2:3]
	v_max_f32_e32 v44, v44, v45
	s_mov_b32 s24, 0x41000000
	v_cmp_lt_f32_e32 vcc, s24, v44
	s_cmp_lg_u64 vcc, 0
	v_add_f32_e32 v250, v167, v130
	s_cselect_b64 s[24:25], -1, 0
	s_cbranch_vccnz .LBB0_844

.LBB0_873:
	v_add_u32_e32 v166, s29, v212
	ds_read_b64_tr_b16 v[162:163], v166 offset:24576
	ds_read_b64_tr_b16 v[164:165], v166 offset:25088
	s_waitcnt lgkmcnt(9)
	v_mfma_f32_32x32x16_bf16 v[48:63], v[158:161], v[110:113], v[48:63]
	v_add_f32_e32 v114, v80, v81
	v_add_f32_e32 v114, v82, v114
	v_add_f32_e32 v114, v83, v114
	v_add_f32_e32 v114, v84, v114
	v_add_f32_e32 v114, v85, v114
	v_cvt_pk_bf16_f32 v126, v80, v81
	v_cvt_pk_bf16_f32 v127, v82, v83
	ds_read_b64_tr_b16 v[80:81], v166 offset:28672
	ds_read_b64_tr_b16 v[82:83], v166 offset:29184
	s_waitcnt lgkmcnt(10)
	v_mfma_f32_32x32x16_bf16 v[32:47], v[154:157], v[110:113], v[32:47]
	v_add_f32_e32 v114, v86, v114
	v_add_f32_e32 v114, v87, v114
	v_add_f32_e32 v114, v88, v114
	v_add_f32_e32 v114, v89, v114
	v_cvt_pk_bf16_f32 v128, v84, v85
	v_cvt_pk_bf16_f32 v129, v86, v87
	ds_read_b64_tr_b16 v[84:85], v166 offset:25600
	ds_read_b64_tr_b16 v[86:87], v166 offset:26112
	s_waitcnt lgkmcnt(11)
	v_mfma_f32_32x32x16_bf16 v[48:63], v[150:153], v[106:109], v[48:63]
	v_add_f32_e32 v114, v90, v114
	v_add_f32_e32 v114, v91, v114
	v_add_f32_e32 v114, v92, v114
	v_add_f32_e32 v114, v93, v114
	v_cvt_pk_bf16_f32 v122, v88, v89
	v_cvt_pk_bf16_f32 v123, v90, v91
	ds_read_b64_tr_b16 v[88:89], v166 offset:29696
	ds_read_b64_tr_b16 v[90:91], v166 offset:30208
	s_waitcnt lgkmcnt(12)
	v_mfma_f32_32x32x16_bf16 v[32:47], v[146:149], v[106:109], v[32:47]
	v_add_f32_e32 v114, v94, v114
	v_add_f32_e32 v114, v95, v114
	v_add_f32_e32 v114, v64, v114
	v_add_f32_e32 v114, v65, v114
	v_cvt_pk_bf16_f32 v124, v92, v93
	v_cvt_pk_bf16_f32 v125, v94, v95
	ds_read_b64_tr_b16 v[92:93], v166 offset:26624
	ds_read_b64_tr_b16 v[94:95], v166 offset:27136
	s_waitcnt lgkmcnt(13)
	v_mfma_f32_32x32x16_bf16 v[48:63], v[142:145], v[102:105], v[48:63]
	v_add_f32_e32 v114, v66, v114
	v_add_f32_e32 v114, v67, v114
	v_add_f32_e32 v114, v68, v114
	v_add_f32_e32 v114, v69, v114
	v_cvt_pk_bf16_f32 v118, v64, v65
	v_cvt_pk_bf16_f32 v119, v66, v67
	ds_read_b64_tr_b16 v[64:65], v166 offset:30720
	ds_read_b64_tr_b16 v[66:67], v166 offset:31232
	s_waitcnt lgkmcnt(14)
	v_mfma_f32_32x32x16_bf16 v[32:47], v[138:141], v[102:105], v[32:47]
	v_add_f32_e32 v114, v70, v114
	v_add_f32_e32 v114, v71, v114
	v_add_f32_e32 v114, v72, v114
	v_add_f32_e32 v114, v73, v114
	v_cvt_pk_bf16_f32 v120, v68, v69
	v_cvt_pk_bf16_f32 v121, v70, v71
	ds_read_b64_tr_b16 v[68:69], v166 offset:27648
	ds_read_b64_tr_b16 v[70:71], v166 offset:28160
	s_waitcnt lgkmcnt(14)
	v_mfma_f32_32x32x16_bf16 v[48:63], v[134:137], v[98:101], v[48:63]
	v_add_f32_e32 v114, v74, v114
	v_add_f32_e32 v114, v75, v114
	v_add_f32_e32 v114, v76, v114
	v_add_f32_e32 v134, v77, v114
	v_cvt_pk_bf16_f32 v114, v72, v73
	v_cvt_pk_bf16_f32 v115, v74, v75
	ds_read_b64_tr_b16 v[72:73], v166 offset:31744
	ds_read_b64_tr_b16 v[74:75], v166 offset:32256
	v_mfma_f32_32x32x16_bf16 v[32:47], v[130:133], v[98:101], v[32:47]
	v_add_f32_e32 v116, v78, v134
	v_add_f32_e32 v116, v79, v116
	v_add_f32_e32 v130, 0, v116
	v_cvt_pk_bf16_f32 v116, v76, v77
	v_cvt_pk_bf16_f32 v117, v78, v79
	s_add_i32 s86, s2, 1
	s_cmp_ge_i32 s86, s52
	s_cselect_b64 s[22:23], -1, 0
	s_and_b64 vcc, exec, s[22:23]
	s_cbranch_vccnz .LBB0_875
	s_add_i32 s3, s55, s53
	s_lshl_b64 s[24:25], s[86:87], 15
	s_add_u32 s24, s18, s24
	s_addc_u32 s25, s19, s25
	s_mov_b32 m0, s3
	s_nop 0
	global_load_lds_dwordx4 v247, s[24:25]
.LBB0_875:
	s_add_i32 s86, s2, -1
	s_lshl_b64 s[24:25], s[86:87], 15
	s_add_u32 s24, s20, s24
	s_addc_u32 s25, s21, s25
	s_add_i32 s3, s56, s54
	s_add_i32 s58, s57, s2
	s_mov_b32 m0, s3
	s_nop 0
	global_load_lds_dwordx4 v248, s[24:25]
	s_add_i32 s3, s58, 2
	s_cmp_gt_i32 s3, -1
	s_cselect_b64 s[24:25], -1, 0
	s_and_b64 s[24:25], s[16:17], s[24:25]
	s_andn2_b64 vcc, exec, s[24:25]
	s_cbranch_vccnz .LBB0_877
	v_add_u32_e32 v77, 0xffffffa5, v251
	v_add_u32_e32 v76, 0xffffff85, v251
	v_cmp_le_i32_e32 vcc, v77, v246
	s_nop 1
	v_cndmask_b32_e32 v32, v242, v32, vcc
	v_cmp_lt_i32_e32 vcc, v76, v246
	s_nop 1
	v_cndmask_b32_e32 v49, v242, v49, vcc
	v_cmp_le_i32_e32 vcc, v76, v246
	v_add_u32_e32 v76, 0xffffffa6, v251
	s_nop 0
	v_cndmask_b32_e32 v48, v242, v48, vcc
	v_cmp_le_i32_e32 vcc, v76, v246
	v_add_u32_e32 v76, 0xffffff87, v251
	s_nop 0
	v_cndmask_b32_e32 v33, v242, v33, vcc
	v_cmp_le_i32_e32 vcc, v76, v246
	v_add_u32_e32 v76, 0xffffffa7, v251
	s_nop 0
	v_cndmask_b32_e32 v50, v242, v50, vcc
	v_cmp_le_i32_e32 vcc, v76, v246
	v_add_u32_e32 v76, 0xffffff88, v251
	s_nop 0
	v_cndmask_b32_e32 v34, v242, v34, vcc
	v_cmp_le_i32_e32 vcc, v76, v246
	v_add_u32_e32 v76, 0xffffffa8, v251
	s_nop 0
	v_cndmask_b32_e32 v51, v242, v51, vcc
	v_cmp_le_i32_e32 vcc, v76, v246
	v_add_u32_e32 v76, 0xffffff8d, v251
	s_nop 0
	v_cndmask_b32_e32 v35, v242, v35, vcc
	v_cmp_le_i32_e32 vcc, v76, v246
	v_add_u32_e32 v76, 0xffffffad, v251
	s_nop 0
	v_cndmask_b32_e32 v52, v242, v52, vcc
	v_cmp_le_i32_e32 vcc, v76, v246
	v_add_u32_e32 v76, 0xffffff8e, v251
	s_nop 0
	v_cndmask_b32_e32 v36, v242, v36, vcc
	v_cmp_le_i32_e32 vcc, v76, v246
	v_add_u32_e32 v76, 0xffffffae, v251
	s_nop 0
	v_cndmask_b32_e32 v53, v242, v53, vcc
	v_cmp_le_i32_e32 vcc, v76, v246
	v_add_u32_e32 v76, 0xffffff8f, v251
	s_nop 0
	v_cndmask_b32_e32 v37, v242, v37, vcc
	v_cmp_le_i32_e32 vcc, v76, v246
	v_add_u32_e32 v76, 0xffffffaf, v251
	s_nop 0
	v_cndmask_b32_e32 v54, v242, v54, vcc
	v_cmp_le_i32_e32 vcc, v76, v246
	v_add_u32_e32 v76, 0xffffff90, v251
	s_nop 0
	v_cndmask_b32_e32 v38, v242, v38, vcc
	v_cmp_le_i32_e32 vcc, v76, v246
	v_add_u32_e32 v76, 0xffffffb0, v251
	s_nop 0
	v_cndmask_b32_e32 v55, v242, v55, vcc
	v_cmp_le_i32_e32 vcc, v76, v246
	v_add_u32_e32 v76, 0xffffff95, v251
	s_nop 0
	v_cndmask_b32_e32 v39, v242, v39, vcc
	v_cmp_le_i32_e32 vcc, v76, v246
	v_add_u32_e32 v76, 0xffffffb5, v251
	s_nop 0
	v_cndmask_b32_e32 v56, v242, v56, vcc
	v_cmp_le_i32_e32 vcc, v76, v246
	v_add_u32_e32 v76, 0xffffff96, v251
	s_nop 0
	v_cndmask_b32_e32 v40, v242, v40, vcc
	v_cmp_le_i32_e32 vcc, v76, v246
	v_add_u32_e32 v76, 0xffffffb6, v251
	s_nop 0
	v_cndmask_b32_e32 v57, v242, v57, vcc
	v_cmp_le_i32_e32 vcc, v76, v246
	v_add_u32_e32 v76, 0xffffff97, v251
	s_nop 0
	v_cndmask_b32_e32 v41, v242, v41, vcc
	v_cmp_le_i32_e32 vcc, v76, v246
	v_add_u32_e32 v76, 0xffffffb7, v251
	s_nop 0
	v_cndmask_b32_e32 v58, v242, v58, vcc
	v_cmp_le_i32_e32 vcc, v76, v246
	v_add_u32_e32 v76, 0xffffff98, v251
	s_nop 0
	v_cndmask_b32_e32 v42, v242, v42, vcc
	v_cmp_le_i32_e32 vcc, v76, v246
	v_add_u32_e32 v76, 0xffffffb8, v251
	s_nop 0
	v_cndmask_b32_e32 v59, v242, v59, vcc
	v_cmp_le_i32_e32 vcc, v76, v246
	v_add_u32_e32 v76, 0xffffff9d, v251
	s_nop 0
	v_cndmask_b32_e32 v43, v242, v43, vcc
	v_cmp_le_i32_e32 vcc, v76, v246
	v_add_u32_e32 v76, 0xffffffbd, v251
	s_nop 0
	v_cndmask_b32_e32 v60, v242, v60, vcc
	v_cmp_le_i32_e32 vcc, v76, v246
	v_add_u32_e32 v76, 0xffffff9e, v251
	s_nop 0
	v_cndmask_b32_e32 v44, v242, v44, vcc
	v_cmp_le_i32_e32 vcc, v76, v246
	v_add_u32_e32 v76, 0xffffffbe, v251
	s_nop 0
	v_cndmask_b32_e32 v61, v242, v61, vcc
	v_cmp_le_i32_e32 vcc, v76, v246
	v_add_u32_e32 v76, 0xffffff9f, v251
	s_nop 0
	v_cndmask_b32_e32 v45, v242, v45, vcc
	v_cmp_le_i32_e32 vcc, v76, v246
	v_add_u32_e32 v76, 0xffffffbf, v251
	s_nop 0
	v_cndmask_b32_e32 v62, v242, v62, vcc
	v_cmp_le_i32_e32 vcc, v76, v246
	v_add_u32_e32 v76, 0xffffffa0, v251
	s_nop 0
	v_cndmask_b32_e32 v46, v242, v46, vcc
	v_cmp_le_i32_e32 vcc, v76, v246
	v_subrev_u32_e32 v76, 64, v251
	s_nop 0
	v_cndmask_b32_e32 v63, v242, v63, vcc
	v_cmp_le_i32_e32 vcc, v76, v246
	s_nop 1
	v_cndmask_b32_e32 v47, v242, v47, vcc

.LBB0_886:
	v_add_u32_e32 v164, s55, v212
	ds_read_b64_tr_b16 v[190:191], v164 offset:24576
	ds_read_b64_tr_b16 v[192:193], v164 offset:25088
	s_waitcnt lgkmcnt(9)
	v_mfma_f32_32x32x16_bf16 v[80:95], v[158:161], v[110:113], v[80:95]
	v_add_f32_e32 v114, v48, v49
	v_add_f32_e32 v114, v50, v114
	v_add_f32_e32 v114, v51, v114
	v_add_f32_e32 v114, v52, v114
	v_add_f32_e32 v114, v53, v114
	v_cvt_pk_bf16_f32 v126, v48, v49
	v_cvt_pk_bf16_f32 v127, v50, v51
	ds_read_b64_tr_b16 v[186:187], v164 offset:28672
	ds_read_b64_tr_b16 v[188:189], v164 offset:29184
	s_waitcnt lgkmcnt(10)
	v_mfma_f32_32x32x16_bf16 v[64:79], v[154:157], v[110:113], v[64:79]
	v_add_f32_e32 v114, v54, v114
	v_add_f32_e32 v114, v55, v114
	v_add_f32_e32 v114, v56, v114
	v_add_f32_e32 v114, v57, v114
	v_cvt_pk_bf16_f32 v128, v52, v53
	v_cvt_pk_bf16_f32 v129, v54, v55
	ds_read_b64_tr_b16 v[182:183], v164 offset:25600
	ds_read_b64_tr_b16 v[184:185], v164 offset:26112
	s_waitcnt lgkmcnt(11)
	v_mfma_f32_32x32x16_bf16 v[80:95], v[150:153], v[106:109], v[80:95]
	v_add_f32_e32 v114, v58, v114
	v_add_f32_e32 v114, v59, v114
	v_add_f32_e32 v114, v60, v114
	v_add_f32_e32 v114, v61, v114
	v_cvt_pk_bf16_f32 v122, v56, v57
	v_cvt_pk_bf16_f32 v123, v58, v59
	ds_read_b64_tr_b16 v[178:179], v164 offset:29696
	ds_read_b64_tr_b16 v[180:181], v164 offset:30208
	s_waitcnt lgkmcnt(12)
	v_mfma_f32_32x32x16_bf16 v[64:79], v[146:149], v[106:109], v[64:79]
	v_add_f32_e32 v114, v62, v114
	v_add_f32_e32 v114, v63, v114
	v_add_f32_e32 v114, v32, v114
	v_add_f32_e32 v114, v33, v114
	v_cvt_pk_bf16_f32 v124, v60, v61
	v_cvt_pk_bf16_f32 v125, v62, v63
	ds_read_b64_tr_b16 v[174:175], v164 offset:26624
	ds_read_b64_tr_b16 v[176:177], v164 offset:27136
	s_waitcnt lgkmcnt(13)
	v_mfma_f32_32x32x16_bf16 v[80:95], v[142:145], v[102:105], v[80:95]
	v_add_f32_e32 v114, v34, v114
	v_add_f32_e32 v114, v35, v114
	v_add_f32_e32 v114, v36, v114
	v_add_f32_e32 v114, v37, v114
	v_cvt_pk_bf16_f32 v118, v32, v33
	v_cvt_pk_bf16_f32 v119, v34, v35
	ds_read_b64_tr_b16 v[170:171], v164 offset:30720
	ds_read_b64_tr_b16 v[172:173], v164 offset:31232
	s_waitcnt lgkmcnt(14)
	v_mfma_f32_32x32x16_bf16 v[64:79], v[138:141], v[102:105], v[64:79]
	v_add_f32_e32 v114, v38, v114
	v_add_f32_e32 v114, v39, v114
	v_add_f32_e32 v114, v40, v114
	v_add_f32_e32 v114, v41, v114
	v_cvt_pk_bf16_f32 v120, v36, v37
	v_cvt_pk_bf16_f32 v121, v38, v39
	ds_read_b64_tr_b16 v[166:167], v164 offset:27648
	ds_read_b64_tr_b16 v[168:169], v164 offset:28160
	s_waitcnt lgkmcnt(14)
	v_mfma_f32_32x32x16_bf16 v[80:95], v[134:137], v[98:101], v[80:95]
	v_add_f32_e32 v114, v42, v114
	v_add_f32_e32 v114, v43, v114
	v_add_f32_e32 v114, v44, v114
	v_add_f32_e32 v194, v45, v114
	v_cvt_pk_bf16_f32 v114, v40, v41
	v_cvt_pk_bf16_f32 v115, v42, v43
	ds_read_b64_tr_b16 v[162:163], v164 offset:31744
	ds_read_b64_tr_b16 v[164:165], v164 offset:32256
	v_mfma_f32_32x32x16_bf16 v[64:79], v[130:133], v[98:101], v[64:79]
	v_add_f32_e32 v116, v46, v194
	v_add_f32_e32 v116, v47, v116
	v_add_f32_e32 v228, 0, v116
	v_cvt_pk_bf16_f32 v116, v44, v45
	v_cvt_pk_bf16_f32 v117, v46, v47
	s_add_i32 s86, s2, 2
	s_cmp_ge_i32 s86, s52
	s_cselect_b64 s[24:25], -1, 0
	s_and_b64 vcc, exec, s[24:25]
	s_cbranch_vccnz .LBB0_888
	s_add_i32 s3, s56, s53
	s_lshl_b64 s[26:27], s[86:87], 15
	s_add_u32 s26, s18, s26
	s_addc_u32 s27, s19, s27
	s_mov_b32 m0, s3
	s_nop 0
	global_load_lds_dwordx4 v247, s[26:27]
.LBB0_888:
	s_add_i32 s3, s56, 0x2000
	s_cmpk_lg_i32 s56, 0x4000
	s_cselect_b32 s55, s3, 0
	s_cmp_lt_i32 s2, s52
	s_cselect_b64 s[28:29], -1, 0
	s_cmp_ge_i32 s2, s52
	s_cbranch_scc1 .LBB0_890
	s_mov_b32 s3, s87
	s_add_i32 s26, s55, s54
	s_lshl_b64 s[2:3], s[2:3], 15
	s_add_u32 s2, s20, s2
	s_addc_u32 s3, s21, s3
	s_mov_b32 m0, s26
	s_nop 0
	global_load_lds_dwordx4 v248, s[2:3]

.LBB0_1137:
	s_andn2_b64 vcc, exec, s[2:3]
	v_readlane_b32 s2, v252, 58
	v_readlane_b32 s3, v252, 59
	s_nop 1
	v_cndmask_b32_e64 v0, 0, 1, s[2:3]
	v_cmp_ne_u32_e64 s[36:37], 1, v0
	s_cbranch_vccnz .LBB0_1219
	v_readlane_b32 s4, v252, 0
	v_readlane_b32 s5, v252, 1
	s_waitcnt vmcnt(0) expcnt(0) lgkmcnt(0)
	v_mbcnt_lo_u32_b32 v0, -1, 0
	v_mbcnt_hi_u32_b32 v0, -1, v0
	s_movk_i32 s2, 0x300
	v_add_u32_e32 v0, s93, v0
	s_and_b64 vcc, exec, s[36:37]
	s_nop 0
	v_readfirstlane_b32 s18, v0
	s_cbranch_vccnz .LBB0_1167
	v_bfe_i32 v3, v0, 27, 1
	v_lshlrev_b32_e32 v1, 4, v0
	v_lshrrev_b32_e32 v3, 22, v3
	v_add_u32_e32 v3, v1, v3
	v_and_b32_e32 v3, 0xfffffc00, v3
	v_sub_u32_e32 v3, v1, v3
	v_lshrrev_b32_e32 v4, 4, v3
	s_load_dwordx2 s[4:5], s[4:5], 0x98
	v_ashrrev_i32_e32 v2, 31, v0
	v_bitop3_b32 v3, v4, v3, 32 bitop3:0x6c
	v_lshrrev_b32_e32 v2, 26, v2
	v_ashrrev_i32_e32 v5, 31, v3
	v_add_u32_e32 v2, v0, v2
	v_lshrrev_b32_e32 v5, 26, v5
	s_mul_i32 s86, s44, 0xc0000
	v_ashrrev_i32_e32 v2, 6, v2
	v_add_u32_e32 v5, v3, v5
	s_lshl_b64 s[6:7], s[86:87], 1
	v_lshlrev_b32_e32 v4, 3, v2
	v_ashrrev_i32_e32 v6, 6, v5
	v_and_b32_e32 v5, 0xc0, v5
	s_waitcnt lgkmcnt(0)
	s_add_u32 s3, s4, s6
	v_and_b32_e32 v4, -16, v4
	v_lshlrev_b32_e32 v2, 5, v2
	v_sub_u32_e32 v3, v3, v5
	s_addc_u32 s6, s5, s7
	v_add_u32_e32 v4, v6, v4
	v_and_b32_e32 v2, 32, v2
	v_ashrrev_i16_sdwa v3, v239, sext(v3) dst_sel:DWORD dst_unused:UNUSED_PAD src0_sel:DWORD src1_sel:BYTE_0
	s_add_u32 s30, s3, 0x2d00000
	v_add_u32_sdwa v2, v2, sext(v3) dst_sel:DWORD dst_unused:UNUSED_PAD src0_sel:DWORD src1_sel:WORD_0
	v_lshlrev_b32_e32 v3, 1, v4
	v_lshrrev_b32_e32 v5, 2, v4
	v_and_b32_e32 v6, 3, v6
	s_mov_b32 s3, 0x7fffffe0
	v_and_b32_e32 v3, 24, v3
	v_and_b32_e32 v5, 4, v5
	v_and_or_b32 v6, v4, s3, v6
	v_or3_b32 v3, v6, v5, v3
	v_mul_lo_u32 v4, v4, s2
	v_mul_lo_u32 v3, v3, s2
	v_add_u32_e32 v1, 0x2000, v1
	v_add_lshl_u32 v164, v2, v4, 1
	v_add_lshl_u32 v165, v3, v2, 1
	v_ashrrev_i32_e32 v2, 31, v1
	v_lshrrev_b32_e32 v2, 22, v2
	v_add_u32_e32 v2, v1, v2
	v_ashrrev_i32_e32 v2, 10, v2
	v_mul_i32_i24_e32 v3, 0x400, v2
	v_sub_u32_e32 v1, v1, v3
	v_lshrrev_b32_e32 v3, 4, v1
	v_bitop3_b32 v1, v3, v1, 32 bitop3:0x6c
	v_ashrrev_i32_e32 v4, 31, v1
	v_lshrrev_b32_e32 v4, 26, v4
	v_lshlrev_b32_e32 v3, 3, v2
	v_add_u32_e32 v4, v1, v4
	s_addc_u32 s31, s6, 0
	v_and_b32_e32 v3, -16, v3
	v_ashrrev_i32_e32 v5, 6, v4
	s_add_u32 s34, s4, 0x42d00000
	v_add_u32_e32 v3, v5, v3
	v_and_b32_e32 v5, 3, v5
	s_addc_u32 s35, s5, 0
	v_and_or_b32 v5, v3, s3, v5
	s_ashr_i32 s3, s2, 31
	s_lshl_b32 s12, s2, 1
	s_lshl_b64 s[8:9], s[2:3], 1
	s_lshr_b64 s[10:11], s[2:3], 31
	v_readlane_b32 s16, v253, 31
	s_mul_i32 s10, s10, s16
	s_mul_hi_u32 s11, s8, s16
	s_ashr_i32 s13, s12, 31
	v_readlane_b32 s22, v253, 35
	v_and_b32_e32 v4, 0xc0, v4
	v_readlane_b32 s17, v253, 32
	s_add_i32 s15, s11, s10
	s_lshl_b64 s[10:11], s[12:13], 8
	v_readlane_b32 s23, v253, 36
	v_lshlrev_b32_e32 v2, 5, v2
	v_sub_u32_e32 v1, v1, v4
	s_mul_i32 s21, s8, s16
	s_mul_i32 s16, s10, s23
	s_mul_hi_u32 s17, s10, s22
	s_lshr_b64 s[12:13], s[12:13], 24
	s_ashr_i32 s19, s18, 6
	v_and_b32_e32 v2, 32, v2
	v_ashrrev_i16_sdwa v1, v239, sext(v1) dst_sel:DWORD dst_unused:UNUSED_PAD src0_sel:DWORD src1_sel:BYTE_0
	s_add_i32 s16, s17, s16
	s_mul_i32 s12, s12, s22
	v_add_u32_sdwa v1, v2, sext(v1) dst_sel:DWORD dst_unused:UNUSED_PAD src0_sel:DWORD src1_sel:WORD_0
	v_lshlrev_b32_e32 v2, 1, v3
	v_lshrrev_b32_e32 v4, 2, v3
	s_ashr_i32 s20, s18, 8
	s_lshl_b64 s[6:7], s[2:3], 8
	s_lshl_b32 s14, s19, 10
	s_add_i32 s16, s16, s12
	s_mul_i32 s12, s10, s22
	v_and_b32_e32 v2, 24, v2
	v_and_b32_e32 v4, 4, v4
	s_add_u32 s22, s30, s12
	v_or3_b32 v2, v5, v4, v2
	s_addc_u32 s23, s31, s16
	s_add_i32 s38, s14, 0
	v_mul_lo_u32 v2, v2, s2
	s_add_i32 s39, s38, 0x10000
	s_mov_b32 m0, s39
	s_nop 0
	global_load_lds_dwordx4 v165, s[22:23]
	s_add_i32 s40, s38, 0x12000
	v_add_lshl_u32 v167, v2, v1, 1
	s_mov_b32 m0, s40
	s_nop 0
	global_load_lds_dwordx4 v167, s[22:23]
	s_add_u32 s16, s22, s6
	s_addc_u32 s17, s23, s7
	s_add_i32 s41, s38, 0x14000
	s_mov_b32 m0, s41
	s_nop 0
	global_load_lds_dwordx4 v165, s[16:17]
	s_add_i32 s42, s38, 0x16000
	s_mov_b32 m0, s42
	s_nop 0
	global_load_lds_dwordx4 v167, s[16:17]
	s_add_u32 s24, s34, s21
	v_mul_lo_u32 v3, v3, s2
	s_addc_u32 s25, s35, s15
	s_mov_b32 m0, s38
	s_nop 0
	global_load_lds_dwordx4 v164, s[24:25]
	v_add_lshl_u32 v166, v1, v3, 1
	s_add_i32 s43, s38, 0x2000
	s_mov_b32 m0, s43
	s_nop 0
	global_load_lds_dwordx4 v166, s[24:25]
	s_add_u32 s12, s24, s6
	s_addc_u32 s13, s25, s7
	s_add_i32 s44, s38, 0x4000
	s_mov_b32 m0, s44
	s_nop 0
	global_load_lds_dwordx4 v164, s[12:13]
	s_add_i32 s45, s38, 0x6000
	s_mov_b32 m0, s45
	s_nop 0
	global_load_lds_dwordx4 v166, s[12:13]
	s_cmp_eq_u32 s20, 1
	s_cselect_b64 s[12:13], -1, 0
	s_cmp_lg_u32 s20, 1
	s_cbranch_scc1 .LBB0_1141
	s_barrier
.LBB0_1141:
	s_add_u32 s46, s4, 0x3c300000
	s_addc_u32 s47, s5, 0
	s_add_u32 s14, s4, 0x48500000
	s_addc_u32 s15, s5, 0
	v_bfe_u32 v168, v0, 4, 2
	s_lshr_b32 s3, s3, 26
	v_and_b32_e32 v169, 15, v0
	s_add_i32 s3, s2, s3
	v_lshlrev_b32_e32 v1, 4, v168
	v_lshlrev_b32_e32 v0, 2, v0
	s_and_b32 s19, s19, 3
	s_ashr_i32 s48, s3, 6
	v_lshl_or_b32 v1, v169, 6, v1
	s_lshl_b32 s3, s20, 13
	v_and_b32_e32 v0, 32, v0
	s_lshl_b32 s49, s20, 6
	v_bitop3_b32 v2, v1, s3, v0 bitop3:0xde
	s_lshl_b32 s50, s19, 5
	s_lshl_b32 s3, s19, 12
	s_add_u32 s4, s22, 0x80
	v_bitop3_b32 v0, v1, s3, v0 bitop3:0xde
	s_waitcnt vmcnt(2)
	s_barrier
	s_addc_u32 s5, s23, 0
	s_add_i32 s51, s38, 0x18000
	s_mov_b32 m0, s51
	s_nop 0
	global_load_lds_dwordx4 v165, s[4:5]
	s_add_i32 s52, s38, 0x1a000
	s_mov_b32 m0, s52
	s_nop 0
	global_load_lds_dwordx4 v167, s[4:5]
	s_add_u32 s4, s24, 0x80
	s_addc_u32 s5, s25, 0
	s_add_i32 s53, s38, 0x8000
	s_mov_b32 m0, s53
	s_nop 0
	global_load_lds_dwordx4 v164, s[4:5]
	s_add_i32 s54, s38, 0xa000
	s_mov_b32 m0, s54
	s_nop 0
	global_load_lds_dwordx4 v166, s[4:5]
	s_add_u32 s4, s16, 0x80
	s_addc_u32 s5, s17, 0
	s_add_i32 s55, s38, 0x1c000
	s_mov_b32 m0, s55
	s_nop 0
	global_load_lds_dwordx4 v165, s[4:5]
	s_add_i32 s56, s38, 0x1e000
	s_mov_b32 m0, s56
	s_nop 0
	global_load_lds_dwordx4 v167, s[4:5]
	s_cmp_gt_i32 s2, 63
	s_cselect_b64 s[16:17], -1, 0
	s_and_b32 s2, s18, 0xfffff00
	s_lshl_b32 s3, s19, 6
	s_waitcnt vmcnt(6)
	s_or_b32 s57, s3, s2
	s_add_i32 s58, s48, -2
	s_add_i32 s59, s38, 0xc000
	s_cmpk_lt_u32 s18, 0x100
	s_mov_b32 s60, 0
	s_cselect_b64 s[18:19], -1, 0
	v_add_u32_e32 v170, 0, v0
	v_add_u32_e32 v171, 0, v2
	v_readlane_b32 s63, v253, 20
	v_readlane_b32 s64, v253, 19
	s_barrier
	s_branch .LBB0_1144

.LBB0_1158:
	v_add_u32_e32 v96, 0x10000, v170
	ds_read_b128 v[132:135], v96
	ds_read_b128 v[136:139], v96 offset:1024
	ds_read_b128 v[140:143], v96 offset:2048
	ds_read_b128 v[144:147], v96 offset:3072
	v_add_u32_e32 v96, 0x14000, v170
	ds_read_b128 v[148:151], v96
	ds_read_b128 v[152:155], v96 offset:1024
	ds_read_b128 v[156:159], v96 offset:2048
	ds_read_b128 v[160:163], v96 offset:3072
	s_add_i32 s71, s28, 2
	s_cmp_eq_u32 s58, s28
	s_cselect_b32 s28, s20, s69
	s_cselect_b32 s29, s21, s70
	s_cselect_b32 s26, s4, s67
	s_cselect_b32 s27, s5, s68
	s_add_u32 s24, s28, 0x80
	s_addc_u32 s25, s29, 0
	ds_read_b128 v[172:175], v171
	ds_read_b128 v[176:179], v171 offset:1024
	ds_read_b128 v[180:183], v171 offset:2048
	ds_read_b128 v[184:187], v171 offset:3072
	ds_read_b128 v[188:191], v171 offset:4096
	ds_read_b128 v[192:195], v171 offset:5120
	ds_read_b128 v[196:199], v171 offset:6144
	ds_read_b128 v[200:203], v171 offset:7168
	s_mov_b32 m0, s59
	s_nop 0
	global_load_lds_dwordx4 v164, s[22:23]
	s_add_i32 s72, s38, 0xe000
	s_mov_b32 m0, s72
	s_nop 0
	global_load_lds_dwordx4 v166, s[22:23]
	s_waitcnt vmcnt(8)
	s_waitcnt lgkmcnt(0)
	s_barrier
	s_setprio 1
	s_waitcnt lgkmcnt(7)
	v_mfma_f32_16x16x32_bf16 v[124:127], v[132:135], v[172:175], v[124:127]
	v_mfma_f32_16x16x32_bf16 v[128:131], v[140:143], v[172:175], v[128:131]
	s_waitcnt lgkmcnt(5)
	v_mfma_f32_16x16x32_bf16 v[112:115], v[132:135], v[180:183], v[112:115]
	v_mfma_f32_16x16x32_bf16 v[108:111], v[140:143], v[180:183], v[108:111]
	s_waitcnt lgkmcnt(3)
	v_mfma_f32_16x16x32_bf16 v[92:95], v[132:135], v[188:191], v[92:95]
	v_mfma_f32_16x16x32_bf16 v[88:91], v[140:143], v[188:191], v[88:91]
	s_waitcnt lgkmcnt(1)
	v_mfma_f32_16x16x32_bf16 v[76:79], v[132:135], v[196:199], v[76:79]
	v_mfma_f32_16x16x32_bf16 v[72:75], v[140:143], v[196:199], v[72:75]
	v_mfma_f32_16x16x32_bf16 v[124:127], v[136:139], v[176:179], v[124:127]
	v_mfma_f32_16x16x32_bf16 v[128:131], v[144:147], v[176:179], v[128:131]
	v_mfma_f32_16x16x32_bf16 v[112:115], v[136:139], v[184:187], v[112:115]
	v_mfma_f32_16x16x32_bf16 v[108:111], v[144:147], v[184:187], v[108:111]
	v_mfma_f32_16x16x32_bf16 v[92:95], v[136:139], v[192:195], v[92:95]
	v_mfma_f32_16x16x32_bf16 v[88:91], v[144:147], v[192:195], v[88:91]
	s_waitcnt lgkmcnt(0)
	v_mfma_f32_16x16x32_bf16 v[76:79], v[136:139], v[200:203], v[76:79]
	v_mfma_f32_16x16x32_bf16 v[72:75], v[144:147], v[200:203], v[72:75]
	s_setprio 0
	s_setprio 1
	v_mfma_f32_16x16x32_bf16 v[120:123], v[148:151], v[172:175], v[120:123]
	v_mfma_f32_16x16x32_bf16 v[116:119], v[156:159], v[172:175], v[116:119]
	v_mfma_f32_16x16x32_bf16 v[104:107], v[148:151], v[180:183], v[104:107]
	v_mfma_f32_16x16x32_bf16 v[98:101], v[156:159], v[180:183], v[100:103]
	v_mfma_f32_16x16x32_bf16 v[84:87], v[148:151], v[188:191], v[84:87]
	v_mfma_f32_16x16x32_bf16 v[80:83], v[156:159], v[188:191], v[80:83]
	v_mfma_f32_16x16x32_bf16 v[68:71], v[148:151], v[196:199], v[68:71]
	v_mfma_f32_16x16x32_bf16 v[64:67], v[156:159], v[196:199], v[64:67]
	v_mfma_f32_16x16x32_bf16 v[120:123], v[152:155], v[176:179], v[120:123]
	v_mfma_f32_16x16x32_bf16 v[116:119], v[160:163], v[176:179], v[116:119]
	v_mfma_f32_16x16x32_bf16 v[104:107], v[152:155], v[184:187], v[104:107]
	v_mfma_f32_16x16x32_bf16 v[98:101], v[160:163], v[184:187], v[98:101]
	v_mfma_f32_16x16x32_bf16 v[84:87], v[152:155], v[192:195], v[84:87]
	v_mfma_f32_16x16x32_bf16 v[80:83], v[160:163], v[192:195], v[80:83]
	v_mfma_f32_16x16x32_bf16 v[68:71], v[152:155], v[200:203], v[68:71]
	v_mfma_f32_16x16x32_bf16 v[64:67], v[160:163], v[200:203], v[64:67]
	s_setprio 0
	s_barrier
	ds_read_b128 v[172:175], v171 offset:16384
	ds_read_b128 v[176:179], v171 offset:17408
	ds_read_b128 v[180:183], v171 offset:18432
	ds_read_b128 v[184:187], v171 offset:19456
	ds_read_b128 v[188:191], v171 offset:20480
	ds_read_b128 v[192:195], v171 offset:21504
	ds_read_b128 v[196:199], v171 offset:22528
	ds_read_b128 v[200:203], v171 offset:23552
	s_mov_b32 m0, s39
	s_nop 0
	global_load_lds_dwordx4 v165, s[26:27]
	s_nop 0
	s_mov_b32 m0, s40
	s_nop 0
	global_load_lds_dwordx4 v167, s[26:27]
	s_add_u32 s72, s26, s6
	s_addc_u32 s73, s27, s7
	s_mov_b32 m0, s41
	s_nop 0
	global_load_lds_dwordx4 v165, s[72:73]
	s_nop 0
	s_mov_b32 m0, s42
	s_nop 0
	global_load_lds_dwordx4 v167, s[72:73]
	s_mov_b32 m0, s38
	s_nop 0
	global_load_lds_dwordx4 v164, s[28:29]
	s_nop 0
	s_mov_b32 m0, s43
	s_nop 0
	global_load_lds_dwordx4 v166, s[28:29]
	s_waitcnt vmcnt(8)
	s_waitcnt lgkmcnt(0)
	s_barrier
	s_setprio 1
	s_waitcnt lgkmcnt(7)
	v_mfma_f32_16x16x32_bf16 v[60:63], v[132:135], v[172:175], v[60:63]
	v_mfma_f32_16x16x32_bf16 v[56:59], v[140:143], v[172:175], v[56:59]
	s_waitcnt lgkmcnt(5)
	v_mfma_f32_16x16x32_bf16 v[44:47], v[132:135], v[180:183], v[44:47]
	v_mfma_f32_16x16x32_bf16 v[40:43], v[140:143], v[180:183], v[40:43]
	s_waitcnt lgkmcnt(3)
	v_mfma_f32_16x16x32_bf16 v[28:31], v[132:135], v[188:191], v[28:31]
	v_mfma_f32_16x16x32_bf16 v[24:27], v[140:143], v[188:191], v[24:27]
	s_waitcnt lgkmcnt(1)
	v_mfma_f32_16x16x32_bf16 v[12:15], v[132:135], v[196:199], v[12:15]
	v_mfma_f32_16x16x32_bf16 v[8:11], v[140:143], v[196:199], v[8:11]
	v_mfma_f32_16x16x32_bf16 v[60:63], v[136:139], v[176:179], v[60:63]
	v_mfma_f32_16x16x32_bf16 v[56:59], v[144:147], v[176:179], v[56:59]
	v_mfma_f32_16x16x32_bf16 v[44:47], v[136:139], v[184:187], v[44:47]
	v_mfma_f32_16x16x32_bf16 v[40:43], v[144:147], v[184:187], v[40:43]
	v_mfma_f32_16x16x32_bf16 v[28:31], v[136:139], v[192:195], v[28:31]
	v_mfma_f32_16x16x32_bf16 v[24:27], v[144:147], v[192:195], v[24:27]
	s_waitcnt lgkmcnt(0)
	v_mfma_f32_16x16x32_bf16 v[12:15], v[136:139], v[200:203], v[12:15]
	v_mfma_f32_16x16x32_bf16 v[8:11], v[144:147], v[200:203], v[8:11]
	s_setprio 0
	s_setprio 1
	v_mfma_f32_16x16x32_bf16 v[52:55], v[148:151], v[172:175], v[52:55]
	v_mfma_f32_16x16x32_bf16 v[48:51], v[156:159], v[172:175], v[48:51]
	v_mfma_f32_16x16x32_bf16 v[36:39], v[148:151], v[180:183], v[36:39]
	v_mfma_f32_16x16x32_bf16 v[32:35], v[156:159], v[180:183], v[32:35]
	v_mfma_f32_16x16x32_bf16 v[20:23], v[148:151], v[188:191], v[20:23]
	v_mfma_f32_16x16x32_bf16 v[16:19], v[156:159], v[188:191], v[16:19]
	v_mfma_f32_16x16x32_bf16 v[4:7], v[148:151], v[196:199], v[4:7]
	v_mfma_f32_16x16x32_bf16 v[0:3], v[156:159], v[196:199], v[0:3]
	v_mfma_f32_16x16x32_bf16 v[52:55], v[152:155], v[176:179], v[52:55]
	v_mfma_f32_16x16x32_bf16 v[48:51], v[160:163], v[176:179], v[48:51]
	v_mfma_f32_16x16x32_bf16 v[36:39], v[152:155], v[184:187], v[36:39]
	v_mfma_f32_16x16x32_bf16 v[32:35], v[160:163], v[184:187], v[32:35]
	v_mfma_f32_16x16x32_bf16 v[20:23], v[152:155], v[192:195], v[20:23]
	v_mfma_f32_16x16x32_bf16 v[16:19], v[160:163], v[192:195], v[16:19]
	v_mfma_f32_16x16x32_bf16 v[4:7], v[152:155], v[200:203], v[4:7]
	v_mfma_f32_16x16x32_bf16 v[0:3], v[160:163], v[200:203], v[0:3]
	s_setprio 0
	s_barrier
	v_add_u32_e32 v96, 0x18000, v170
	ds_read_b128 v[132:135], v96
	ds_read_b128 v[136:139], v96 offset:1024
	ds_read_b128 v[140:143], v96 offset:2048
	ds_read_b128 v[144:147], v96 offset:3072
	v_add_u32_e32 v96, 0x1c000, v170
	ds_read_b128 v[148:151], v96
	ds_read_b128 v[152:155], v96 offset:1024
	ds_read_b128 v[156:159], v96 offset:2048
	ds_read_b128 v[160:163], v96 offset:3072
	ds_read_b128 v[172:175], v171 offset:32768
	ds_read_b128 v[176:179], v171 offset:33792
	ds_read_b128 v[180:183], v171 offset:34816
	ds_read_b128 v[184:187], v171 offset:35840
	ds_read_b128 v[188:191], v171 offset:36864
	ds_read_b128 v[192:195], v171 offset:37888
	ds_read_b128 v[196:199], v171 offset:38912
	ds_read_b128 v[200:203], v171 offset:39936
	s_add_u32 s28, s28, s6
	s_addc_u32 s29, s29, s7
	s_mov_b32 m0, s44
	s_nop 0
	global_load_lds_dwordx4 v164, s[28:29]
	s_nop 0
	s_mov_b32 m0, s45
	s_nop 0
	global_load_lds_dwordx4 v166, s[28:29]
	s_waitcnt vmcnt(8)
	s_waitcnt lgkmcnt(0)
	s_barrier
	s_setprio 1
	s_waitcnt lgkmcnt(7)
	v_mfma_f32_16x16x32_bf16 v[124:127], v[132:135], v[172:175], v[124:127]
	v_mfma_f32_16x16x32_bf16 v[128:131], v[140:143], v[172:175], v[128:131]
	s_waitcnt lgkmcnt(5)
	v_mfma_f32_16x16x32_bf16 v[112:115], v[132:135], v[180:183], v[112:115]
	v_mfma_f32_16x16x32_bf16 v[108:111], v[140:143], v[180:183], v[108:111]
	s_waitcnt lgkmcnt(3)
	v_mfma_f32_16x16x32_bf16 v[92:95], v[132:135], v[188:191], v[92:95]
	v_mfma_f32_16x16x32_bf16 v[88:91], v[140:143], v[188:191], v[88:91]
	s_waitcnt lgkmcnt(1)
	v_mfma_f32_16x16x32_bf16 v[76:79], v[132:135], v[196:199], v[76:79]
	v_mfma_f32_16x16x32_bf16 v[72:75], v[140:143], v[196:199], v[72:75]
	v_mfma_f32_16x16x32_bf16 v[124:127], v[136:139], v[176:179], v[124:127]
	v_mfma_f32_16x16x32_bf16 v[128:131], v[144:147], v[176:179], v[128:131]
	v_mfma_f32_16x16x32_bf16 v[112:115], v[136:139], v[184:187], v[112:115]
	v_mfma_f32_16x16x32_bf16 v[108:111], v[144:147], v[184:187], v[108:111]
	v_mfma_f32_16x16x32_bf16 v[92:95], v[136:139], v[192:195], v[92:95]
	v_mfma_f32_16x16x32_bf16 v[88:91], v[144:147], v[192:195], v[88:91]
	s_waitcnt lgkmcnt(0)
	v_mfma_f32_16x16x32_bf16 v[76:79], v[136:139], v[200:203], v[76:79]
	v_mfma_f32_16x16x32_bf16 v[72:75], v[144:147], v[200:203], v[72:75]
	s_setprio 0
	s_setprio 1
	v_mfma_f32_16x16x32_bf16 v[120:123], v[148:151], v[172:175], v[120:123]
	v_mfma_f32_16x16x32_bf16 v[116:119], v[156:159], v[172:175], v[116:119]
	v_mfma_f32_16x16x32_bf16 v[102:105], v[148:151], v[180:183], v[104:107]
	v_mfma_f32_16x16x32_bf16 v[98:101], v[156:159], v[180:183], v[98:101]
	v_mfma_f32_16x16x32_bf16 v[84:87], v[148:151], v[188:191], v[84:87]
	v_mfma_f32_16x16x32_bf16 v[80:83], v[156:159], v[188:191], v[80:83]
	v_mfma_f32_16x16x32_bf16 v[68:71], v[148:151], v[196:199], v[68:71]
	v_mfma_f32_16x16x32_bf16 v[64:67], v[156:159], v[196:199], v[64:67]
	v_mfma_f32_16x16x32_bf16 v[120:123], v[152:155], v[176:179], v[120:123]
	v_mfma_f32_16x16x32_bf16 v[116:119], v[160:163], v[176:179], v[116:119]
	v_mfma_f32_16x16x32_bf16 v[104:107], v[152:155], v[184:187], v[102:105]
	v_mfma_f32_16x16x32_bf16 v[100:103], v[160:163], v[184:187], v[98:101]
	v_mfma_f32_16x16x32_bf16 v[84:87], v[152:155], v[192:195], v[84:87]
	v_mfma_f32_16x16x32_bf16 v[80:83], v[160:163], v[192:195], v[80:83]
	v_mfma_f32_16x16x32_bf16 v[68:71], v[152:155], v[200:203], v[68:71]
	v_mfma_f32_16x16x32_bf16 v[64:67], v[160:163], v[200:203], v[64:67]
	s_setprio 0
	s_barrier
	ds_read_b128 v[172:175], v171 offset:49152
	ds_read_b128 v[176:179], v171 offset:50176
	ds_read_b128 v[180:183], v171 offset:51200
	ds_read_b128 v[184:187], v171 offset:52224
	ds_read_b128 v[188:191], v171 offset:53248
	ds_read_b128 v[192:195], v171 offset:54272
	ds_read_b128 v[196:199], v171 offset:55296
	ds_read_b128 v[200:203], v171 offset:56320
	s_add_u32 s26, s26, 0x80
	s_addc_u32 s27, s27, 0
	s_mov_b32 m0, s51
	s_nop 0
	global_load_lds_dwordx4 v165, s[26:27]
	s_nop 0
	s_mov_b32 m0, s52
	s_nop 0
	global_load_lds_dwordx4 v167, s[26:27]
	s_add_u32 s26, s26, s6
	s_addc_u32 s27, s27, s7
	s_mov_b32 m0, s55
	s_nop 0
	global_load_lds_dwordx4 v165, s[26:27]
	s_nop 0
	s_mov_b32 m0, s56
	s_nop 0
	global_load_lds_dwordx4 v167, s[26:27]
	s_mov_b32 m0, s53
	s_nop 0
	global_load_lds_dwordx4 v164, s[24:25]
	s_nop 0
	s_mov_b32 m0, s54
	s_nop 0
	global_load_lds_dwordx4 v166, s[24:25]
	s_waitcnt vmcnt(8)
	s_waitcnt lgkmcnt(0)
	s_barrier
	s_setprio 1
	s_waitcnt lgkmcnt(7)
	v_mfma_f32_16x16x32_bf16 v[60:63], v[132:135], v[172:175], v[60:63]
	v_mfma_f32_16x16x32_bf16 v[56:59], v[140:143], v[172:175], v[56:59]
	s_waitcnt lgkmcnt(5)
	v_mfma_f32_16x16x32_bf16 v[44:47], v[132:135], v[180:183], v[44:47]
	v_mfma_f32_16x16x32_bf16 v[40:43], v[140:143], v[180:183], v[40:43]
	s_waitcnt lgkmcnt(3)
	v_mfma_f32_16x16x32_bf16 v[28:31], v[132:135], v[188:191], v[28:31]
	v_mfma_f32_16x16x32_bf16 v[24:27], v[140:143], v[188:191], v[24:27]
	s_waitcnt lgkmcnt(1)
	v_mfma_f32_16x16x32_bf16 v[12:15], v[132:135], v[196:199], v[12:15]
	v_mfma_f32_16x16x32_bf16 v[8:11], v[140:143], v[196:199], v[8:11]
	v_mfma_f32_16x16x32_bf16 v[60:63], v[136:139], v[176:179], v[60:63]
	v_mfma_f32_16x16x32_bf16 v[56:59], v[144:147], v[176:179], v[56:59]
	v_mfma_f32_16x16x32_bf16 v[44:47], v[136:139], v[184:187], v[44:47]
	v_mfma_f32_16x16x32_bf16 v[40:43], v[144:147], v[184:187], v[40:43]
	v_mfma_f32_16x16x32_bf16 v[28:31], v[136:139], v[192:195], v[28:31]
	v_mfma_f32_16x16x32_bf16 v[24:27], v[144:147], v[192:195], v[24:27]
	s_waitcnt lgkmcnt(0)
	v_mfma_f32_16x16x32_bf16 v[12:15], v[136:139], v[200:203], v[12:15]
	v_mfma_f32_16x16x32_bf16 v[8:11], v[144:147], v[200:203], v[8:11]
	s_setprio 0
	s_setprio 1
	v_mfma_f32_16x16x32_bf16 v[52:55], v[148:151], v[172:175], v[52:55]
	v_mfma_f32_16x16x32_bf16 v[48:51], v[156:159], v[172:175], v[48:51]
	v_mfma_f32_16x16x32_bf16 v[36:39], v[148:151], v[180:183], v[36:39]
	v_mfma_f32_16x16x32_bf16 v[32:35], v[156:159], v[180:183], v[32:35]
	v_mfma_f32_16x16x32_bf16 v[20:23], v[148:151], v[188:191], v[20:23]
	v_mfma_f32_16x16x32_bf16 v[16:19], v[156:159], v[188:191], v[16:19]
	v_mfma_f32_16x16x32_bf16 v[4:7], v[148:151], v[196:199], v[4:7]
	v_mfma_f32_16x16x32_bf16 v[0:3], v[156:159], v[196:199], v[0:3]
	v_mfma_f32_16x16x32_bf16 v[52:55], v[152:155], v[176:179], v[52:55]
	v_mfma_f32_16x16x32_bf16 v[48:51], v[160:163], v[176:179], v[48:51]
	v_mfma_f32_16x16x32_bf16 v[36:39], v[152:155], v[184:187], v[36:39]
	v_mfma_f32_16x16x32_bf16 v[32:35], v[160:163], v[184:187], v[32:35]
	v_mfma_f32_16x16x32_bf16 v[20:23], v[152:155], v[192:195], v[20:23]
	v_mfma_f32_16x16x32_bf16 v[16:19], v[160:163], v[192:195], v[16:19]
	v_mfma_f32_16x16x32_bf16 v[4:7], v[152:155], v[200:203], v[4:7]
	v_mfma_f32_16x16x32_bf16 v[0:3], v[160:163], v[200:203], v[0:3]
	s_setprio 0
	s_barrier
	s_add_u32 s67, s67, 0x100
	s_addc_u32 s68, s68, 0
	s_add_u32 s69, s69, 0x100
	s_addc_u32 s70, s70, 0
	s_add_u32 s22, s22, 0x100
	s_addc_u32 s23, s23, 0
	s_cmp_ge_i32 s71, s48
	s_cbranch_scc1 .LBB0_1161
	s_mov_b32 s28, s71
	s_cmp_lt_i32 s28, 8
	s_cbranch_scc1 .LBB0_1154

.LBB0_1221:
	s_andn2_b64 vcc, exec, s[2:3]
	s_cbranch_vccnz .LBB0_1337
	v_readlane_b32 s8, v252, 0
	v_readlane_b32 s9, v252, 1
	s_waitcnt vmcnt(0) expcnt(0) lgkmcnt(0)
	v_mbcnt_lo_u32_b32 v0, -1, 0
	v_mbcnt_hi_u32_b32 v0, -1, v0
	s_and_b64 vcc, exec, s[36:37]
	v_add_u32_e32 v0, s93, v0
	s_nop 0
	s_nop 0
	v_readfirstlane_b32 s24, v0
	s_cbranch_vccnz .LBB0_1284
	v_bfe_i32 v3, v0, 27, 1
	v_lshlrev_b32_e32 v1, 4, v0
	v_lshrrev_b32_e32 v3, 22, v3
	v_add_u32_e32 v3, v1, v3
	v_and_b32_e32 v3, 0xfffffc00, v3
	v_sub_u32_e32 v3, v1, v3
	v_ashrrev_i32_e32 v2, 31, v0
	v_lshrrev_b32_e32 v4, 4, v3
	v_lshrrev_b32_e32 v2, 26, v2
	v_bitop3_b32 v3, v4, v3, 32 bitop3:0x6c
	v_add_u32_e32 v2, v0, v2
	v_ashrrev_i32_e32 v5, 31, v3
	v_ashrrev_i32_e32 v2, 6, v2
	v_lshrrev_b32_e32 v5, 26, v5
	v_lshlrev_b32_e32 v4, 3, v2
	v_add_u32_e32 v5, v3, v5
	v_and_b32_e32 v4, -16, v4
	v_ashrrev_i32_e32 v6, 6, v5
	v_and_b32_e32 v5, 0xc0, v5
	v_add_u32_e32 v4, v6, v4
	v_sub_u32_e32 v3, v3, v5
	v_lshlrev_b32_e32 v2, 5, v2
	v_ashrrev_i16_sdwa v3, v239, sext(v3) dst_sel:DWORD dst_unused:UNUSED_PAD src0_sel:DWORD src1_sel:BYTE_0
	v_lshlrev_b32_e32 v5, 1, v4
	v_lshlrev_b32_e32 v7, 2, v4
	v_lshrrev_b32_e32 v8, 2, v4
	v_and_b32_e32 v6, 3, v6
	v_and_b32_e32 v2, 32, v2
	v_bfe_i32 v3, v3, 0, 16
	v_and_b32_e32 v5, 0x1fffc0, v5
	v_and_b32_e32 v8, 4, v8
	v_and_or_b32 v6, v7, 48, v6
	v_or3_b32 v5, v6, v5, v8
	v_add_lshl_u32 v2, v2, v3, 1
	v_add_u32_e32 v1, 0x2000, v1
	v_lshl_add_u32 v96, v4, 11, v2
	v_lshl_add_u32 v244, v5, 11, v2
	v_ashrrev_i32_e32 v2, 31, v1
	s_load_dwordx2 s[2:3], s[8:9], 0x98
	v_lshrrev_b32_e32 v2, 22, v2
	v_add_u32_e32 v2, v1, v2
	v_ashrrev_i32_e32 v2, 10, v2
	v_mul_i32_i24_e32 v3, 0x400, v2
	s_lshl_b32 s4, s44, 21
	v_sub_u32_e32 v1, v1, v3
	s_waitcnt lgkmcnt(0)
	s_add_u32 s4, s2, s4
	v_lshrrev_b32_e32 v3, 4, v1
	s_addc_u32 s5, s3, 0
	v_bitop3_b32 v1, v3, v1, 32 bitop3:0x6c
	s_add_u32 s46, s4, 0x3300000
	v_ashrrev_i32_e32 v4, 31, v1
	s_addc_u32 s47, s5, 0
	v_lshrrev_b32_e32 v4, 26, v4
	s_add_u32 s48, s2, 0x48500000
	v_lshlrev_b32_e32 v3, 3, v2
	v_add_u32_e32 v4, v1, v4
	s_addc_u32 s49, s3, 0
	s_ashr_i32 s25, s24, 6
	v_and_b32_e32 v3, -16, v3
	v_ashrrev_i32_e32 v5, 6, v4
	v_and_b32_e32 v4, 0xc0, v4
	s_load_dwordx4 s[4:7], s[8:9], 0x40
	v_add_u32_e32 v3, v5, v3
	v_sub_u32_e32 v1, v1, v4
	s_ashr_i32 s26, s24, 8
	s_lshl_b32 s50, s25, 10
	v_readlane_b32 s8, v253, 37
	v_lshlrev_b32_e32 v2, 5, v2
	v_ashrrev_i16_sdwa v1, v239, sext(v1) dst_sel:DWORD dst_unused:UNUSED_PAD src0_sel:DWORD src1_sel:BYTE_0
	v_lshlrev_b32_e32 v4, 1, v3
	v_lshlrev_b32_e32 v6, 2, v3
	v_lshrrev_b32_e32 v7, 2, v3
	v_and_b32_e32 v5, 3, v5
	v_readlane_b32 s9, v253, 38
	s_add_u32 s40, s46, s8
	v_and_b32_e32 v2, 32, v2
	v_bfe_i32 v1, v1, 0, 16
	v_and_b32_e32 v4, 0x1fffc0, v4
	v_and_b32_e32 v7, 4, v7
	v_and_or_b32 v5, v6, 48, v5
	s_addc_u32 s41, s47, s9
	s_add_i32 s50, s50, 0
	v_or3_b32 v4, v5, v4, v7
	v_add_lshl_u32 v1, v2, v1, 1
	s_add_i32 s51, s50, 0x10000
	s_mov_b32 m0, s51
	s_nop 0
	global_load_lds_dwordx4 v244, s[40:41]
	v_lshl_add_u32 v246, v4, 11, v1
	s_add_i32 s52, s50, 0x12000
	s_mov_b32 m0, s52
	s_nop 0
	global_load_lds_dwordx4 v246, s[40:41]
	s_add_u32 s8, s40, 0x4000
	s_addc_u32 s9, s41, 0
	s_add_i32 s53, s50, 0x14000
	s_mov_b32 m0, s53
	s_nop 0
	global_load_lds_dwordx4 v244, s[8:9]
	s_add_i32 s54, s50, 0x16000
	s_mov_b32 m0, s54
	s_nop 0
	global_load_lds_dwordx4 v246, s[8:9]
	v_readlane_b32 s8, v253, 33
	v_readlane_b32 s9, v253, 34
	s_add_u32 s38, s48, s8
	s_addc_u32 s39, s49, s9
	s_mov_b32 m0, s50
	s_nop 0
	global_load_lds_dwordx4 v96, s[38:39]
	v_lshl_add_u32 v245, v3, 11, v1
	s_add_i32 s55, s50, 0x2000
	s_mov_b32 m0, s55
	s_nop 0
	global_load_lds_dwordx4 v245, s[38:39]
	s_add_u32 s8, s38, 0x40000
	s_addc_u32 s9, s39, 0
	s_add_i32 s56, s50, 0x4000
	s_mov_b32 m0, s56
	s_nop 0
	global_load_lds_dwordx4 v96, s[8:9]
	s_add_i32 s57, s50, 0x6000
	s_mov_b32 m0, s57
	s_nop 0
	global_load_lds_dwordx4 v245, s[8:9]
	s_cmp_eq_u32 s26, 1
	s_cselect_b64 s[8:9], -1, 0
	s_cmp_lg_u32 s26, 1
	s_cbranch_scc1 .LBB0_1225
	s_barrier
.LBB0_1225:
	s_add_u32 s10, s2, 0x33b00000
	s_addc_u32 s11, s3, 0
	s_add_u32 s12, s2, 0x35b00000
	s_addc_u32 s13, s3, 0
	s_add_u32 s14, s2, 0x69100000
	s_addc_u32 s15, s3, 0
	s_lshl_b32 s86, s44, 10
	s_lshl_b64 s[18:19], s[86:87], 2
	s_waitcnt lgkmcnt(0)
	s_add_u32 s16, s4, s18
	s_addc_u32 s17, s5, s19
	s_add_u32 s18, s6, s18
	s_addc_u32 s19, s7, s19
	s_add_u32 s20, s2, 0x4a500000
	s_addc_u32 s21, s3, 0
	s_lshl_b32 s86, s44, 12
	s_lshl_b64 s[4:5], s[86:87], 2
	s_add_u32 s4, s2, s4
	s_addc_u32 s5, s3, s5
	s_add_u32 s58, s4, 0x40000
	s_addc_u32 s59, s5, 0
	v_bfe_u32 v248, v0, 4, 2
	s_add_u32 s22, s2, 0x3ff00
	v_and_b32_e32 v247, 15, v0
	v_lshlrev_b32_e32 v1, 4, v248
	v_lshlrev_b32_e32 v0, 2, v0
	s_addc_u32 s23, s3, 0
	s_and_b32 s4, s25, 3
	v_lshl_or_b32 v1, v247, 6, v1
	s_lshl_b32 s2, s26, 13
	v_and_b32_e32 v0, 32, v0
	s_lshl_b32 s60, s26, 6
	v_bitop3_b32 v2, v1, s2, v0 bitop3:0xde
	s_lshl_b32 s2, s4, 12
	v_bitop3_b32 v0, v1, s2, v0 bitop3:0xde
	s_add_u32 s2, s40, 0x80
	s_waitcnt vmcnt(2)
	s_barrier
	s_addc_u32 s3, s41, 0
	s_add_i32 s61, s50, 0x18000
	s_mov_b32 m0, s61
	s_nop 0
	global_load_lds_dwordx4 v244, s[2:3]
	s_add_i32 s62, s50, 0x1a000
	s_mov_b32 m0, s62
	s_nop 0
	global_load_lds_dwordx4 v246, s[2:3]
	s_add_u32 s2, s38, 0x80
	s_addc_u32 s3, s39, 0
	s_add_i32 s63, s50, 0x8000
	s_mov_b32 m0, s63
	s_nop 0
	global_load_lds_dwordx4 v96, s[2:3]
	s_add_i32 s64, s50, 0xa000
	s_mov_b32 m0, s64
	s_nop 0
	global_load_lds_dwordx4 v245, s[2:3]
	s_add_u32 s2, s40, 0x4080
	s_addc_u32 s3, s41, 0
	s_add_i32 s65, s50, 0x1c000
	s_add_i32 s66, s50, 0x1e000
	s_add_i32 s67, s50, 0xc000
	s_mov_b32 m0, s65
	s_nop 0
	global_load_lds_dwordx4 v244, s[2:3]
	s_cmpk_lt_u32 s24, 0x100
	s_mov_b32 m0, s66
	s_nop 0
	global_load_lds_dwordx4 v246, s[2:3]
	s_cselect_b64 s[24:25], -1, 0
	s_lshl_b32 s2, s26, 2
	s_or_b32 s2, s2, s4
	s_lshl_b32 s68, s4, 6
	s_lshl_b32 s69, s2, 5
	s_cmp_eq_u32 s2, 0
	s_waitcnt vmcnt(6)
	s_cselect_b64 s[26:27], -1, 0
	s_lshl_b32 s2, s4, 3
	s_add_i32 s71, s2, 0
	v_readlane_b32 s2, v253, 20
	s_mov_b32 s70, 0
	s_add_i32 s71, s71, 0x22000
	v_add_u32_e32 v249, 0, v0
	v_add_u32_e32 v250, 0, v2
	s_mov_b32 s4, s2
	v_readlane_b32 s44, v253, 19
	s_barrier
	s_branch .LBB0_1228

.LBB0_1237:
	v_add_u32_e32 v142, 0x10000, v249
	v_add_u32_e32 v158, 0x14000, v249
	ds_read_b128 v[130:133], v142
	ds_read_b128 v[134:137], v142 offset:1024
	ds_read_b128 v[138:141], v142 offset:2048
	ds_read_b128 v[142:145], v142 offset:3072
	ds_read_b128 v[146:149], v158
	ds_read_b128 v[150:153], v158 offset:1024
	ds_read_b128 v[154:157], v158 offset:2048
	ds_read_b128 v[158:161], v158 offset:3072
	s_add_u32 s2, s38, 0x100
	s_addc_u32 s3, s39, 0
	s_cmp_eq_u32 s45, 12
	s_cselect_b32 s42, s34, s2
	s_cselect_b32 s43, s35, s3
	s_cselect_b32 s40, s30, s5
	s_cselect_b32 s41, s31, s29
	s_add_u32 s6, s42, 0x80
	s_addc_u32 s7, s43, 0
	ds_read_b128 v[162:165], v250
	ds_read_b128 v[166:169], v250 offset:1024
	ds_read_b128 v[170:173], v250 offset:2048
	ds_read_b128 v[174:177], v250 offset:3072
	ds_read_b128 v[178:181], v250 offset:4096
	ds_read_b128 v[182:185], v250 offset:5120
	ds_read_b128 v[186:189], v250 offset:6144
	ds_read_b128 v[190:193], v250 offset:7168
	s_add_u32 s38, s38, 0x40080
	s_addc_u32 s39, s39, 0
	s_mov_b32 m0, s67
	s_nop 0
	global_load_lds_dwordx4 v96, s[38:39]
	s_add_i32 s73, s50, 0xe000
	s_mov_b32 m0, s73
	s_nop 0
	global_load_lds_dwordx4 v245, s[38:39]
	s_waitcnt vmcnt(8)
	s_waitcnt lgkmcnt(0)
	s_barrier
	s_setprio 1
	s_waitcnt lgkmcnt(7)
	v_mfma_f32_16x16x32_bf16 v[126:129], v[130:133], v[162:165], v[126:129]
	v_mfma_f32_16x16x32_bf16 v[122:125], v[138:141], v[162:165], v[122:125]
	s_waitcnt lgkmcnt(5)
	v_mfma_f32_16x16x32_bf16 v[110:113], v[130:133], v[170:173], v[110:113]
	v_mfma_f32_16x16x32_bf16 v[106:109], v[138:141], v[170:173], v[106:109]
	s_waitcnt lgkmcnt(3)
	v_mfma_f32_16x16x32_bf16 v[92:95], v[130:133], v[178:181], v[92:95]
	v_mfma_f32_16x16x32_bf16 v[88:91], v[138:141], v[178:181], v[88:91]
	s_waitcnt lgkmcnt(1)
	v_mfma_f32_16x16x32_bf16 v[76:79], v[130:133], v[186:189], v[76:79]
	v_mfma_f32_16x16x32_bf16 v[72:75], v[138:141], v[186:189], v[72:75]
	v_mfma_f32_16x16x32_bf16 v[126:129], v[134:137], v[166:169], v[126:129]
	v_mfma_f32_16x16x32_bf16 v[122:125], v[142:145], v[166:169], v[122:125]
	v_mfma_f32_16x16x32_bf16 v[110:113], v[134:137], v[174:177], v[110:113]
	v_mfma_f32_16x16x32_bf16 v[106:109], v[142:145], v[174:177], v[106:109]
	v_mfma_f32_16x16x32_bf16 v[92:95], v[134:137], v[182:185], v[92:95]
	v_mfma_f32_16x16x32_bf16 v[88:91], v[142:145], v[182:185], v[88:91]
	s_waitcnt lgkmcnt(0)
	v_mfma_f32_16x16x32_bf16 v[76:79], v[134:137], v[190:193], v[76:79]
	v_mfma_f32_16x16x32_bf16 v[72:75], v[142:145], v[190:193], v[72:75]
	s_setprio 0
	s_setprio 1
	v_mfma_f32_16x16x32_bf16 v[118:121], v[146:149], v[162:165], v[118:121]
	v_mfma_f32_16x16x32_bf16 v[114:117], v[154:157], v[162:165], v[114:117]
	v_mfma_f32_16x16x32_bf16 v[102:105], v[146:149], v[170:173], v[102:105]
	v_mfma_f32_16x16x32_bf16 v[98:101], v[154:157], v[170:173], v[98:101]
	v_mfma_f32_16x16x32_bf16 v[84:87], v[146:149], v[178:181], v[84:87]
	v_mfma_f32_16x16x32_bf16 v[80:83], v[154:157], v[178:181], v[80:83]
	v_mfma_f32_16x16x32_bf16 v[68:71], v[146:149], v[186:189], v[68:71]
	v_mfma_f32_16x16x32_bf16 v[64:67], v[154:157], v[186:189], v[64:67]
	v_mfma_f32_16x16x32_bf16 v[118:121], v[150:153], v[166:169], v[118:121]
	v_mfma_f32_16x16x32_bf16 v[114:117], v[158:161], v[166:169], v[114:117]
	v_mfma_f32_16x16x32_bf16 v[102:105], v[150:153], v[174:177], v[102:105]
	v_mfma_f32_16x16x32_bf16 v[98:101], v[158:161], v[174:177], v[98:101]
	v_mfma_f32_16x16x32_bf16 v[84:87], v[150:153], v[182:185], v[84:87]
	v_mfma_f32_16x16x32_bf16 v[80:83], v[158:161], v[182:185], v[80:83]
	v_mfma_f32_16x16x32_bf16 v[68:71], v[150:153], v[190:193], v[68:71]
	v_mfma_f32_16x16x32_bf16 v[64:67], v[158:161], v[190:193], v[64:67]
	s_setprio 0
	s_barrier
	ds_read_b128 v[162:165], v250 offset:16384
	ds_read_b128 v[166:169], v250 offset:17408
	ds_read_b128 v[170:173], v250 offset:18432
	ds_read_b128 v[174:177], v250 offset:19456
	ds_read_b128 v[178:181], v250 offset:20480
	ds_read_b128 v[182:185], v250 offset:21504
	ds_read_b128 v[186:189], v250 offset:22528
	ds_read_b128 v[190:193], v250 offset:23552
	s_mov_b32 m0, s51
	s_nop 0
	global_load_lds_dwordx4 v244, s[40:41]
	s_nop 0
	s_mov_b32 m0, s52
	s_nop 0
	global_load_lds_dwordx4 v246, s[40:41]
	s_add_u32 s38, s40, 0x4000
	s_addc_u32 s39, s41, 0
	s_mov_b32 m0, s53
	s_nop 0
	global_load_lds_dwordx4 v244, s[38:39]
	s_nop 0
	s_mov_b32 m0, s54
	s_nop 0
	global_load_lds_dwordx4 v246, s[38:39]
	s_mov_b32 m0, s50
	s_nop 0
	global_load_lds_dwordx4 v96, s[42:43]
	s_nop 0
	s_mov_b32 m0, s55
	s_nop 0
	global_load_lds_dwordx4 v245, s[42:43]
	s_waitcnt vmcnt(8)
	s_waitcnt lgkmcnt(0)
	s_barrier
	s_setprio 1
	s_waitcnt lgkmcnt(7)
	v_mfma_f32_16x16x32_bf16 v[60:63], v[130:133], v[162:165], v[60:63]
	v_mfma_f32_16x16x32_bf16 v[56:59], v[138:141], v[162:165], v[56:59]
	s_waitcnt lgkmcnt(5)
	v_mfma_f32_16x16x32_bf16 v[44:47], v[130:133], v[170:173], v[44:47]
	v_mfma_f32_16x16x32_bf16 v[40:43], v[138:141], v[170:173], v[40:43]
	s_waitcnt lgkmcnt(3)
	v_mfma_f32_16x16x32_bf16 v[28:31], v[130:133], v[178:181], v[28:31]
	v_mfma_f32_16x16x32_bf16 v[24:27], v[138:141], v[178:181], v[24:27]
	s_waitcnt lgkmcnt(1)
	v_mfma_f32_16x16x32_bf16 v[12:15], v[130:133], v[186:189], v[12:15]
	v_mfma_f32_16x16x32_bf16 v[8:11], v[138:141], v[186:189], v[8:11]
	v_mfma_f32_16x16x32_bf16 v[60:63], v[134:137], v[166:169], v[60:63]
	v_mfma_f32_16x16x32_bf16 v[56:59], v[142:145], v[166:169], v[56:59]
	v_mfma_f32_16x16x32_bf16 v[44:47], v[134:137], v[174:177], v[44:47]
	v_mfma_f32_16x16x32_bf16 v[40:43], v[142:145], v[174:177], v[40:43]
	v_mfma_f32_16x16x32_bf16 v[28:31], v[134:137], v[182:185], v[28:31]
	v_mfma_f32_16x16x32_bf16 v[24:27], v[142:145], v[182:185], v[24:27]
	s_waitcnt lgkmcnt(0)
	v_mfma_f32_16x16x32_bf16 v[12:15], v[134:137], v[190:193], v[12:15]
	v_mfma_f32_16x16x32_bf16 v[8:11], v[142:145], v[190:193], v[8:11]
	s_setprio 0
	s_setprio 1
	v_mfma_f32_16x16x32_bf16 v[52:55], v[146:149], v[162:165], v[52:55]
	v_mfma_f32_16x16x32_bf16 v[48:51], v[154:157], v[162:165], v[48:51]
	v_mfma_f32_16x16x32_bf16 v[36:39], v[146:149], v[170:173], v[36:39]
	v_mfma_f32_16x16x32_bf16 v[32:35], v[154:157], v[170:173], v[32:35]
	v_mfma_f32_16x16x32_bf16 v[20:23], v[146:149], v[178:181], v[20:23]
	v_mfma_f32_16x16x32_bf16 v[16:19], v[154:157], v[178:181], v[16:19]
	v_mfma_f32_16x16x32_bf16 v[4:7], v[146:149], v[186:189], v[4:7]
	v_mfma_f32_16x16x32_bf16 v[0:3], v[154:157], v[186:189], v[0:3]
	v_mfma_f32_16x16x32_bf16 v[52:55], v[150:153], v[166:169], v[52:55]
	v_mfma_f32_16x16x32_bf16 v[48:51], v[158:161], v[166:169], v[48:51]
	v_mfma_f32_16x16x32_bf16 v[36:39], v[150:153], v[174:177], v[36:39]
	v_mfma_f32_16x16x32_bf16 v[32:35], v[158:161], v[174:177], v[32:35]
	v_mfma_f32_16x16x32_bf16 v[20:23], v[150:153], v[182:185], v[20:23]
	v_mfma_f32_16x16x32_bf16 v[16:19], v[158:161], v[182:185], v[16:19]
	v_mfma_f32_16x16x32_bf16 v[4:7], v[150:153], v[190:193], v[4:7]
	v_mfma_f32_16x16x32_bf16 v[0:3], v[158:161], v[190:193], v[0:3]
	s_setprio 0
	s_barrier
	v_add_u32_e32 v142, 0x18000, v249
	v_add_u32_e32 v158, 0x1c000, v249
	ds_read_b128 v[130:133], v142
	ds_read_b128 v[134:137], v142 offset:1024
	ds_read_b128 v[138:141], v142 offset:2048
	ds_read_b128 v[142:145], v142 offset:3072
	ds_read_b128 v[146:149], v158
	ds_read_b128 v[150:153], v158 offset:1024
	ds_read_b128 v[154:157], v158 offset:2048
	ds_read_b128 v[158:161], v158 offset:3072
	ds_read_b128 v[162:165], v250 offset:32768
	ds_read_b128 v[166:169], v250 offset:33792
	ds_read_b128 v[170:173], v250 offset:34816
	ds_read_b128 v[174:177], v250 offset:35840
	ds_read_b128 v[178:181], v250 offset:36864
	ds_read_b128 v[182:185], v250 offset:37888
	ds_read_b128 v[186:189], v250 offset:38912
	ds_read_b128 v[190:193], v250 offset:39936
	s_add_u32 s38, s42, 0x40000
	s_addc_u32 s39, s43, 0
	s_mov_b32 m0, s56
	s_nop 0
	global_load_lds_dwordx4 v96, s[38:39]
	s_nop 0
	s_mov_b32 m0, s57
	s_nop 0
	global_load_lds_dwordx4 v245, s[38:39]
	s_waitcnt vmcnt(8)
	s_waitcnt lgkmcnt(0)
	s_barrier
	s_setprio 1
	s_waitcnt lgkmcnt(7)
	v_mfma_f32_16x16x32_bf16 v[126:129], v[130:133], v[162:165], v[126:129]
	v_mfma_f32_16x16x32_bf16 v[122:125], v[138:141], v[162:165], v[122:125]
	s_waitcnt lgkmcnt(5)
	v_mfma_f32_16x16x32_bf16 v[110:113], v[130:133], v[170:173], v[110:113]
	v_mfma_f32_16x16x32_bf16 v[106:109], v[138:141], v[170:173], v[106:109]
	s_waitcnt lgkmcnt(3)
	v_mfma_f32_16x16x32_bf16 v[92:95], v[130:133], v[178:181], v[92:95]
	v_mfma_f32_16x16x32_bf16 v[88:91], v[138:141], v[178:181], v[88:91]
	s_waitcnt lgkmcnt(1)
	v_mfma_f32_16x16x32_bf16 v[76:79], v[130:133], v[186:189], v[76:79]
	v_mfma_f32_16x16x32_bf16 v[72:75], v[138:141], v[186:189], v[72:75]
	v_mfma_f32_16x16x32_bf16 v[126:129], v[134:137], v[166:169], v[126:129]
	v_mfma_f32_16x16x32_bf16 v[122:125], v[142:145], v[166:169], v[122:125]
	v_mfma_f32_16x16x32_bf16 v[110:113], v[134:137], v[174:177], v[110:113]
	v_mfma_f32_16x16x32_bf16 v[106:109], v[142:145], v[174:177], v[106:109]
	v_mfma_f32_16x16x32_bf16 v[92:95], v[134:137], v[182:185], v[92:95]
	v_mfma_f32_16x16x32_bf16 v[88:91], v[142:145], v[182:185], v[88:91]
	s_waitcnt lgkmcnt(0)
	v_mfma_f32_16x16x32_bf16 v[76:79], v[134:137], v[190:193], v[76:79]
	v_mfma_f32_16x16x32_bf16 v[72:75], v[142:145], v[190:193], v[72:75]
	s_setprio 0
	s_setprio 1
	v_mfma_f32_16x16x32_bf16 v[118:121], v[146:149], v[162:165], v[118:121]
	v_mfma_f32_16x16x32_bf16 v[114:117], v[154:157], v[162:165], v[114:117]
	v_mfma_f32_16x16x32_bf16 v[102:105], v[146:149], v[170:173], v[102:105]
	v_mfma_f32_16x16x32_bf16 v[98:101], v[154:157], v[170:173], v[98:101]
	v_mfma_f32_16x16x32_bf16 v[84:87], v[146:149], v[178:181], v[84:87]
	v_mfma_f32_16x16x32_bf16 v[80:83], v[154:157], v[178:181], v[80:83]
	v_mfma_f32_16x16x32_bf16 v[68:71], v[146:149], v[186:189], v[68:71]
	v_mfma_f32_16x16x32_bf16 v[64:67], v[154:157], v[186:189], v[64:67]
	v_mfma_f32_16x16x32_bf16 v[118:121], v[150:153], v[166:169], v[118:121]
	v_mfma_f32_16x16x32_bf16 v[114:117], v[158:161], v[166:169], v[114:117]
	v_mfma_f32_16x16x32_bf16 v[102:105], v[150:153], v[174:177], v[102:105]
	v_mfma_f32_16x16x32_bf16 v[98:101], v[158:161], v[174:177], v[98:101]
	v_mfma_f32_16x16x32_bf16 v[84:87], v[150:153], v[182:185], v[84:87]
	v_mfma_f32_16x16x32_bf16 v[80:83], v[158:161], v[182:185], v[80:83]
	v_mfma_f32_16x16x32_bf16 v[68:71], v[150:153], v[190:193], v[68:71]
	v_mfma_f32_16x16x32_bf16 v[64:67], v[158:161], v[190:193], v[64:67]
	s_setprio 0
	s_barrier
	ds_read_b128 v[162:165], v250 offset:49152
	ds_read_b128 v[166:169], v250 offset:50176
	ds_read_b128 v[170:173], v250 offset:51200
	ds_read_b128 v[174:177], v250 offset:52224
	ds_read_b128 v[178:181], v250 offset:53248
	ds_read_b128 v[182:185], v250 offset:54272
	ds_read_b128 v[186:189], v250 offset:55296
	ds_read_b128 v[190:193], v250 offset:56320
	s_add_u32 s38, s40, 0x80
	s_addc_u32 s39, s41, 0
	s_mov_b32 m0, s61
	s_nop 0
	global_load_lds_dwordx4 v244, s[38:39]
	s_nop 0
	s_mov_b32 m0, s62
	s_nop 0
	global_load_lds_dwordx4 v246, s[38:39]
	s_add_u32 s38, s40, 0x4080
	s_addc_u32 s39, s41, 0
	s_mov_b32 m0, s65
	s_nop 0
	global_load_lds_dwordx4 v244, s[38:39]
	s_nop 0
	s_mov_b32 m0, s66
	s_nop 0
	global_load_lds_dwordx4 v246, s[38:39]
	s_mov_b32 m0, s63
	s_nop 0
	global_load_lds_dwordx4 v96, s[6:7]
	s_nop 0
	s_mov_b32 m0, s64
	s_nop 0
	global_load_lds_dwordx4 v245, s[6:7]
	s_waitcnt vmcnt(8)
	s_waitcnt lgkmcnt(0)
	s_barrier
	s_setprio 1
	s_waitcnt lgkmcnt(7)
	v_mfma_f32_16x16x32_bf16 v[60:63], v[130:133], v[162:165], v[60:63]
	v_mfma_f32_16x16x32_bf16 v[56:59], v[138:141], v[162:165], v[56:59]
	s_waitcnt lgkmcnt(5)
	v_mfma_f32_16x16x32_bf16 v[44:47], v[130:133], v[170:173], v[44:47]
	v_mfma_f32_16x16x32_bf16 v[40:43], v[138:141], v[170:173], v[40:43]
	s_waitcnt lgkmcnt(3)
	v_mfma_f32_16x16x32_bf16 v[28:31], v[130:133], v[178:181], v[28:31]
	v_mfma_f32_16x16x32_bf16 v[24:27], v[138:141], v[178:181], v[24:27]
	s_waitcnt lgkmcnt(1)
	v_mfma_f32_16x16x32_bf16 v[12:15], v[130:133], v[186:189], v[12:15]
	v_mfma_f32_16x16x32_bf16 v[8:11], v[138:141], v[186:189], v[8:11]
	v_mfma_f32_16x16x32_bf16 v[60:63], v[134:137], v[166:169], v[60:63]
	v_mfma_f32_16x16x32_bf16 v[56:59], v[142:145], v[166:169], v[56:59]
	v_mfma_f32_16x16x32_bf16 v[44:47], v[134:137], v[174:177], v[44:47]
	v_mfma_f32_16x16x32_bf16 v[40:43], v[142:145], v[174:177], v[40:43]
	v_mfma_f32_16x16x32_bf16 v[28:31], v[134:137], v[182:185], v[28:31]
	v_mfma_f32_16x16x32_bf16 v[24:27], v[142:145], v[182:185], v[24:27]
	s_waitcnt lgkmcnt(0)
	v_mfma_f32_16x16x32_bf16 v[12:15], v[134:137], v[190:193], v[12:15]
	v_mfma_f32_16x16x32_bf16 v[8:11], v[142:145], v[190:193], v[8:11]
	s_setprio 0
	s_setprio 1
	v_mfma_f32_16x16x32_bf16 v[52:55], v[146:149], v[162:165], v[52:55]
	v_mfma_f32_16x16x32_bf16 v[48:51], v[154:157], v[162:165], v[48:51]
	v_mfma_f32_16x16x32_bf16 v[36:39], v[146:149], v[170:173], v[36:39]
	v_mfma_f32_16x16x32_bf16 v[32:35], v[154:157], v[170:173], v[32:35]
	v_mfma_f32_16x16x32_bf16 v[20:23], v[146:149], v[178:181], v[20:23]
	v_mfma_f32_16x16x32_bf16 v[16:19], v[154:157], v[178:181], v[16:19]
	v_mfma_f32_16x16x32_bf16 v[4:7], v[146:149], v[186:189], v[4:7]
	v_mfma_f32_16x16x32_bf16 v[0:3], v[154:157], v[186:189], v[0:3]
	v_mfma_f32_16x16x32_bf16 v[52:55], v[150:153], v[166:169], v[52:55]
	v_mfma_f32_16x16x32_bf16 v[48:51], v[158:161], v[166:169], v[48:51]
	v_mfma_f32_16x16x32_bf16 v[36:39], v[150:153], v[174:177], v[36:39]
	v_mfma_f32_16x16x32_bf16 v[32:35], v[158:161], v[174:177], v[32:35]
	v_mfma_f32_16x16x32_bf16 v[20:23], v[150:153], v[182:185], v[20:23]
	v_mfma_f32_16x16x32_bf16 v[16:19], v[158:161], v[182:185], v[16:19]
	v_mfma_f32_16x16x32_bf16 v[4:7], v[150:153], v[190:193], v[4:7]
	v_mfma_f32_16x16x32_bf16 v[0:3], v[158:161], v[190:193], v[0:3]
	s_setprio 0
	s_barrier
	s_add_i32 s45, s45, 2
	s_add_u32 s5, s5, 0x100
	s_addc_u32 s29, s29, 0
	s_cmp_gt_u32 s45, 13
	s_mov_b64 s[38:39], s[2:3]
	s_cbranch_scc0 .LBB0_1237
	s_and_b64 vcc, exec, s[24:25]
	s_cbranch_vccz .LBB0_1240
	s_barrier

.LBB0_1437:
	s_or_b64 exec, exec, s[4:5]
	v_lshlrev_b32_e32 v0, 5, v5
	v_lshlrev_b32_e32 v5, 6, v4
	v_sub_u32_e32 v5, v6, v5
	v_ashrrev_i16_sdwa v5, v239, sext(v5) dst_sel:DWORD dst_unused:UNUSED_PAD src0_sel:DWORD src1_sel:BYTE_0
	v_and_b32_e32 v0, 32, v0
	v_bfe_i32 v5, v5, 0, 16
	v_add_lshl_u32 v96, v0, v5, 1
	v_lshlrev_b32_e32 v5, 6, v1
	v_sub_u32_e32 v5, v11, v5
	v_lshlrev_b32_e32 v0, 5, v10
	v_ashrrev_i16_sdwa v5, v239, sext(v5) dst_sel:DWORD dst_unused:UNUSED_PAD src0_sel:DWORD src1_sel:BYTE_0
	v_and_b32_e32 v0, 32, v0
	v_bfe_i32 v5, v5, 0, 16
	v_add_lshl_u32 v200, v0, v5, 1
	s_waitcnt vmcnt(0)
	v_mad_u64_u32 v[214:215], s[4:5], v13, s12, v[96:97]
	v_mad_u64_u32 v[216:217], s[4:5], v8, s12, v[200:201]
	v_mad_u64_u32 v[218:219], s[4:5], v7, s12, v[96:97]
	s_lshl_b32 s86, s44, 16
	v_lshlrev_b32_e32 v0, 1, v199
	v_lshrrev_b32_e32 v5, 2, v199
	v_and_b32_e32 v4, 3, v4
	s_movk_i32 s13, 0xffe0
	s_lshl_b64 s[4:5], s[86:87], 10
	v_and_b32_e32 v0, 24, v0
	v_and_b32_e32 v5, 4, v5
	v_and_or_b32 v4, v199, s13, v4
	s_add_u32 s54, s50, s4
	v_or3_b32 v0, v4, v5, v0
	s_addc_u32 s55, s51, s5
	v_mad_u64_u32 v[202:203], s[4:5], v0, s12, v[96:97]
	v_lshlrev_b32_e32 v0, 1, v201
	v_lshrrev_b32_e32 v4, 2, v201
	v_and_b32_e32 v1, 3, v1
	v_and_b32_e32 v0, 24, v0
	v_and_b32_e32 v4, 4, v4
	v_and_or_b32 v1, v201, s13, v1
	s_add_u32 s18, s10, 0x69100000
	v_or3_b32 v0, v1, v4, v0
	s_addc_u32 s19, s11, 0
	v_mad_u64_u32 v[204:205], s[4:5], v0, s12, v[200:201]
	s_ashr_i32 s26, s6, 6
	s_ashr_i32 s13, s12, 31
	v_mad_u64_u32 v[220:221], s[4:5], v9, s12, v[200:201]
	s_ashr_i32 s15, s14, 31
	s_ashr_i32 s7, s6, 8
	s_lshl_b64 s[20:21], s[12:13], 7
	s_lshl_b32 s22, s26, 10
	s_lshl_b64 s[4:5], s[14:15], 21
	s_add_u32 s4, s54, s4
	s_addc_u32 s5, s55, s5
	v_readlane_b32 s24, v253, 29
	v_readlane_b32 s25, v253, 30
	s_add_u32 s38, s4, s24
	s_addc_u32 s39, s5, s25
	s_add_i32 s56, s22, 0
	s_add_i32 s57, s56, 0x10000
	s_mov_b32 m0, s57
	s_nop 0
	global_load_lds_dwordx4 v202, s[38:39]
	s_add_i32 s58, s56, 0x12000
	s_mov_b32 m0, s58
	s_nop 0
	global_load_lds_dwordx4 v204, s[38:39]
	s_add_u32 s4, s38, s20
	s_addc_u32 s5, s39, s21
	s_add_i32 s59, s56, 0x14000
	s_mov_b32 m0, s59
	s_nop 0
	global_load_lds_dwordx4 v202, s[4:5]
	s_add_i32 s60, s56, 0x16000
	s_mov_b32 m0, s60
	s_nop 0
	global_load_lds_dwordx4 v204, s[4:5]
	s_add_i32 s61, s56, 0x2000
	s_mov_b32 m0, s56
	s_nop 0
	global_load_lds_dwordx4 v218, s[18:19]
	s_add_i32 s62, s56, 0x4000
	s_mov_b32 m0, s61
	s_nop 0
	global_load_lds_dwordx4 v216, s[18:19]
	s_add_i32 s63, s56, 0x6000
	s_mov_b32 m0, s62
	s_nop 0
	global_load_lds_dwordx4 v214, s[18:19]
	s_cmp_eq_u32 s7, 1
	s_mov_b32 m0, s63
	s_nop 0
	global_load_lds_dwordx4 v220, s[18:19]
	s_cselect_b64 s[22:23], -1, 0
	s_cmp_lg_u32 s7, 1
	s_cbranch_scc1 .LBB0_1439
	s_barrier
.LBB0_1439:
	s_add_u32 s24, s10, 0x4e500000
	s_addc_u32 s25, s11, 0
	s_lshl_b64 s[28:29], s[86:87], 2
	s_add_u32 s64, s2, s28
	s_addc_u32 s65, s3, s29
	s_lshr_b32 s2, s13, 25
	v_and_b32_e32 v0, 63, v3
	v_bfe_u32 v203, v3, 4, 2
	v_and_b32_e32 v205, 15, v3
	s_add_i32 s2, s12, s2
	v_and_b32_e32 v1, 48, v3
	v_lshlrev_b32_e32 v3, 2, v3
	s_ashr_i32 s13, s2, 7
	s_lshl_b32 s2, s7, 13
	v_lshl_or_b32 v1, v205, 6, v1
	v_and_b32_e32 v3, 32, v3
	v_bitop3_b32 v244, v1, s2, v3 bitop3:0xde
	s_lshl_b32 s2, s26, 5
	s_and_b32 s67, s2, 0x60
	s_lshl_b32 s66, s7, 6
	s_lshl_b32 s2, s67, 7
	v_bitop3_b32 v245, s2, v1, v3 bitop3:0xf6
	s_add_u32 s2, s38, 0x80
	s_waitcnt vmcnt(2)
	s_barrier
	s_addc_u32 s3, s39, 0
	s_add_i32 s68, s56, 0x18000
	s_mov_b32 m0, s68
	s_nop 0
	global_load_lds_dwordx4 v202, s[2:3]
	s_add_i32 s69, s56, 0x1a000
	s_mov_b32 m0, s69
	s_nop 0
	global_load_lds_dwordx4 v204, s[2:3]
	s_add_u32 s2, s18, 0x80
	s_addc_u32 s3, s19, 0
	s_add_i32 s70, s56, 0x8000
	s_mov_b32 m0, s70
	s_nop 0
	global_load_lds_dwordx4 v218, s[2:3]
	s_add_i32 s71, s56, 0xa000
	s_mov_b32 m0, s71
	s_nop 0
	global_load_lds_dwordx4 v216, s[2:3]
	s_add_u32 s2, s4, 0x80
	s_addc_u32 s3, s5, 0
	s_add_i32 s72, s56, 0x1c000
	s_add_i32 s73, s56, 0x1e000
	s_mov_b32 m0, s72
	s_nop 0
	global_load_lds_dwordx4 v202, s[2:3]
	s_cmp_lt_u32 s6, 64
	s_mov_b32 m0, s73
	s_nop 0
	global_load_lds_dwordx4 v204, s[2:3]
	s_cselect_b64 s[26:27], -1, 0
	s_cmpk_gt_i32 s12, 0x7f
	s_waitcnt vmcnt(6)
	s_cselect_b64 s[28:29], -1, 0
	s_add_i32 s74, s13, -2
	s_add_i32 s75, s56, 0xc000
	s_cmpk_lt_u32 s6, 0x100
	v_readlane_b32 s2, v253, 27
	v_lshlrev_b32_e32 v246, 4, v0
	s_mov_b32 s76, 0
	s_cselect_b64 s[30:31], -1, 0
	s_mov_b32 s77, s2
	s_barrier
	v_readlane_b32 s3, v253, 28
	s_branch .LBB0_1442

.LBB0_1442:
	v_cndmask_b32_e64 v0, 0, 1, s[26:27]
	v_cmp_ne_u32_e64 s[4:5], 1, v0
	s_andn2_b64 vcc, exec, s[26:27]
	s_and_b32 s78, s76, 1
	s_cbranch_vccnz .LBB0_1444
	s_ashr_i32 s15, s14, 31
	s_lshl_b64 s[2:3], s[14:15], 13
	s_add_u32 s6, s64, s2
	s_addc_u32 s7, s65, s3
	s_lshl_b32 s2, s77, 8
	s_ashr_i32 s3, s2, 31
	s_lshl_b64 s[2:3], s[2:3], 2
	s_add_u32 s2, s6, s2
	s_addc_u32 s3, s7, s3
	s_lshl_b32 s6, s78, 10
	s_add_i32 s6, s6, 0
	s_add_i32 s6, s6, 0x21000
	s_mov_b32 m0, s6
	s_nop 0
	global_load_lds_dwordx4 v246, s[2:3]

.LBB0_1446:
	v_cndmask_b32_e64 v0, 0, 1, s[40:41]
	v_cmp_ne_u32_e64 s[2:3], 1, v0
	s_andn2_b64 vcc, exec, s[40:41]
	s_mov_b64 s[36:37], s[38:39]
	s_cbranch_vccnz .LBB0_1449
	s_ashr_i32 s15, s14, 31
	s_lshl_b64 s[6:7], s[14:15], 21
	s_add_u32 s15, s54, s6
	s_addc_u32 s37, s55, s7
	s_ashr_i32 s35, s34, 31
	s_lshl_b64 s[6:7], s[34:35], 18
	s_add_u32 s36, s15, s6
	s_addc_u32 s37, s37, s7
	s_and_b64 vcc, exec, s[4:5]
	s_cbranch_vccnz .LBB0_1449
	s_lshl_b32 s4, s14, 14
	s_ashr_i32 s5, s4, 31
	s_lshl_b64 s[4:5], s[4:5], 2
	s_add_u32 s4, s16, s4
	s_addc_u32 s5, s17, s5
	s_lshl_b32 s6, s14, 2
	s_add_i32 s6, s6, 0
	s_add_i32 s6, s6, 0x20480
	v_mov_b32_e32 v0, s6
	ds_read_b32 v0, v0
	s_lshl_b32 s6, s76, 10
	s_and_b32 s6, s6, 0x400
	s_add_i32 s6, s6, 0
	s_add_i32 s6, s6, 0x21800
	s_waitcnt lgkmcnt(0)
	v_sub_u32_e32 v0, v247, v0
	v_lshlrev_b32_e32 v0, 8, v0
	v_ashrrev_i32_e32 v1, 31, v0
	v_lshlrev_b64 v[0:1], 2, v[0:1]
	v_lshl_add_u64 v[0:1], s[4:5], 0, v[0:1]
	s_nop 0
	v_readfirstlane_b32 s5, v1
	v_readfirstlane_b32 s4, v0
	s_mov_b32 m0, s6
	s_nop 0
	global_load_lds_dwordx4 v246, s[4:5]

.LBB0_1452:
	s_add_i32 s79, s79, 2
	s_and_b64 s[44:45], s[48:49], exec
	s_cselect_b32 s45, 0, s42
	s_cselect_b32 s44, 0, s43
	s_add_u32 s46, s18, s45
	s_addc_u32 s47, s19, s44
	s_add_u32 s80, s38, s42
	s_addc_u32 s81, s39, s43
	s_add_u32 s44, s46, 0x80
	s_addc_u32 s45, s47, 0
	s_waitcnt vmcnt(8)
	s_and_b64 s[48:49], s[48:49], exec
	s_waitcnt lgkmcnt(0)
	s_cselect_b32 s80, s36, s80
	s_cselect_b32 s81, s37, s81
	s_add_u32 s48, s80, 0x80
	s_addc_u32 s49, s81, 0
	s_barrier
	s_setprio 1
	s_waitcnt lgkmcnt(0)
	v_mfma_scale_f32_16x16x128_f8f6f4 v[98:101], v[24:31], v[32:39], v[98:101], v243, v243 op_sel_hi:[0,0,0]
	v_mfma_scale_f32_16x16x128_f8f6f4 v[66:69], v[16:23], v[56:63], v[170:173], v243, v243 op_sel_hi:[0,0,0]
	v_mfma_scale_f32_16x16x128_f8f6f4 v[70:73], v[24:31], v[56:63], v[162:165], v243, v243 op_sel_hi:[0,0,0]
	v_mfma_scale_f32_16x16x128_f8f6f4 v[74:77], v[16:23], v[48:55], v[146:149], v243, v243 op_sel_hi:[0,0,0]
	v_mfma_scale_f32_16x16x128_f8f6f4 v[78:81], v[24:31], v[48:55], v[138:141], v243, v243 op_sel_hi:[0,0,0]
	v_mfma_scale_f32_16x16x128_f8f6f4 v[82:85], v[16:23], v[40:47], v[130:133], v243, v243 op_sel_hi:[0,0,0]
	v_mfma_scale_f32_16x16x128_f8f6f4 v[86:89], v[24:31], v[40:47], v[114:117], v243, v243 op_sel_hi:[0,0,0]
	v_mfma_scale_f32_16x16x128_f8f6f4 v[90:93], v[16:23], v[32:39], v[106:109], v243, v243 op_sel_hi:[0,0,0]
	s_setprio 0
	s_setprio 1
	v_mfma_scale_f32_16x16x128_f8f6f4 v[142:145], v[8:15], v[48:55], v[142:145], v243, v243 op_sel_hi:[0,0,0]
	v_mfma_scale_f32_16x16x128_f8f6f4 v[134:137], v[0:7], v[40:47], v[134:137], v243, v243 op_sel_hi:[0,0,0]
	v_mfma_scale_f32_16x16x128_f8f6f4 v[122:125], v[8:15], v[40:47], v[122:125], v243, v243 op_sel_hi:[0,0,0]
	v_mfma_scale_f32_16x16x128_f8f6f4 v[110:113], v[0:7], v[32:39], v[110:113], v243, v243 op_sel_hi:[0,0,0]
	v_mfma_scale_f32_16x16x128_f8f6f4 v[102:105], v[8:15], v[32:39], v[102:105], v243, v243 op_sel_hi:[0,0,0]
	v_mfma_scale_f32_16x16x128_f8f6f4 v[118:121], v[0:7], v[56:63], v[174:177], v243, v243 op_sel_hi:[0,0,0]
	v_mfma_scale_f32_16x16x128_f8f6f4 v[126:129], v[8:15], v[56:63], v[166:169], v243, v243 op_sel_hi:[0,0,0]
	v_mfma_scale_f32_16x16x128_f8f6f4 v[150:153], v[0:7], v[48:55], v[154:157], v243, v243 op_sel_hi:[0,0,0]
	s_setprio 0
	s_barrier
	s_mov_b32 m0, s57
	s_nop 0
	global_load_lds_dwordx4 v202, s[80:81]
	s_nop 0
	s_mov_b32 m0, s58
	s_nop 0
	global_load_lds_dwordx4 v204, s[80:81]
	s_add_u32 s80, s80, s20
	s_addc_u32 s81, s81, s21
	s_mov_b32 m0, s59
	s_nop 0
	global_load_lds_dwordx4 v202, s[80:81]
	s_nop 0
	s_mov_b32 m0, s60
	s_nop 0
	global_load_lds_dwordx4 v204, s[80:81]
	s_mov_b32 m0, s56
	s_nop 0
	global_load_lds_dwordx4 v206, s[46:47]
	s_nop 0
	s_mov_b32 m0, s61
	s_nop 0
	global_load_lds_dwordx4 v208, s[46:47]
	s_waitcnt vmcnt(8)
	s_waitcnt lgkmcnt(0)
	s_barrier
	s_barrier
	v_add_u32_e32 v12, 0x18000, v65
	v_add_u32_e32 v28, 0x1c000, v65
	ds_read_b128 v[0:3], v12
	ds_read_b128 v[4:7], v12 offset:1024
	ds_read_b128 v[8:11], v12 offset:2048
	ds_read_b128 v[12:15], v12 offset:3072
	ds_read_b128 v[16:19], v28
	ds_read_b128 v[20:23], v28 offset:1024
	ds_read_b128 v[24:27], v28 offset:2048
	ds_read_b128 v[28:31], v28 offset:3072
	ds_read_b128 v[32:35], v64 offset:32768
	ds_read_b128 v[36:39], v64 offset:33792
	ds_read_b128 v[40:43], v64 offset:34816
	ds_read_b128 v[44:47], v64 offset:35840
	ds_read_b128 v[48:51], v64 offset:36864
	ds_read_b128 v[52:55], v64 offset:37888
	ds_read_b128 v[56:59], v64 offset:38912
	ds_read_b128 v[60:63], v64 offset:39936
	s_mov_b32 m0, s62
	s_nop 0
	global_load_lds_dwordx4 v210, s[46:47]
	s_nop 0
	s_mov_b32 m0, s63
	s_nop 0
	global_load_lds_dwordx4 v212, s[46:47]
	s_waitcnt vmcnt(8)
	s_waitcnt lgkmcnt(0)
	s_barrier
	s_setprio 1
	s_waitcnt lgkmcnt(6)
	v_mfma_scale_f32_16x16x128_f8f6f4 v[170:173], v[0:7], v[32:39], v[66:69], v243, v243 op_sel_hi:[0,0,0]
	v_mfma_scale_f32_16x16x128_f8f6f4 v[162:165], v[8:15], v[32:39], v[70:73], v243, v243 op_sel_hi:[0,0,0]
	s_waitcnt lgkmcnt(4)
	v_mfma_scale_f32_16x16x128_f8f6f4 v[146:149], v[0:7], v[40:47], v[74:77], v243, v243 op_sel_hi:[0,0,0]
	v_mfma_scale_f32_16x16x128_f8f6f4 v[138:141], v[8:15], v[40:47], v[78:81], v243, v243 op_sel_hi:[0,0,0]
	s_waitcnt lgkmcnt(2)
	v_mfma_scale_f32_16x16x128_f8f6f4 v[130:133], v[0:7], v[48:55], v[82:85], v243, v243 op_sel_hi:[0,0,0]
	v_mfma_scale_f32_16x16x128_f8f6f4 v[114:117], v[8:15], v[48:55], v[86:89], v243, v243 op_sel_hi:[0,0,0]
	s_waitcnt lgkmcnt(0)
	v_mfma_scale_f32_16x16x128_f8f6f4 v[106:109], v[0:7], v[56:63], v[90:93], v243, v243 op_sel_hi:[0,0,0]
	v_mfma_scale_f32_16x16x128_f8f6f4 v[98:101], v[8:15], v[56:63], v[98:101], v243, v243 op_sel_hi:[0,0,0]
	s_setprio 0
	s_setprio 1
	v_mfma_scale_f32_16x16x128_f8f6f4 v[174:177], v[16:23], v[32:39], v[118:121], v243, v243 op_sel_hi:[0,0,0]
	v_mfma_scale_f32_16x16x128_f8f6f4 v[166:169], v[24:31], v[32:39], v[126:129], v243, v243 op_sel_hi:[0,0,0]
	v_mfma_scale_f32_16x16x128_f8f6f4 v[154:157], v[16:23], v[40:47], v[150:153], v243, v243 op_sel_hi:[0,0,0]
	v_mfma_scale_f32_16x16x128_f8f6f4 v[142:145], v[24:31], v[40:47], v[142:145], v243, v243 op_sel_hi:[0,0,0]
	v_mfma_scale_f32_16x16x128_f8f6f4 v[134:137], v[16:23], v[48:55], v[134:137], v243, v243 op_sel_hi:[0,0,0]
	v_mfma_scale_f32_16x16x128_f8f6f4 v[122:125], v[24:31], v[48:55], v[122:125], v243, v243 op_sel_hi:[0,0,0]
	v_mfma_scale_f32_16x16x128_f8f6f4 v[110:113], v[16:23], v[56:63], v[110:113], v243, v243 op_sel_hi:[0,0,0]
	v_mfma_scale_f32_16x16x128_f8f6f4 v[102:105], v[24:31], v[56:63], v[102:105], v243, v243 op_sel_hi:[0,0,0]
	s_setprio 0
	s_barrier
	s_mov_b32 m0, s68
	s_nop 0
	global_load_lds_dwordx4 v202, s[48:49]
	s_nop 0
	s_mov_b32 m0, s69
	s_nop 0
	global_load_lds_dwordx4 v204, s[48:49]
	s_add_u32 s46, s48, s20
	s_addc_u32 s47, s49, s21
	s_mov_b32 m0, s72
	s_nop 0
	global_load_lds_dwordx4 v202, s[46:47]
	s_nop 0
	s_mov_b32 m0, s73
	s_nop 0
	global_load_lds_dwordx4 v204, s[46:47]
	s_mov_b32 m0, s70
	s_nop 0
	global_load_lds_dwordx4 v206, s[44:45]
	s_nop 0
	s_mov_b32 m0, s71
	s_nop 0
	global_load_lds_dwordx4 v208, s[44:45]
	s_waitcnt vmcnt(8)
	s_waitcnt lgkmcnt(0)
	s_barrier
	s_barrier
	s_add_u32 s42, s42, 0x100
	s_addc_u32 s43, s43, 0
	s_cmp_ge_i32 s79, s13
	s_cbranch_scc1 .LBB0_1455
.LBB0_1453:
	v_add_u32_e32 v65, 0, v245
	v_add_u32_e32 v0, 0x10000, v65
	v_add_u32_e32 v12, 0x14000, v65
	ds_read_b128 v[16:19], v0
	ds_read_b128 v[20:23], v0 offset:1024
	ds_read_b128 v[24:27], v0 offset:2048
	ds_read_b128 v[28:31], v0 offset:3072
	ds_read_b128 v[0:3], v12
	ds_read_b128 v[4:7], v12 offset:1024
	ds_read_b128 v[8:11], v12 offset:2048
	ds_read_b128 v[12:15], v12 offset:3072
	s_cmp_eq_u32 s74, s79
	s_cselect_b64 s[48:49], -1, 0
	s_add_u32 s44, s18, s42
	s_addc_u32 s45, s19, s43
	s_add_u32 s44, s44, 0xffffff80
	s_addc_u32 s45, s45, -1
	v_add_u32_e32 v64, 0, v244
	ds_read_b128 v[56:59], v64
	ds_read_b128 v[60:63], v64 offset:1024
	ds_read_b128 v[48:51], v64 offset:2048
	ds_read_b128 v[52:55], v64 offset:3072
	ds_read_b128 v[40:43], v64 offset:4096
	ds_read_b128 v[44:47], v64 offset:5120
	ds_read_b128 v[32:35], v64 offset:6144
	ds_read_b128 v[36:39], v64 offset:7168
	s_mov_b32 m0, s75
	s_nop 0
	global_load_lds_dwordx4 v210, s[44:45]
	s_add_i32 s46, s56, 0xe000
	s_mov_b32 m0, s46
	s_nop 0
	global_load_lds_dwordx4 v212, s[44:45]
	s_and_b64 s[44:45], s[40:41], s[48:49]
	s_andn2_b64 vcc, exec, s[44:45]
	s_cbranch_vccnz .LBB0_1452
	v_mov_b32_e32 v66, s35
	ds_read2_b32 v[66:67], v66 offset1:32
	s_waitcnt lgkmcnt(0)
	v_sub_u32_e32 v67, v67, v247
	v_lshlrev_b32_e32 v67, 8, v67
	v_add_u32_e32 v66, v67, v66
	v_min_i32_e32 v66, 0x100, v66
	v_add_u32_e32 v66, -1, v66
	v_min_i32_e32 v67, v199, v66
	v_min_i32_e32 v68, v201, v66
	v_min_i32_e32 v69, v222, v66
	v_min_i32_e32 v66, v223, v66
	v_lshl_add_u32 v67, v67, 2, s15
	v_lshl_add_u32 v68, v68, 2, s15
	v_lshl_add_u32 v69, v69, 2, s15
	v_lshl_add_u32 v66, v66, 2, s15
	ds_read_b32 v67, v67
	ds_read_b32 v68, v68
	ds_read_b32 v69, v69
	ds_read_b32 v66, v66
	s_waitcnt lgkmcnt(3)
	v_mad_u64_u32 v[206:207], s[44:45], v67, s12, v[96:97]
	s_waitcnt lgkmcnt(2)
	v_mad_u64_u32 v[208:209], s[44:45], v68, s12, v[200:201]
	s_waitcnt lgkmcnt(1)
	v_mad_u64_u32 v[210:211], s[44:45], v69, s12, v[96:97]
	s_waitcnt lgkmcnt(0)
	v_mad_u64_u32 v[212:213], s[44:45], v66, s12, v[200:201]
	s_branch .LBB0_1452

.LBB0_1460:
	s_add_i32 s79, s79, 2
	s_and_b64 s[42:43], s[46:47], exec
	s_cselect_b32 s43, 0, s6
	s_cselect_b32 s42, 0, s7
	s_add_u32 s44, s18, s43
	s_addc_u32 s45, s19, s42
	s_add_u32 s48, s38, s6
	s_addc_u32 s49, s39, s7
	s_add_u32 s42, s44, 0x80
	s_addc_u32 s43, s45, 0
	s_waitcnt vmcnt(8)
	s_and_b64 s[46:47], s[46:47], exec
	s_waitcnt lgkmcnt(0)
	s_cselect_b32 s48, s36, s48
	s_cselect_b32 s49, s37, s49
	s_add_u32 s46, s48, 0x80
	s_addc_u32 s47, s49, 0
	s_barrier
	s_setprio 1
	s_waitcnt lgkmcnt(6)
	v_mfma_scale_f32_16x16x128_f8f6f4 v[170:173], v[16:23], v[56:63], v[170:173], v243, v243 op_sel_hi:[0,0,0]
	v_mfma_scale_f32_16x16x128_f8f6f4 v[162:165], v[24:31], v[56:63], v[162:165], v243, v243 op_sel_hi:[0,0,0]
	s_waitcnt lgkmcnt(4)
	v_mfma_scale_f32_16x16x128_f8f6f4 v[146:149], v[16:23], v[48:55], v[146:149], v243, v243 op_sel_hi:[0,0,0]
	v_mfma_scale_f32_16x16x128_f8f6f4 v[138:141], v[24:31], v[48:55], v[138:141], v243, v243 op_sel_hi:[0,0,0]
	s_waitcnt lgkmcnt(2)
	v_mfma_scale_f32_16x16x128_f8f6f4 v[130:133], v[16:23], v[40:47], v[130:133], v243, v243 op_sel_hi:[0,0,0]
	v_mfma_scale_f32_16x16x128_f8f6f4 v[114:117], v[24:31], v[40:47], v[114:117], v243, v243 op_sel_hi:[0,0,0]
	s_waitcnt lgkmcnt(0)
	v_mfma_scale_f32_16x16x128_f8f6f4 v[106:109], v[16:23], v[32:39], v[106:109], v243, v243 op_sel_hi:[0,0,0]
	v_mfma_scale_f32_16x16x128_f8f6f4 v[98:101], v[24:31], v[32:39], v[98:101], v243, v243 op_sel_hi:[0,0,0]
	s_setprio 0
	s_setprio 1
	v_mfma_scale_f32_16x16x128_f8f6f4 v[174:177], v[0:7], v[56:63], v[174:177], v243, v243 op_sel_hi:[0,0,0]
	v_mfma_scale_f32_16x16x128_f8f6f4 v[166:169], v[8:15], v[56:63], v[166:169], v243, v243 op_sel_hi:[0,0,0]
	v_mfma_scale_f32_16x16x128_f8f6f4 v[154:157], v[0:7], v[48:55], v[154:157], v243, v243 op_sel_hi:[0,0,0]
	v_mfma_scale_f32_16x16x128_f8f6f4 v[142:145], v[8:15], v[48:55], v[142:145], v243, v243 op_sel_hi:[0,0,0]
	v_mfma_scale_f32_16x16x128_f8f6f4 v[134:137], v[0:7], v[40:47], v[134:137], v243, v243 op_sel_hi:[0,0,0]
	v_mfma_scale_f32_16x16x128_f8f6f4 v[122:125], v[8:15], v[40:47], v[122:125], v243, v243 op_sel_hi:[0,0,0]
	v_mfma_scale_f32_16x16x128_f8f6f4 v[110:113], v[0:7], v[32:39], v[110:113], v243, v243 op_sel_hi:[0,0,0]
	v_mfma_scale_f32_16x16x128_f8f6f4 v[102:105], v[8:15], v[32:39], v[102:105], v243, v243 op_sel_hi:[0,0,0]
	s_setprio 0
	s_barrier
	ds_read_b128 v[32:35], v206 offset:16384
	ds_read_b128 v[36:39], v206 offset:17408
	ds_read_b128 v[40:43], v206 offset:18432
	ds_read_b128 v[44:47], v206 offset:19456
	ds_read_b128 v[48:51], v206 offset:20480
	ds_read_b128 v[52:55], v206 offset:21504
	ds_read_b128 v[56:59], v206 offset:22528
	ds_read_b128 v[60:63], v206 offset:23552
	s_mov_b32 m0, s57
	s_nop 0
	global_load_lds_dwordx4 v202, s[48:49]
	s_nop 0
	s_mov_b32 m0, s58
	s_nop 0
	global_load_lds_dwordx4 v204, s[48:49]
	s_add_u32 s48, s48, s20
	s_addc_u32 s49, s49, s21
	s_mov_b32 m0, s59
	s_nop 0
	global_load_lds_dwordx4 v202, s[48:49]
	s_nop 0
	s_mov_b32 m0, s60
	s_nop 0
	global_load_lds_dwordx4 v204, s[48:49]
	s_mov_b32 m0, s56
	s_nop 0
	global_load_lds_dwordx4 v218, s[44:45]
	s_nop 0
	s_mov_b32 m0, s61
	s_nop 0
	global_load_lds_dwordx4 v216, s[44:45]
	s_waitcnt vmcnt(8)
	s_waitcnt lgkmcnt(0)
	s_barrier
	s_setprio 1
	s_waitcnt lgkmcnt(6)
	v_mfma_scale_f32_16x16x128_f8f6f4 v[190:193], v[16:23], v[32:39], v[190:193], v243, v243 op_sel_hi:[0,0,0]
	v_mfma_scale_f32_16x16x128_f8f6f4 v[182:185], v[24:31], v[32:39], v[182:185], v243, v243 op_sel_hi:[0,0,0]
	s_waitcnt lgkmcnt(4)
	v_mfma_scale_f32_16x16x128_f8f6f4 v[158:161], v[16:23], v[40:47], v[158:161], v243, v243 op_sel_hi:[0,0,0]
	v_mfma_scale_f32_16x16x128_f8f6f4 v[126:129], v[24:31], v[40:47], v[126:129], v243, v243 op_sel_hi:[0,0,0]
	s_waitcnt lgkmcnt(2)
	v_mfma_scale_f32_16x16x128_f8f6f4 v[92:95], v[16:23], v[48:55], v[92:95], v243, v243 op_sel_hi:[0,0,0]
	v_mfma_scale_f32_16x16x128_f8f6f4 v[84:87], v[24:31], v[48:55], v[84:87], v243, v243 op_sel_hi:[0,0,0]
	s_waitcnt lgkmcnt(0)
	v_mfma_scale_f32_16x16x128_f8f6f4 v[76:79], v[16:23], v[56:63], v[76:79], v243, v243 op_sel_hi:[0,0,0]
	v_mfma_scale_f32_16x16x128_f8f6f4 v[68:71], v[24:31], v[56:63], v[68:71], v243, v243 op_sel_hi:[0,0,0]
	s_setprio 0
	s_setprio 1
	v_mfma_scale_f32_16x16x128_f8f6f4 v[186:189], v[0:7], v[32:39], v[186:189], v243, v243 op_sel_hi:[0,0,0]
	v_mfma_scale_f32_16x16x128_f8f6f4 v[178:181], v[8:15], v[32:39], v[178:181], v243, v243 op_sel_hi:[0,0,0]
	v_mfma_scale_f32_16x16x128_f8f6f4 v[150:153], v[0:7], v[40:47], v[150:153], v243, v243 op_sel_hi:[0,0,0]
	v_mfma_scale_f32_16x16x128_f8f6f4 v[118:121], v[8:15], v[40:47], v[118:121], v243, v243 op_sel_hi:[0,0,0]
	v_mfma_scale_f32_16x16x128_f8f6f4 v[88:91], v[0:7], v[48:55], v[88:91], v243, v243 op_sel_hi:[0,0,0]
	v_mfma_scale_f32_16x16x128_f8f6f4 v[80:83], v[8:15], v[48:55], v[80:83], v243, v243 op_sel_hi:[0,0,0]
	v_mfma_scale_f32_16x16x128_f8f6f4 v[72:75], v[0:7], v[56:63], v[72:75], v243, v243 op_sel_hi:[0,0,0]
	v_mfma_scale_f32_16x16x128_f8f6f4 v[64:67], v[8:15], v[56:63], v[64:67], v243, v243 op_sel_hi:[0,0,0]
	s_setprio 0
	s_barrier
	v_add_u32_e32 v12, 0x18000, v207
	v_add_u32_e32 v28, 0x1c000, v207
	ds_read_b128 v[0:3], v12
	ds_read_b128 v[4:7], v12 offset:1024
	ds_read_b128 v[8:11], v12 offset:2048
	ds_read_b128 v[12:15], v12 offset:3072
	ds_read_b128 v[16:19], v28
	ds_read_b128 v[20:23], v28 offset:1024
	ds_read_b128 v[24:27], v28 offset:2048
	ds_read_b128 v[28:31], v28 offset:3072
	ds_read_b128 v[32:35], v206 offset:32768
	ds_read_b128 v[36:39], v206 offset:33792
	ds_read_b128 v[40:43], v206 offset:34816
	ds_read_b128 v[44:47], v206 offset:35840
	ds_read_b128 v[48:51], v206 offset:36864
	ds_read_b128 v[52:55], v206 offset:37888
	ds_read_b128 v[56:59], v206 offset:38912
	ds_read_b128 v[60:63], v206 offset:39936
	s_mov_b32 m0, s62
	s_nop 0
	global_load_lds_dwordx4 v214, s[44:45]
	s_nop 0
	s_mov_b32 m0, s63
	s_nop 0
	global_load_lds_dwordx4 v220, s[44:45]
	s_waitcnt vmcnt(8)
	s_waitcnt lgkmcnt(0)
	s_barrier
	s_setprio 1
	s_waitcnt lgkmcnt(6)
	v_mfma_scale_f32_16x16x128_f8f6f4 v[170:173], v[0:7], v[32:39], v[170:173], v243, v243 op_sel_hi:[0,0,0]
	v_mfma_scale_f32_16x16x128_f8f6f4 v[162:165], v[8:15], v[32:39], v[162:165], v243, v243 op_sel_hi:[0,0,0]
	s_waitcnt lgkmcnt(4)
	v_mfma_scale_f32_16x16x128_f8f6f4 v[146:149], v[0:7], v[40:47], v[146:149], v243, v243 op_sel_hi:[0,0,0]
	v_mfma_scale_f32_16x16x128_f8f6f4 v[138:141], v[8:15], v[40:47], v[138:141], v243, v243 op_sel_hi:[0,0,0]
	s_waitcnt lgkmcnt(2)
	v_mfma_scale_f32_16x16x128_f8f6f4 v[130:133], v[0:7], v[48:55], v[130:133], v243, v243 op_sel_hi:[0,0,0]
	v_mfma_scale_f32_16x16x128_f8f6f4 v[114:117], v[8:15], v[48:55], v[114:117], v243, v243 op_sel_hi:[0,0,0]
	s_waitcnt lgkmcnt(0)
	v_mfma_scale_f32_16x16x128_f8f6f4 v[106:109], v[0:7], v[56:63], v[106:109], v243, v243 op_sel_hi:[0,0,0]
	v_mfma_scale_f32_16x16x128_f8f6f4 v[98:101], v[8:15], v[56:63], v[98:101], v243, v243 op_sel_hi:[0,0,0]
	s_setprio 0
	s_setprio 1
	v_mfma_scale_f32_16x16x128_f8f6f4 v[174:177], v[16:23], v[32:39], v[174:177], v243, v243 op_sel_hi:[0,0,0]
	v_mfma_scale_f32_16x16x128_f8f6f4 v[166:169], v[24:31], v[32:39], v[166:169], v243, v243 op_sel_hi:[0,0,0]
	v_mfma_scale_f32_16x16x128_f8f6f4 v[154:157], v[16:23], v[40:47], v[154:157], v243, v243 op_sel_hi:[0,0,0]
	v_mfma_scale_f32_16x16x128_f8f6f4 v[142:145], v[24:31], v[40:47], v[142:145], v243, v243 op_sel_hi:[0,0,0]
	v_mfma_scale_f32_16x16x128_f8f6f4 v[134:137], v[16:23], v[48:55], v[134:137], v243, v243 op_sel_hi:[0,0,0]
	v_mfma_scale_f32_16x16x128_f8f6f4 v[122:125], v[24:31], v[48:55], v[122:125], v243, v243 op_sel_hi:[0,0,0]
	v_mfma_scale_f32_16x16x128_f8f6f4 v[110:113], v[16:23], v[56:63], v[110:113], v243, v243 op_sel_hi:[0,0,0]
	v_mfma_scale_f32_16x16x128_f8f6f4 v[102:105], v[24:31], v[56:63], v[102:105], v243, v243 op_sel_hi:[0,0,0]
	s_setprio 0
	s_barrier
	ds_read_b128 v[32:35], v206 offset:49152
	ds_read_b128 v[36:39], v206 offset:50176
	ds_read_b128 v[40:43], v206 offset:51200
	ds_read_b128 v[44:47], v206 offset:52224
	ds_read_b128 v[48:51], v206 offset:53248
	ds_read_b128 v[52:55], v206 offset:54272
	ds_read_b128 v[56:59], v206 offset:55296
	ds_read_b128 v[60:63], v206 offset:56320
	s_mov_b32 m0, s68
	s_nop 0
	global_load_lds_dwordx4 v202, s[46:47]
	s_nop 0
	s_mov_b32 m0, s69
	s_nop 0
	global_load_lds_dwordx4 v204, s[46:47]
	s_add_u32 s44, s46, s20
	s_addc_u32 s45, s47, s21
	s_mov_b32 m0, s72
	s_nop 0
	global_load_lds_dwordx4 v202, s[44:45]
	s_nop 0
	s_mov_b32 m0, s73
	s_nop 0
	global_load_lds_dwordx4 v204, s[44:45]
	s_mov_b32 m0, s70
	s_nop 0
	global_load_lds_dwordx4 v218, s[42:43]
	s_nop 0
	s_mov_b32 m0, s71
	s_nop 0
	global_load_lds_dwordx4 v216, s[42:43]
	s_waitcnt vmcnt(8)
	s_waitcnt lgkmcnt(0)
	s_barrier
	s_setprio 1
	s_waitcnt lgkmcnt(6)
	v_mfma_scale_f32_16x16x128_f8f6f4 v[190:193], v[0:7], v[32:39], v[190:193], v243, v243 op_sel_hi:[0,0,0]
	v_mfma_scale_f32_16x16x128_f8f6f4 v[182:185], v[8:15], v[32:39], v[182:185], v243, v243 op_sel_hi:[0,0,0]
	s_waitcnt lgkmcnt(4)
	v_mfma_scale_f32_16x16x128_f8f6f4 v[158:161], v[0:7], v[40:47], v[158:161], v243, v243 op_sel_hi:[0,0,0]
	v_mfma_scale_f32_16x16x128_f8f6f4 v[126:129], v[8:15], v[40:47], v[126:129], v243, v243 op_sel_hi:[0,0,0]
	s_waitcnt lgkmcnt(2)
	v_mfma_scale_f32_16x16x128_f8f6f4 v[92:95], v[0:7], v[48:55], v[92:95], v243, v243 op_sel_hi:[0,0,0]
	v_mfma_scale_f32_16x16x128_f8f6f4 v[84:87], v[8:15], v[48:55], v[84:87], v243, v243 op_sel_hi:[0,0,0]
	s_waitcnt lgkmcnt(0)
	v_mfma_scale_f32_16x16x128_f8f6f4 v[76:79], v[0:7], v[56:63], v[76:79], v243, v243 op_sel_hi:[0,0,0]
	v_mfma_scale_f32_16x16x128_f8f6f4 v[68:71], v[8:15], v[56:63], v[68:71], v243, v243 op_sel_hi:[0,0,0]
	s_setprio 0
	s_setprio 1
	v_mfma_scale_f32_16x16x128_f8f6f4 v[186:189], v[16:23], v[32:39], v[186:189], v243, v243 op_sel_hi:[0,0,0]
	v_mfma_scale_f32_16x16x128_f8f6f4 v[178:181], v[24:31], v[32:39], v[178:181], v243, v243 op_sel_hi:[0,0,0]
	v_mfma_scale_f32_16x16x128_f8f6f4 v[150:153], v[16:23], v[40:47], v[150:153], v243, v243 op_sel_hi:[0,0,0]
	v_mfma_scale_f32_16x16x128_f8f6f4 v[118:121], v[24:31], v[40:47], v[118:121], v243, v243 op_sel_hi:[0,0,0]
	v_mfma_scale_f32_16x16x128_f8f6f4 v[88:91], v[16:23], v[48:55], v[88:91], v243, v243 op_sel_hi:[0,0,0]
	v_mfma_scale_f32_16x16x128_f8f6f4 v[80:83], v[24:31], v[48:55], v[80:83], v243, v243 op_sel_hi:[0,0,0]
	v_mfma_scale_f32_16x16x128_f8f6f4 v[72:75], v[16:23], v[56:63], v[72:75], v243, v243 op_sel_hi:[0,0,0]
	v_mfma_scale_f32_16x16x128_f8f6f4 v[64:67], v[24:31], v[56:63], v[64:67], v243, v243 op_sel_hi:[0,0,0]
	s_setprio 0
	s_barrier
	s_add_u32 s6, s6, 0x100
	s_addc_u32 s7, s7, 0
	s_cmp_ge_i32 s79, s13
	s_cbranch_scc1 .LBB0_1464
.LBB0_1461:
	v_add_u32_e32 v207, 0, v245
	v_add_u32_e32 v0, 0x10000, v207
	v_add_u32_e32 v12, 0x14000, v207
	ds_read_b128 v[16:19], v0
	ds_read_b128 v[20:23], v0 offset:1024
	ds_read_b128 v[24:27], v0 offset:2048
	ds_read_b128 v[28:31], v0 offset:3072
	ds_read_b128 v[0:3], v12
	ds_read_b128 v[4:7], v12 offset:1024
	ds_read_b128 v[8:11], v12 offset:2048
	ds_read_b128 v[12:15], v12 offset:3072
	s_cmp_eq_u32 s74, s79
	s_cselect_b64 s[46:47], -1, 0
	s_add_u32 s42, s18, s6
	s_addc_u32 s43, s19, s7
	s_add_u32 s42, s42, 0xffffff80
	s_addc_u32 s43, s43, -1
	v_add_u32_e32 v206, 0, v244
	ds_read_b128 v[56:59], v206
	ds_read_b128 v[60:63], v206 offset:1024
	ds_read_b128 v[48:51], v206 offset:2048
	ds_read_b128 v[52:55], v206 offset:3072
	ds_read_b128 v[40:43], v206 offset:4096
	ds_read_b128 v[44:47], v206 offset:5120
	ds_read_b128 v[32:35], v206 offset:6144
	ds_read_b128 v[36:39], v206 offset:7168
	s_mov_b32 m0, s75
	s_nop 0
	global_load_lds_dwordx4 v214, s[42:43]
	s_add_i32 s44, s56, 0xe000
	s_mov_b32 m0, s44
	s_nop 0
	global_load_lds_dwordx4 v220, s[42:43]
	s_and_b64 s[42:43], s[40:41], s[46:47]
	s_andn2_b64 vcc, exec, s[42:43]
	s_cbranch_vccnz .LBB0_1460
	v_mov_b32_e32 v194, s35
	ds_read2_b32 v[194:195], v194 offset1:32
	s_waitcnt lgkmcnt(0)
	v_sub_u32_e32 v195, v195, v247
	v_lshlrev_b32_e32 v195, 8, v195
	v_add_u32_e32 v194, v195, v194
	v_min_i32_e32 v194, 0x100, v194
	v_add_u32_e32 v194, -1, v194
	v_min_i32_e32 v195, v199, v194
	v_min_i32_e32 v196, v201, v194
	v_min_i32_e32 v197, v222, v194
	v_min_i32_e32 v194, v223, v194
	v_lshl_add_u32 v195, v195, 2, s15
	v_lshl_add_u32 v196, v196, 2, s15
	v_lshl_add_u32 v197, v197, 2, s15
	v_lshl_add_u32 v194, v194, 2, s15
	ds_read_b32 v195, v195
	ds_read_b32 v196, v196
	ds_read_b32 v197, v197
	ds_read_b32 v194, v194
	s_waitcnt lgkmcnt(3)
	v_mad_u64_u32 v[218:219], s[42:43], v195, s12, v[96:97]
	s_waitcnt lgkmcnt(2)
	v_mad_u64_u32 v[216:217], s[42:43], v196, s12, v[200:201]
	s_waitcnt lgkmcnt(1)
	v_mad_u64_u32 v[214:215], s[42:43], v197, s12, v[96:97]
	s_waitcnt lgkmcnt(0)
	v_mad_u64_u32 v[220:221], s[42:43], v194, s12, v[200:201]
	s_branch .LBB0_1460

.LBB0_1551:
	s_or_b64 exec, exec, s[2:3]
	v_readlane_b32 s2, v253, 62
	s_waitcnt lgkmcnt(0)
	s_barrier
	v_mov_b32_e32 v0, s2
	ds_read_b32 v0, v0
	s_add_u32 s53, s8, 0x23b00000
	s_addc_u32 s54, s9, 0
	s_movk_i32 s12, 0x400
	v_mov_b32_e32 v1, v130
	s_waitcnt lgkmcnt(0)
	v_readfirstlane_b32 s2, v0
	s_lshl_b32 s55, s2, 2
	s_cmp_ge_i32 s90, s55
	v_readfirstlane_b32 s6, v1
	s_cbranch_scc1 .LBB0_1582
	v_bfe_i32 v3, v1, 27, 1
	v_lshlrev_b32_e32 v2, 4, v1
	v_lshrrev_b32_e32 v3, 22, v3
	v_add_u32_e32 v3, v2, v3
	v_and_b32_e32 v3, 0xfffffc00, v3
	v_sub_u32_e32 v3, v2, v3
	v_ashrrev_i32_e32 v0, 31, v1
	v_lshrrev_b32_e32 v4, 4, v3
	v_lshrrev_b32_e32 v0, 26, v0
	v_bitop3_b32 v3, v4, v3, 32 bitop3:0x6c
	v_add_u32_e32 v0, v1, v0
	v_ashrrev_i32_e32 v5, 31, v3
	v_ashrrev_i32_e32 v0, 6, v0
	v_lshrrev_b32_e32 v5, 26, v5
	v_lshlrev_b32_e32 v4, 3, v0
	v_add_u32_e32 v5, v3, v5
	v_and_b32_e32 v4, -16, v4
	v_ashrrev_i32_e32 v6, 6, v5
	v_and_b32_e32 v5, 0xc0, v5
	v_add_u32_e32 v4, v6, v4
	v_sub_u32_e32 v3, v3, v5
	v_lshlrev_b32_e32 v0, 5, v0
	v_ashrrev_i16_sdwa v3, v239, sext(v3) dst_sel:DWORD dst_unused:UNUSED_PAD src0_sel:DWORD src1_sel:BYTE_0
	v_lshlrev_b32_e32 v5, 1, v4
	v_lshlrev_b32_e32 v7, 2, v4
	v_lshrrev_b32_e32 v8, 2, v4
	v_and_b32_e32 v6, 3, v6
	v_and_b32_e32 v0, 32, v0
	v_bfe_i32 v3, v3, 0, 16
	v_and_b32_e32 v5, 0xffffffc0, v5
	v_and_b32_e32 v8, 4, v8
	v_and_or_b32 v6, v7, 48, v6
	v_or3_b32 v5, v6, v5, v8
	v_add_lshl_u32 v0, v0, v3, 1
	v_mad_u64_u32 v[132:133], s[4:5], v4, s12, v[0:1]
	v_mad_u64_u32 v[134:135], s[4:5], v5, s12, v[0:1]
	v_add_u32_e32 v0, 0x2000, v2
	v_ashrrev_i32_e32 v2, 31, v0
	v_lshrrev_b32_e32 v2, 22, v2
	v_add_u32_e32 v2, v0, v2
	v_ashrrev_i32_e32 v2, 10, v2
	v_mul_i32_i24_e32 v3, 0x400, v2
	v_sub_u32_e32 v0, v0, v3
	v_lshrrev_b32_e32 v3, 4, v0
	v_bitop3_b32 v0, v3, v0, 32 bitop3:0x6c
	v_ashrrev_i32_e32 v4, 31, v0
	v_lshrrev_b32_e32 v4, 26, v4
	v_lshlrev_b32_e32 v3, 3, v2
	v_add_u32_e32 v4, v0, v4
	v_and_b32_e32 v3, -16, v3
	v_ashrrev_i32_e32 v5, 6, v4
	v_and_b32_e32 v4, 0xc0, v4
	v_add_u32_e32 v3, v5, v3
	v_sub_u32_e32 v0, v0, v4
	v_lshlrev_b32_e32 v2, 5, v2
	v_ashrrev_i16_sdwa v0, v239, sext(v0) dst_sel:DWORD dst_unused:UNUSED_PAD src0_sel:DWORD src1_sel:BYTE_0
	v_lshlrev_b32_e32 v4, 1, v3
	v_lshlrev_b32_e32 v6, 2, v3
	v_lshrrev_b32_e32 v7, 2, v3
	v_and_b32_e32 v5, 3, v5
	v_and_b32_e32 v2, 32, v2
	v_bfe_i32 v0, v0, 0, 16
	v_and_b32_e32 v4, 0xffffffc0, v4
	v_and_b32_e32 v7, 4, v7
	v_and_or_b32 v5, v6, 48, v5
	v_or3_b32 v4, v5, v4, v7
	v_add_lshl_u32 v0, v2, v0, 1
	v_mad_u64_u32 v[136:137], s[4:5], v3, s12, v[0:1]
	v_mad_u64_u32 v[138:139], s[4:5], v4, s12, v[0:1]
	v_readlane_b32 s4, v253, 4
	s_lshl_b32 s86, s44, 15
	s_lshl_b64 s[2:3], s[86:87], 10
	v_mov_b32_e32 v0, s4
	ds_read_b32 v152, v0 offset:1792
	s_add_u32 s56, s53, s2
	s_addc_u32 s57, s54, s3
	v_readlane_b32 s19, v254, 16
	s_add_u32 s58, s8, 0x4e500000
	s_waitcnt lgkmcnt(0)
	v_lshlrev_b32_e32 v0, 2, v152
	v_add_u32_e32 v0, 0, v0
	v_add_u32_e32 v0, 0x20600, v0
	ds_read_b32 v0, v0
	v_mov_b32_e32 v2, s19
	v_readfirstlane_b32 s19, v152
	s_addc_u32 s59, s9, 0
	s_ashr_i32 s13, s12, 31
	ds_read_b32 v2, v2
	s_waitcnt lgkmcnt(1)
	v_readfirstlane_b32 s4, v0
	s_lshl_b32 s19, s19, 8
	s_ashr_i32 s7, s6, 6
	s_ashr_i32 s5, s4, 31
	s_mul_i32 s20, s19, s13
	s_mul_hi_u32 s21, s19, s12
	s_ashr_i32 s24, s6, 8
	s_lshl_b64 s[14:15], s[12:13], 3
	s_lshl_b64 s[16:17], s[12:13], 7
	s_lshl_b32 s18, s7, 10
	s_add_i32 s21, s21, s20
	s_lshl_b64 s[4:5], s[4:5], 20
	s_add_u32 s4, s56, s4
	s_addc_u32 s5, s57, s5
	v_readlane_b32 s22, v253, 7
	v_readlane_b32 s23, v253, 8
	s_add_u32 s40, s4, s22
	s_addc_u32 s41, s5, s23
	s_add_i32 s60, s18, 0
	s_load_dwordx2 s[2:3], s[10:11], 0x78
	s_add_i32 s61, s60, 0x10000
	s_mov_b32 m0, s61
	s_nop 0
	global_load_lds_dwordx4 v134, s[40:41]
	s_add_i32 s62, s60, 0x12000
	s_mov_b32 m0, s62
	s_nop 0
	global_load_lds_dwordx4 v138, s[40:41]
	s_add_u32 s4, s40, s14
	s_mul_i32 s19, s19, s12
	s_addc_u32 s5, s41, s15
	s_add_i32 s63, s60, 0x14000
	s_mov_b32 m0, s63
	s_nop 0
	global_load_lds_dwordx4 v134, s[4:5]
	s_add_i32 s64, s60, 0x16000
	s_mov_b32 m0, s64
	s_nop 0
	global_load_lds_dwordx4 v138, s[4:5]
	s_add_u32 s42, s58, s19
	s_addc_u32 s43, s59, s21
	s_mov_b32 m0, s60
	s_nop 0
	global_load_lds_dwordx4 v132, s[42:43]
	s_add_i32 s65, s60, 0x2000
	s_mov_b32 m0, s65
	s_nop 0
	global_load_lds_dwordx4 v136, s[42:43]
	s_add_u32 s18, s42, s16
	s_addc_u32 s19, s43, s17
	s_add_i32 s66, s60, 0x4000
	s_mov_b32 m0, s66
	s_nop 0
	global_load_lds_dwordx4 v132, s[18:19]
	s_add_i32 s67, s60, 0x6000
	s_mov_b32 m0, s67
	s_nop 0
	global_load_lds_dwordx4 v136, s[18:19]
	s_cmp_eq_u32 s24, 1
	s_cselect_b64 s[18:19], -1, 0
	s_cmp_lg_u32 s24, 1
	s_cbranch_scc1 .LBB0_1554
	s_barrier
.LBB0_1554:
	v_readlane_b32 s20, v253, 3
	v_and_b32_e32 v3, 63, v1
	v_bfe_u32 v96, v1, 4, 2
	s_waitcnt lgkmcnt(0)
	v_cmp_ge_i32_e32 vcc, s20, v2
	s_add_u32 s20, s8, 0x57500000
	s_addc_u32 s21, s9, 0
	s_lshl_b64 s[22:23], s[86:87], 2
	s_add_u32 s22, s2, s22
	s_addc_u32 s23, s3, s23
	s_lshr_b32 s2, s13, 25
	v_and_b32_e32 v131, 15, v1
	s_add_i32 s2, s12, s2
	v_and_b32_e32 v4, 48, v1
	v_lshlrev_b32_e32 v1, 2, v1
	s_and_b32 s7, s7, 3
	s_ashr_i32 s68, s2, 7
	s_lshl_b32 s2, s24, 13
	v_lshl_or_b32 v4, v131, 6, v4
	v_and_b32_e32 v1, 32, v1
	s_lshl_b32 s69, s24, 6
	v_bitop3_b32 v133, v4, s2, v1 bitop3:0xde
	s_lshl_b32 s2, s7, 12
	v_bitop3_b32 v135, v4, s2, v1 bitop3:0xde
	s_add_u32 s2, s40, 0x80
	s_waitcnt vmcnt(2)
	s_barrier
	s_addc_u32 s3, s41, 0
	s_add_i32 s70, s60, 0x18000
	s_mov_b32 m0, s70
	s_nop 0
	global_load_lds_dwordx4 v134, s[2:3]
	s_add_i32 s71, s60, 0x1a000
	s_mov_b32 m0, s71
	s_nop 0
	global_load_lds_dwordx4 v138, s[2:3]
	s_add_u32 s2, s42, 0x80
	s_addc_u32 s3, s43, 0
	s_add_i32 s72, s60, 0x8000
	s_mov_b32 m0, s72
	s_nop 0
	global_load_lds_dwordx4 v132, s[2:3]
	s_add_i32 s73, s60, 0xa000
	s_mov_b32 m0, s73
	s_nop 0
	global_load_lds_dwordx4 v136, s[2:3]
	s_add_u32 s2, s4, 0x80
	s_addc_u32 s3, s5, 0
	s_add_i32 s74, s60, 0x1c000
	s_add_i32 s75, s60, 0x1e000
	s_cmp_lt_u32 s6, 64
	s_cselect_b64 s[24:25], -1, 0
	s_cmpk_gt_i32 s12, 0x7f
	s_mov_b32 m0, s74
	s_nop 0
	global_load_lds_dwordx4 v134, s[2:3]
	s_cselect_b64 s[26:27], -1, 0
	s_add_i32 s76, s68, -2
	s_add_i32 s77, s60, 0xc000
	s_mov_b32 m0, s75
	s_nop 0
	global_load_lds_dwordx4 v138, s[2:3]
	s_cmpk_lt_u32 s6, 0x100
	s_waitcnt vmcnt(6)
	s_cselect_b64 s[28:29], -1, 0
	s_lshl_b32 s2, s7, 8
	s_add_i32 s79, s2, 0
	v_readlane_b32 s2, v253, 5
	v_cndmask_b32_e64 v2, 0, 1, vcc
	v_lshlrev_b32_e32 v137, 4, v3
	s_lshl_b32 s78, s7, 6
	s_add_i32 s79, s79, 0x21000
	s_mov_b32 s80, 0
	s_mov_b32 s82, s2
	s_barrier
	v_readlane_b32 s3, v253, 6
	s_branch .LBB0_1557

.LBB0_1557:
	s_andn2_b64 vcc, exec, s[24:25]
	s_and_b32 s83, s80, 1
	s_cbranch_vccnz .LBB0_1559
	v_ashrrev_i32_e32 v1, 31, v0
	s_lshl_b32 s2, s82, 8
	v_lshlrev_b64 v[0:1], 12, v[0:1]
	s_ashr_i32 s3, s2, 31
	v_lshl_add_u64 v[0:1], s[22:23], 0, v[0:1]
	s_lshl_b64 s[2:3], s[2:3], 2
	s_lshl_b32 s4, s83, 10
	v_lshl_add_u64 v[0:1], v[0:1], 0, s[2:3]
	s_add_i32 s4, s4, 0
	v_readfirstlane_b32 s3, v1
	v_readfirstlane_b32 s2, v0
	s_add_i32 s4, s4, 0x21000
	s_mov_b32 m0, s4
	s_nop 0
	global_load_lds_dwordx4 v137, s[2:3]

.LBB0_1566:
	v_add_u32_e32 v144, 0, v135
	v_add_u32_e32 v76, 0x10000, v144
	v_add_u32_e32 v92, 0x14000, v144
	ds_read_b128 v[64:67], v76
	ds_read_b128 v[68:71], v76 offset:1024
	ds_read_b128 v[72:75], v76 offset:2048
	ds_read_b128 v[76:79], v76 offset:3072
	ds_read_b128 v[80:83], v92
	ds_read_b128 v[84:87], v92 offset:1024
	ds_read_b128 v[88:91], v92 offset:2048
	ds_read_b128 v[92:95], v92 offset:3072
	s_add_i32 s88, s46, 2
	s_cmp_eq_u32 s76, s46
	s_cselect_b32 s48, s38, s86
	s_cselect_b32 s49, s39, s87
	s_cselect_b32 s50, s36, s84
	s_cselect_b32 s51, s37, s85
	s_add_u32 s46, s48, 0x80
	s_addc_u32 s47, s49, 0
	v_add_u32_e32 v145, 0, v133
	ds_read_b128 v[98:101], v145
	ds_read_b128 v[102:105], v145 offset:1024
	ds_read_b128 v[106:109], v145 offset:2048
	ds_read_b128 v[110:113], v145 offset:3072
	ds_read_b128 v[114:117], v145 offset:4096
	ds_read_b128 v[118:121], v145 offset:5120
	ds_read_b128 v[122:125], v145 offset:6144
	ds_read_b128 v[126:129], v145 offset:7168
	s_mov_b32 m0, s77
	s_nop 0
	global_load_lds_dwordx4 v132, s[44:45]
	s_add_i32 s89, s60, 0xe000
	s_mov_b32 m0, s89
	s_nop 0
	global_load_lds_dwordx4 v136, s[44:45]
	s_waitcnt vmcnt(8)
	s_waitcnt lgkmcnt(0)
	s_barrier
	s_setprio 1
	s_waitcnt lgkmcnt(6)
	v_mfma_scale_f32_16x16x128_f8f6f4 v[60:63], v[64:71], v[98:105], v[60:63], v243, v243 op_sel_hi:[0,0,0]
	v_mfma_scale_f32_16x16x128_f8f6f4 v[56:59], v[72:79], v[98:105], v[56:59], v243, v243 op_sel_hi:[0,0,0]
	s_waitcnt lgkmcnt(4)
	v_mfma_scale_f32_16x16x128_f8f6f4 v[44:47], v[64:71], v[106:113], v[44:47], v243, v243 op_sel_hi:[0,0,0]
	v_mfma_scale_f32_16x16x128_f8f6f4 v[40:43], v[72:79], v[106:113], v[40:43], v243, v243 op_sel_hi:[0,0,0]
	s_waitcnt lgkmcnt(2)
	v_mfma_scale_f32_16x16x128_f8f6f4 v[28:31], v[64:71], v[114:121], v[28:31], v243, v243 op_sel_hi:[0,0,0]
	v_mfma_scale_f32_16x16x128_f8f6f4 v[24:27], v[72:79], v[114:121], v[24:27], v243, v243 op_sel_hi:[0,0,0]
	s_waitcnt lgkmcnt(0)
	v_mfma_scale_f32_16x16x128_f8f6f4 v[12:15], v[64:71], v[122:129], v[12:15], v243, v243 op_sel_hi:[0,0,0]
	v_mfma_scale_f32_16x16x128_f8f6f4 v[8:11], v[72:79], v[122:129], v[8:11], v243, v243 op_sel_hi:[0,0,0]
	s_setprio 0
	s_setprio 1
	v_mfma_scale_f32_16x16x128_f8f6f4 v[52:55], v[80:87], v[98:105], v[52:55], v243, v243 op_sel_hi:[0,0,0]
	v_mfma_scale_f32_16x16x128_f8f6f4 v[48:51], v[88:95], v[98:105], v[48:51], v243, v243 op_sel_hi:[0,0,0]
	v_mfma_scale_f32_16x16x128_f8f6f4 v[140:143], v[80:87], v[106:113], v[36:39], v243, v243 op_sel_hi:[0,0,0]
	v_mfma_scale_f32_16x16x128_f8f6f4 v[106:109], v[88:95], v[106:113], v[32:35], v243, v243 op_sel_hi:[0,0,0]
	v_mfma_scale_f32_16x16x128_f8f6f4 v[110:113], v[80:87], v[114:121], v[20:23], v243, v243 op_sel_hi:[0,0,0]
	v_mfma_scale_f32_16x16x128_f8f6f4 v[114:117], v[88:95], v[114:121], v[16:19], v243, v243 op_sel_hi:[0,0,0]
	v_mfma_scale_f32_16x16x128_f8f6f4 v[118:121], v[80:87], v[122:129], v[4:7], v243, v243 op_sel_hi:[0,0,0]
	v_mfma_scale_f32_16x16x128_f8f6f4 v[122:125], v[88:95], v[122:129], v[0:3], v243, v243 op_sel_hi:[0,0,0]
	s_setprio 0
	s_barrier
	s_mov_b32 m0, s61
	s_nop 0
	global_load_lds_dwordx4 v134, s[50:51]
	s_add_u32 s90, s50, s14
	s_mov_b32 m0, s62
	s_nop 0
	global_load_lds_dwordx4 v138, s[50:51]
	s_addc_u32 s91, s51, s15
	s_mov_b32 m0, s63
	s_nop 0
	global_load_lds_dwordx4 v134, s[90:91]
	s_nop 0
	s_mov_b32 m0, s64
	s_nop 0
	global_load_lds_dwordx4 v138, s[90:91]
	s_nop 0
	s_mov_b32 m0, s60
	s_nop 0
	global_load_lds_dwordx4 v132, s[48:49]
	s_nop 0
	s_mov_b32 m0, s65
	s_nop 0
	global_load_lds_dwordx4 v136, s[48:49]
	s_waitcnt vmcnt(8)
	s_waitcnt lgkmcnt(0)
	s_barrier
	s_barrier
	v_add_u32_e32 v20, 0x18000, v144
	v_add_u32_e32 v32, 0x1c000, v144
	ds_read_b128 v[0:3], v20
	ds_read_b128 v[4:7], v20 offset:1024
	ds_read_b128 v[16:19], v20 offset:2048
	ds_read_b128 v[20:23], v20 offset:3072
	ds_read_b128 v[64:67], v32
	ds_read_b128 v[68:71], v32 offset:1024
	ds_read_b128 v[72:75], v32 offset:2048
	ds_read_b128 v[76:79], v32 offset:3072
	ds_read_b128 v[32:35], v145 offset:32768
	ds_read_b128 v[36:39], v145 offset:33792
	ds_read_b128 v[80:83], v145 offset:34816
	ds_read_b128 v[84:87], v145 offset:35840
	ds_read_b128 v[88:91], v145 offset:36864
	ds_read_b128 v[92:95], v145 offset:37888
	ds_read_b128 v[98:101], v145 offset:38912
	ds_read_b128 v[102:105], v145 offset:39936
	s_add_u32 s48, s48, s16
	s_addc_u32 s49, s49, s17
	s_mov_b32 m0, s66
	s_nop 0
	global_load_lds_dwordx4 v132, s[48:49]
	s_nop 0
	s_mov_b32 m0, s67
	s_nop 0
	global_load_lds_dwordx4 v136, s[48:49]
	s_waitcnt vmcnt(8)
	s_waitcnt lgkmcnt(0)
	s_barrier
	s_setprio 1
	s_waitcnt lgkmcnt(6)
	v_mfma_scale_f32_16x16x128_f8f6f4 v[60:63], v[0:7], v[32:39], v[60:63], v243, v243 op_sel_hi:[0,0,0]
	v_mfma_scale_f32_16x16x128_f8f6f4 v[56:59], v[16:23], v[32:39], v[56:59], v243, v243 op_sel_hi:[0,0,0]
	s_waitcnt lgkmcnt(4)
	v_mfma_scale_f32_16x16x128_f8f6f4 v[44:47], v[0:7], v[80:87], v[44:47], v243, v243 op_sel_hi:[0,0,0]
	v_mfma_scale_f32_16x16x128_f8f6f4 v[40:43], v[16:23], v[80:87], v[40:43], v243, v243 op_sel_hi:[0,0,0]
	s_waitcnt lgkmcnt(2)
	v_mfma_scale_f32_16x16x128_f8f6f4 v[28:31], v[0:7], v[88:95], v[28:31], v243, v243 op_sel_hi:[0,0,0]
	v_mfma_scale_f32_16x16x128_f8f6f4 v[24:27], v[16:23], v[88:95], v[24:27], v243, v243 op_sel_hi:[0,0,0]
	s_waitcnt lgkmcnt(0)
	v_mfma_scale_f32_16x16x128_f8f6f4 v[12:15], v[0:7], v[98:105], v[12:15], v243, v243 op_sel_hi:[0,0,0]
	v_mfma_scale_f32_16x16x128_f8f6f4 v[8:11], v[16:23], v[98:105], v[8:11], v243, v243 op_sel_hi:[0,0,0]
	s_setprio 0
	s_setprio 1
	v_mfma_scale_f32_16x16x128_f8f6f4 v[52:55], v[64:71], v[32:39], v[52:55], v243, v243 op_sel_hi:[0,0,0]
	s_add_u32 s48, s50, 0x80
	s_addc_u32 s49, s51, 0
	v_mfma_scale_f32_16x16x128_f8f6f4 v[48:51], v[72:79], v[32:39], v[48:51], v243, v243 op_sel_hi:[0,0,0]
	v_mfma_scale_f32_16x16x128_f8f6f4 v[36:39], v[64:71], v[80:87], v[140:143], v243, v243 op_sel_hi:[0,0,0]
	v_mfma_scale_f32_16x16x128_f8f6f4 v[32:35], v[72:79], v[80:87], v[106:109], v243, v243 op_sel_hi:[0,0,0]
	v_mfma_scale_f32_16x16x128_f8f6f4 v[20:23], v[64:71], v[88:95], v[110:113], v243, v243 op_sel_hi:[0,0,0]
	v_mfma_scale_f32_16x16x128_f8f6f4 v[16:19], v[72:79], v[88:95], v[114:117], v243, v243 op_sel_hi:[0,0,0]
	v_mfma_scale_f32_16x16x128_f8f6f4 v[4:7], v[64:71], v[98:105], v[118:121], v243, v243 op_sel_hi:[0,0,0]
	v_mfma_scale_f32_16x16x128_f8f6f4 v[0:3], v[72:79], v[98:105], v[122:125], v243, v243 op_sel_hi:[0,0,0]
	s_setprio 0
	s_barrier
	s_mov_b32 m0, s70
	s_nop 0
	global_load_lds_dwordx4 v134, s[48:49]
	s_nop 0
	s_mov_b32 m0, s71
	s_nop 0
	global_load_lds_dwordx4 v138, s[48:49]
	s_add_u32 s48, s48, s14
	s_addc_u32 s49, s49, s15
	s_mov_b32 m0, s74
	s_nop 0
	global_load_lds_dwordx4 v134, s[48:49]
	s_nop 0
	s_mov_b32 m0, s75
	s_nop 0
	global_load_lds_dwordx4 v138, s[48:49]
	s_mov_b32 m0, s72
	s_nop 0
	global_load_lds_dwordx4 v132, s[46:47]
	s_nop 0
	s_mov_b32 m0, s73
	s_nop 0
	global_load_lds_dwordx4 v136, s[46:47]
	s_waitcnt vmcnt(8)
	s_waitcnt lgkmcnt(0)
	s_barrier
	s_barrier
	s_add_u32 s84, s84, 0x100
	s_addc_u32 s85, s85, 0
	s_add_u32 s86, s86, 0x100
	s_addc_u32 s87, s87, 0
	s_add_u32 s44, s44, 0x100
	s_addc_u32 s45, s45, 0
	s_cmp_ge_i32 s88, s68
	s_mov_b32 s46, s88
	s_cbranch_scc0 .LBB0_1566
	v_readlane_b32 s88, v252, 6
	v_readlane_b32 s46, v254, 34
	v_readlane_b32 s90, v254, 25
	v_readlane_b32 s89, v252, 7
	v_readlane_b32 s84, v254, 31
	s_mov_b32 s87, s95
	v_readlane_b32 s47, v254, 35
	v_readlane_b32 s91, v254, 26
	v_readlane_b32 s85, v254, 32

.LBB0_1572:
	v_add_u32_e32 v153, 0, v135
	v_add_u32_e32 v148, 0x10000, v153
	ds_read_b128 v[140:143], v148
	ds_read_b128 v[144:147], v148 offset:1024
	ds_read_b128 v[154:157], v148 offset:2048
	ds_read_b128 v[158:161], v148 offset:3072
	v_add_u32_e32 v148, 0x14000, v153
	ds_read_b128 v[162:165], v148
	ds_read_b128 v[166:169], v148 offset:1024
	ds_read_b128 v[170:173], v148 offset:2048
	ds_read_b128 v[174:177], v148 offset:3072
	s_add_i32 s31, s35, 2
	s_cmp_eq_u32 s76, s35
	s_cselect_b32 s44, s38, s48
	s_cselect_b32 s45, s39, s49
	s_cselect_b32 s42, s36, s46
	s_cselect_b32 s43, s37, s47
	s_add_u32 s40, s44, 0x80
	s_addc_u32 s41, s45, 0
	v_add_u32_e32 v238, 0, v133
	ds_read_b128 v[178:181], v238
	ds_read_b128 v[182:185], v238 offset:1024
	ds_read_b128 v[186:189], v238 offset:2048
	ds_read_b128 v[190:193], v238 offset:3072
	ds_read_b128 v[198:201], v238 offset:4096
	ds_read_b128 v[202:205], v238 offset:5120
	ds_read_b128 v[206:209], v238 offset:6144
	ds_read_b128 v[210:213], v238 offset:7168
	s_mov_b32 m0, s77
	s_nop 0
	global_load_lds_dwordx4 v132, s[6:7]
	s_add_i32 s35, s60, 0xe000
	s_mov_b32 m0, s35
	s_nop 0
	global_load_lds_dwordx4 v136, s[6:7]
	s_waitcnt vmcnt(8)
	s_waitcnt lgkmcnt(0)
	s_barrier
	s_setprio 1
	s_waitcnt lgkmcnt(6)
	v_mfma_scale_f32_16x16x128_f8f6f4 v[60:63], v[140:147], v[178:185], v[60:63], v243, v243 op_sel_hi:[0,0,0]
	v_mfma_scale_f32_16x16x128_f8f6f4 v[56:59], v[154:161], v[178:185], v[56:59], v243, v243 op_sel_hi:[0,0,0]
	s_waitcnt lgkmcnt(4)
	v_mfma_scale_f32_16x16x128_f8f6f4 v[44:47], v[140:147], v[186:193], v[44:47], v243, v243 op_sel_hi:[0,0,0]
	v_mfma_scale_f32_16x16x128_f8f6f4 v[40:43], v[154:161], v[186:193], v[40:43], v243, v243 op_sel_hi:[0,0,0]
	s_waitcnt lgkmcnt(2)
	v_mfma_scale_f32_16x16x128_f8f6f4 v[148:151], v[140:147], v[198:205], v[28:31], v243, v243 op_sel_hi:[0,0,0]
	v_mfma_scale_f32_16x16x128_f8f6f4 v[194:197], v[154:161], v[198:205], v[24:27], v243, v243 op_sel_hi:[0,0,0]
	s_waitcnt lgkmcnt(0)
	v_mfma_scale_f32_16x16x128_f8f6f4 v[214:217], v[140:147], v[206:213], v[12:15], v243, v243 op_sel_hi:[0,0,0]
	v_mfma_scale_f32_16x16x128_f8f6f4 v[218:221], v[154:161], v[206:213], v[8:11], v243, v243 op_sel_hi:[0,0,0]
	s_setprio 0
	s_setprio 1
	v_mfma_scale_f32_16x16x128_f8f6f4 v[52:55], v[162:169], v[178:185], v[52:55], v243, v243 op_sel_hi:[0,0,0]
	v_mfma_scale_f32_16x16x128_f8f6f4 v[48:51], v[170:177], v[178:185], v[48:51], v243, v243 op_sel_hi:[0,0,0]
	v_mfma_scale_f32_16x16x128_f8f6f4 v[36:39], v[162:169], v[186:193], v[36:39], v243, v243 op_sel_hi:[0,0,0]
	v_mfma_scale_f32_16x16x128_f8f6f4 v[32:35], v[170:177], v[186:193], v[32:35], v243, v243 op_sel_hi:[0,0,0]
	v_mfma_scale_f32_16x16x128_f8f6f4 v[178:181], v[162:169], v[198:205], v[20:23], v243, v243 op_sel_hi:[0,0,0]
	v_mfma_scale_f32_16x16x128_f8f6f4 v[182:185], v[170:177], v[198:205], v[16:19], v243, v243 op_sel_hi:[0,0,0]
	v_mfma_scale_f32_16x16x128_f8f6f4 v[186:189], v[162:169], v[206:213], v[4:7], v243, v243 op_sel_hi:[0,0,0]
	v_mfma_scale_f32_16x16x128_f8f6f4 v[190:193], v[170:177], v[206:213], v[0:3], v243, v243 op_sel_hi:[0,0,0]
	s_setprio 0
	s_barrier
	s_nop 4
	ds_read_b128 v[0:3], v238 offset:16384
	ds_read_b128 v[4:7], v238 offset:17408
	ds_read_b128 v[8:11], v238 offset:18432
	ds_read_b128 v[12:15], v238 offset:19456
	ds_read_b128 v[16:19], v238 offset:20480
	ds_read_b128 v[20:23], v238 offset:21504
	ds_read_b128 v[24:27], v238 offset:22528
	ds_read_b128 v[28:31], v238 offset:23552
	s_mov_b32 m0, s61
	s_nop 0
	global_load_lds_dwordx4 v134, s[42:43]
	s_add_u32 s50, s42, s14
	s_mov_b32 m0, s62
	s_nop 0
	global_load_lds_dwordx4 v138, s[42:43]
	s_addc_u32 s51, s43, s15
	s_mov_b32 m0, s63
	s_nop 0
	global_load_lds_dwordx4 v134, s[50:51]
	s_nop 0
	s_mov_b32 m0, s64
	s_nop 0
	global_load_lds_dwordx4 v138, s[50:51]
	s_nop 0
	s_mov_b32 m0, s60
	s_nop 0
	global_load_lds_dwordx4 v132, s[44:45]
	s_nop 0
	s_mov_b32 m0, s65
	s_nop 0
	global_load_lds_dwordx4 v136, s[44:45]
	s_waitcnt vmcnt(8)
	s_waitcnt lgkmcnt(0)
	s_barrier
	s_setprio 1
	s_waitcnt lgkmcnt(6)
	v_mfma_scale_f32_16x16x128_f8f6f4 v[126:129], v[140:147], v[0:7], v[126:129], v243, v243 op_sel_hi:[0,0,0]
	v_mfma_scale_f32_16x16x128_f8f6f4 v[122:125], v[154:161], v[0:7], v[122:125], v243, v243 op_sel_hi:[0,0,0]
	s_waitcnt lgkmcnt(4)
	v_mfma_scale_f32_16x16x128_f8f6f4 v[118:121], v[140:147], v[8:15], v[118:121], v243, v243 op_sel_hi:[0,0,0]
	v_mfma_scale_f32_16x16x128_f8f6f4 v[114:117], v[154:161], v[8:15], v[114:117], v243, v243 op_sel_hi:[0,0,0]
	s_waitcnt lgkmcnt(2)
	v_mfma_scale_f32_16x16x128_f8f6f4 v[106:109], v[140:147], v[16:23], v[106:109], v243, v243 op_sel_hi:[0,0,0]
	v_mfma_scale_f32_16x16x128_f8f6f4 v[98:101], v[154:161], v[16:23], v[98:101], v243, v243 op_sel_hi:[0,0,0]
	s_waitcnt lgkmcnt(0)
	v_mfma_scale_f32_16x16x128_f8f6f4 v[198:201], v[140:147], v[24:31], v[88:91], v243, v243 op_sel_hi:[0,0,0]
	v_mfma_scale_f32_16x16x128_f8f6f4 v[202:205], v[154:161], v[24:31], v[80:83], v243, v243 op_sel_hi:[0,0,0]
	s_setprio 0
	s_setprio 1
	v_mfma_scale_f32_16x16x128_f8f6f4 v[110:113], v[162:169], v[0:7], v[110:113], v243, v243 op_sel_hi:[0,0,0]
	v_mfma_scale_f32_16x16x128_f8f6f4 v[102:105], v[170:177], v[0:7], v[102:105], v243, v243 op_sel_hi:[0,0,0]
	v_mfma_scale_f32_16x16x128_f8f6f4 v[206:209], v[162:169], v[8:15], v[92:95], v243, v243 op_sel_hi:[0,0,0]
	v_mfma_scale_f32_16x16x128_f8f6f4 v[210:213], v[170:177], v[8:15], v[84:87], v243, v243 op_sel_hi:[0,0,0]
	v_mfma_scale_f32_16x16x128_f8f6f4 v[222:225], v[162:169], v[16:23], v[76:79], v243, v243 op_sel_hi:[0,0,0]
	v_mfma_scale_f32_16x16x128_f8f6f4 v[226:229], v[170:177], v[16:23], v[72:75], v243, v243 op_sel_hi:[0,0,0]
	v_mfma_scale_f32_16x16x128_f8f6f4 v[230:233], v[162:169], v[24:31], v[68:71], v243, v243 op_sel_hi:[0,0,0]
	v_mfma_scale_f32_16x16x128_f8f6f4 v[234:237], v[170:177], v[24:31], v[64:67], v243, v243 op_sel_hi:[0,0,0]
	s_setprio 0
	s_barrier
	v_add_u32_e32 v0, 0x18000, v153
	s_nop 3
	ds_read_b128 v[64:67], v0
	ds_read_b128 v[68:71], v0 offset:1024
	ds_read_b128 v[72:75], v0 offset:2048
	ds_read_b128 v[76:79], v0 offset:3072
	v_add_u32_e32 v0, 0x1c000, v153
	ds_read_b128 v[140:143], v0
	ds_read_b128 v[144:147], v0 offset:1024
	ds_read_b128 v[154:157], v0 offset:2048
	ds_read_b128 v[158:161], v0 offset:3072
	ds_read_b128 v[0:3], v238 offset:32768
	ds_read_b128 v[4:7], v238 offset:33792
	ds_read_b128 v[16:19], v238 offset:34816
	ds_read_b128 v[20:23], v238 offset:35840
	ds_read_b128 v[80:83], v238 offset:36864
	ds_read_b128 v[84:87], v238 offset:37888
	ds_read_b128 v[88:91], v238 offset:38912
	ds_read_b128 v[92:95], v238 offset:39936
	s_add_u32 s44, s44, s16
	s_addc_u32 s45, s45, s17
	s_mov_b32 m0, s66
	s_nop 0
	global_load_lds_dwordx4 v132, s[44:45]
	s_nop 0
	s_mov_b32 m0, s67
	s_nop 0
	global_load_lds_dwordx4 v136, s[44:45]
	s_waitcnt vmcnt(8)
	s_waitcnt lgkmcnt(0)
	s_barrier
	s_setprio 1
	s_waitcnt lgkmcnt(6)
	v_mfma_scale_f32_16x16x128_f8f6f4 v[60:63], v[64:71], v[0:7], v[60:63], v243, v243 op_sel_hi:[0,0,0]
	v_mfma_scale_f32_16x16x128_f8f6f4 v[56:59], v[72:79], v[0:7], v[56:59], v243, v243 op_sel_hi:[0,0,0]
	s_waitcnt lgkmcnt(4)
	v_mfma_scale_f32_16x16x128_f8f6f4 v[44:47], v[64:71], v[16:23], v[44:47], v243, v243 op_sel_hi:[0,0,0]
	v_mfma_scale_f32_16x16x128_f8f6f4 v[40:43], v[72:79], v[16:23], v[40:43], v243, v243 op_sel_hi:[0,0,0]
	s_waitcnt lgkmcnt(2)
	v_mfma_scale_f32_16x16x128_f8f6f4 v[28:31], v[64:71], v[80:87], v[148:151], v243, v243 op_sel_hi:[0,0,0]
	v_mfma_scale_f32_16x16x128_f8f6f4 v[24:27], v[72:79], v[80:87], v[194:197], v243, v243 op_sel_hi:[0,0,0]
	s_waitcnt lgkmcnt(0)
	v_mfma_scale_f32_16x16x128_f8f6f4 v[12:15], v[64:71], v[88:95], v[214:217], v243, v243 op_sel_hi:[0,0,0]
	v_mfma_scale_f32_16x16x128_f8f6f4 v[8:11], v[72:79], v[88:95], v[218:221], v243, v243 op_sel_hi:[0,0,0]
	s_setprio 0
	s_setprio 1
	v_mfma_scale_f32_16x16x128_f8f6f4 v[52:55], v[140:147], v[0:7], v[52:55], v243, v243 op_sel_hi:[0,0,0]
	v_mfma_scale_f32_16x16x128_f8f6f4 v[48:51], v[154:161], v[0:7], v[48:51], v243, v243 op_sel_hi:[0,0,0]
	v_mfma_scale_f32_16x16x128_f8f6f4 v[36:39], v[140:147], v[16:23], v[36:39], v243, v243 op_sel_hi:[0,0,0]
	v_mfma_scale_f32_16x16x128_f8f6f4 v[32:35], v[154:161], v[16:23], v[32:35], v243, v243 op_sel_hi:[0,0,0]
	v_mfma_scale_f32_16x16x128_f8f6f4 v[20:23], v[140:147], v[80:87], v[178:181], v243, v243 op_sel_hi:[0,0,0]
	v_mfma_scale_f32_16x16x128_f8f6f4 v[16:19], v[154:161], v[80:87], v[182:185], v243, v243 op_sel_hi:[0,0,0]
	v_mfma_scale_f32_16x16x128_f8f6f4 v[4:7], v[140:147], v[88:95], v[186:189], v243, v243 op_sel_hi:[0,0,0]
	v_mfma_scale_f32_16x16x128_f8f6f4 v[0:3], v[154:161], v[88:95], v[190:193], v243, v243 op_sel_hi:[0,0,0]
	s_setprio 0
	s_barrier
	ds_read_b128 v[162:165], v238 offset:49152
	ds_read_b128 v[166:169], v238 offset:50176
	ds_read_b128 v[170:173], v238 offset:51200
	ds_read_b128 v[174:177], v238 offset:52224
	ds_read_b128 v[178:181], v238 offset:53248
	ds_read_b128 v[182:185], v238 offset:54272
	ds_read_b128 v[186:189], v238 offset:55296
	ds_read_b128 v[190:193], v238 offset:56320
	s_add_u32 s42, s42, 0x80
	s_addc_u32 s43, s43, 0
	s_mov_b32 m0, s70
	s_nop 0
	global_load_lds_dwordx4 v134, s[42:43]
	s_nop 0
	s_mov_b32 m0, s71
	s_nop 0
	global_load_lds_dwordx4 v138, s[42:43]
	s_add_u32 s42, s42, s14
	s_addc_u32 s43, s43, s15
	s_mov_b32 m0, s74
	s_nop 0
	global_load_lds_dwordx4 v134, s[42:43]
	s_nop 0
	s_mov_b32 m0, s75
	s_nop 0
	global_load_lds_dwordx4 v138, s[42:43]
	s_nop 0
	s_mov_b32 m0, s72
	s_nop 0
	global_load_lds_dwordx4 v132, s[40:41]
	s_nop 0
	s_mov_b32 m0, s73
	s_nop 0
	global_load_lds_dwordx4 v136, s[40:41]
	s_waitcnt vmcnt(8)
	s_waitcnt lgkmcnt(0)
	s_barrier
	s_setprio 1
	s_waitcnt lgkmcnt(6)
	v_mfma_scale_f32_16x16x128_f8f6f4 v[126:129], v[64:71], v[162:169], v[126:129], v243, v243 op_sel_hi:[0,0,0]
	v_mfma_scale_f32_16x16x128_f8f6f4 v[122:125], v[72:79], v[162:169], v[122:125], v243, v243 op_sel_hi:[0,0,0]
	s_waitcnt lgkmcnt(4)
	v_mfma_scale_f32_16x16x128_f8f6f4 v[118:121], v[64:71], v[170:177], v[118:121], v243, v243 op_sel_hi:[0,0,0]
	v_mfma_scale_f32_16x16x128_f8f6f4 v[114:117], v[72:79], v[170:177], v[114:117], v243, v243 op_sel_hi:[0,0,0]
	s_waitcnt lgkmcnt(2)
	v_mfma_scale_f32_16x16x128_f8f6f4 v[106:109], v[64:71], v[178:185], v[106:109], v243, v243 op_sel_hi:[0,0,0]
	v_mfma_scale_f32_16x16x128_f8f6f4 v[98:101], v[72:79], v[178:185], v[98:101], v243, v243 op_sel_hi:[0,0,0]
	s_waitcnt lgkmcnt(0)
	v_mfma_scale_f32_16x16x128_f8f6f4 v[88:91], v[64:71], v[186:193], v[198:201], v243, v243 op_sel_hi:[0,0,0]
	v_mfma_scale_f32_16x16x128_f8f6f4 v[80:83], v[72:79], v[186:193], v[202:205], v243, v243 op_sel_hi:[0,0,0]
	s_setprio 0
	s_setprio 1
	v_mfma_scale_f32_16x16x128_f8f6f4 v[110:113], v[140:147], v[162:169], v[110:113], v243, v243 op_sel_hi:[0,0,0]
	v_mfma_scale_f32_16x16x128_f8f6f4 v[102:105], v[154:161], v[162:169], v[102:105], v243, v243 op_sel_hi:[0,0,0]
	v_mfma_scale_f32_16x16x128_f8f6f4 v[92:95], v[140:147], v[170:177], v[206:209], v243, v243 op_sel_hi:[0,0,0]
	v_mfma_scale_f32_16x16x128_f8f6f4 v[84:87], v[154:161], v[170:177], v[210:213], v243, v243 op_sel_hi:[0,0,0]
	v_mfma_scale_f32_16x16x128_f8f6f4 v[76:79], v[140:147], v[178:185], v[222:225], v243, v243 op_sel_hi:[0,0,0]
	v_mfma_scale_f32_16x16x128_f8f6f4 v[72:75], v[154:161], v[178:185], v[226:229], v243, v243 op_sel_hi:[0,0,0]
	v_mfma_scale_f32_16x16x128_f8f6f4 v[68:71], v[140:147], v[186:193], v[230:233], v243, v243 op_sel_hi:[0,0,0]
	v_mfma_scale_f32_16x16x128_f8f6f4 v[64:67], v[154:161], v[186:193], v[234:237], v243, v243 op_sel_hi:[0,0,0]
	s_setprio 0
	s_barrier
	s_add_u32 s46, s46, 0x100
	s_addc_u32 s47, s47, 0
	s_add_u32 s48, s48, 0x100
	s_addc_u32 s49, s49, 0
	s_add_u32 s6, s6, 0x100
	s_addc_u32 s7, s7, 0
	s_cmp_lt_i32 s31, s68
	s_mov_b32 s35, s31
	s_cbranch_scc1 .LBB0_1572
	s_mov_b32 s6, 0x3e800000
	v_readlane_b32 s46, v254, 34
	v_pk_mul_f32 v[150:151], v[128:129], s[6:7] op_sel_hi:[1,0]
	v_pk_mul_f32 v[148:149], v[126:127], s[6:7] op_sel_hi:[1,0]
	v_pk_mul_f32 v[146:147], v[124:125], s[6:7] op_sel_hi:[1,0]
	v_pk_mul_f32 v[144:145], v[122:123], s[6:7] op_sel_hi:[1,0]
	v_pk_mul_f32 v[142:143], v[112:113], s[6:7] op_sel_hi:[1,0]
	v_pk_mul_f32 v[140:141], v[110:111], s[6:7] op_sel_hi:[1,0]
	v_pk_mul_f32 v[128:129], v[104:105], s[6:7] op_sel_hi:[1,0]
	v_pk_mul_f32 v[126:127], v[102:103], s[6:7] op_sel_hi:[1,0]
	v_pk_mul_f32 v[124:125], v[120:121], s[6:7] op_sel_hi:[1,0]
	v_pk_mul_f32 v[122:123], v[118:119], s[6:7] op_sel_hi:[1,0]
	v_pk_mul_f32 v[120:121], v[116:117], s[6:7] op_sel_hi:[1,0]
	v_pk_mul_f32 v[118:119], v[114:115], s[6:7] op_sel_hi:[1,0]
	v_pk_mul_f32 v[116:117], v[94:95], s[6:7] op_sel_hi:[1,0]
	v_pk_mul_f32 v[114:115], v[92:93], s[6:7] op_sel_hi:[1,0]
	v_pk_mul_f32 v[112:113], v[86:87], s[6:7] op_sel_hi:[1,0]
	v_pk_mul_f32 v[110:111], v[84:85], s[6:7] op_sel_hi:[1,0]
	v_pk_mul_f32 v[104:105], v[108:109], s[6:7] op_sel_hi:[1,0]
	v_pk_mul_f32 v[102:103], v[106:107], s[6:7] op_sel_hi:[1,0]
	v_pk_mul_f32 v[100:101], v[100:101], s[6:7] op_sel_hi:[1,0]
	v_pk_mul_f32 v[98:99], v[98:99], s[6:7] op_sel_hi:[1,0]
	v_pk_mul_f32 v[94:95], v[78:79], s[6:7] op_sel_hi:[1,0]
	v_pk_mul_f32 v[92:93], v[76:77], s[6:7] op_sel_hi:[1,0]
	v_pk_mul_f32 v[86:87], v[74:75], s[6:7] op_sel_hi:[1,0]
	v_pk_mul_f32 v[84:85], v[72:73], s[6:7] op_sel_hi:[1,0]
	v_pk_mul_f32 v[78:79], v[90:91], s[6:7] op_sel_hi:[1,0]
	v_pk_mul_f32 v[76:77], v[88:89], s[6:7] op_sel_hi:[1,0]
	v_pk_mul_f32 v[74:75], v[82:83], s[6:7] op_sel_hi:[1,0]
	v_pk_mul_f32 v[72:73], v[80:81], s[6:7] op_sel_hi:[1,0]
	v_pk_mul_f32 v[70:71], v[70:71], s[6:7] op_sel_hi:[1,0]
	v_pk_mul_f32 v[68:69], v[68:69], s[6:7] op_sel_hi:[1,0]
	v_pk_mul_f32 v[66:67], v[66:67], s[6:7] op_sel_hi:[1,0]
	v_pk_mul_f32 v[64:65], v[64:65], s[6:7] op_sel_hi:[1,0]
	v_readlane_b32 s47, v254, 35
	v_readlane_b32 s44, v254, 38
	v_mov_b32_e32 v224, v244
	v_mov_b32_e32 v226, v245
	v_mov_b32_e32 v227, v246
	v_mov_b64_e32 v[230:231], v[248:249]
	v_mov_b64_e32 v[232:233], v[250:251]
	v_mov_b32_e32 v229, v247
